# all 16-byte global stores made write-through (sc1) so the L2 write-back at each grid barrier has less dirty data to flush
# baseline (speedup 1.0000x reference)
.LBB0_23:
	s_waitcnt lgkmcnt(7)
	v_mul_f32_e32 v80, 0x42800000, v80
	v_med3_f32 v88, v80, s20, v171
	v_mul_f32_e32 v80, 0x42800000, v81
	v_med3_f32 v81, v80, s20, v171
	v_mov_b32_e32 v80, v137
	v_cvt_pk_fp8_f32 v80, v88, v81
	s_waitcnt lgkmcnt(6)
	v_mul_f32_e32 v82, 0x42800000, v82
	v_mul_f32_e32 v83, 0x42800000, v83
	v_med3_f32 v82, v82, s20, v171
	v_med3_f32 v83, v83, s20, v171
	s_waitcnt lgkmcnt(1)
	v_mul_f32_e32 v68, 0x42800000, v68
	v_mul_f32_e32 v69, 0x42800000, v69
	v_cvt_pk_fp8_f32 v80, v82, v83 op_sel:[0,0,1]
	v_mul_f32_e32 v76, 0x42800000, v76
	v_mul_f32_e32 v77, 0x42800000, v77
	v_mul_f32_e32 v72, 0x42800000, v72
	v_mul_f32_e32 v73, 0x42800000, v73
	v_med3_f32 v68, v68, s20, v171
	v_med3_f32 v69, v69, s20, v171
	v_mov_b32_e32 v83, v137
	v_med3_f32 v76, v76, s20, v171
	v_med3_f32 v77, v77, s20, v171
	v_mov_b32_e32 v81, v137
	v_med3_f32 v72, v72, s20, v171
	v_med3_f32 v73, v73, s20, v171
	v_mov_b32_e32 v82, v137
	v_cvt_pk_fp8_f32 v83, v68, v69
	v_cvt_pk_fp8_f32 v81, v76, v77
	v_cvt_pk_fp8_f32 v82, v72, v73
	s_waitcnt lgkmcnt(0)
	v_mul_f32_e32 v70, 0x42800000, v70
	v_mul_f32_e32 v71, 0x42800000, v71
	v_mul_f32_e32 v78, 0x42800000, v78
	v_mul_f32_e32 v79, 0x42800000, v79
	v_mul_f32_e32 v74, 0x42800000, v74
	v_mul_f32_e32 v75, 0x42800000, v75
	v_med3_f32 v70, v70, s20, v171
	v_med3_f32 v71, v71, s20, v171
	v_ashrrev_i32_e32 v68, 8, v86
	v_med3_f32 v78, v78, s20, v171
	v_med3_f32 v79, v79, s20, v171
	v_med3_f32 v74, v74, s20, v171
	v_med3_f32 v75, v75, s20, v171
	v_cvt_pk_fp8_f32 v83, v70, v71 op_sel:[0,0,1]
	v_mad_i64_i32 v[66:67], s[0:1], s2, v68, v[66:67]
	v_lshrrev_b32_e32 v70, 3, v87
	v_cvt_pk_fp8_f32 v81, v78, v79 op_sel:[0,0,1]
	v_cvt_pk_fp8_f32 v82, v74, v75 op_sel:[0,0,1]
	v_lshlrev_b64 v[66:67], 15, v[66:67]
	v_lshlrev_b32_e32 v68, 7, v86
	v_and_or_b32 v70, v70, s12, v84
	v_lshlrev_b32_e32 v71, 6, v87
	v_lshlrev_b32_e32 v72, 2, v87
	v_and_b32_e32 v68, 0x4000, v68
	v_mov_b32_e32 v69, v137
	v_and_or_b32 v71, v71, s13, v85
	v_lshlrev_b32_e32 v70, 10, v70
	v_and_b32_e32 v72, 32, v72
	v_lshl_add_u64 v[66:67], s[70:71], 0, v[66:67]
	v_bitop3_b32 v70, v71, v70, v72 bitop3:0xde
	v_mov_b32_e32 v71, v137
	v_lshl_add_u64 v[66:67], v[66:67], 0, v[68:69]
	v_lshl_add_u64 v[66:67], v[66:67], 0, v[70:71]
	global_store_dwordx4 v[66:67], v[80:83], off sc1
	s_waitcnt lgkmcnt(0)

.LBB0_30:
	s_ashr_i32 s0, s4, 31
	v_add_u32_e32 v143, s35, v154
	s_lshr_b32 s0, s0, 26
	s_add_i32 s0, s4, s0
	v_ashrrev_i32_e32 v138, 6, v143
	s_ashr_i32 s2, s0, 6
	v_ashrrev_i32_e32 v140, 8, v177
	v_ashrrev_i32_e32 v139, 31, v138
	v_mad_i64_i32 v[140:141], s[0:1], s2, v140, v[138:139]
	v_lshlrev_b64 v[144:145], 15, v[140:141]
	v_lshlrev_b32_e32 v140, 7, v177
	v_and_b32_e32 v146, 0x4000, v140
	v_lshrrev_b32_e32 v141, 3, v142
	v_bfe_u32 v140, v143, 5, 1
	v_and_or_b32 v148, v141, s12, v140
	v_lshlrev_b32_e32 v141, 1, v143
	v_lshlrev_b32_e32 v149, 6, v142
	v_and_b32_e32 v141, 62, v141
	v_lshlrev_b32_e32 v142, 2, v142
	v_mov_b32_e32 v147, v137
	v_and_or_b32 v143, v149, s13, v141
	v_lshlrev_b32_e32 v148, 10, v148
	v_and_b32_e32 v142, 32, v142
	v_lshl_add_u64 v[144:145], s[70:71], 0, v[144:145]
	v_bitop3_b32 v142, v143, v148, v142 bitop3:0xde
	v_mov_b32_e32 v143, v137
	v_lshl_add_u64 v[144:145], v[144:145], 0, v[146:147]
	v_lshl_add_u64 v[142:143], v[144:145], 0, v[142:143]
	global_store_dwordx4 v[142:143], v[130:133], off sc1
	ds_read2_b32 v[130:131], v155 offset0:8 offset1:73
	ds_read2_b32 v[132:133], v155 offset0:138 offset1:203
	s_waitcnt lgkmcnt(1)
	v_cvt_pk_bf16_f32 v130, v130, v131
	s_waitcnt lgkmcnt(0)
	v_cvt_pk_bf16_f32 v131, v132, v133
	ds_read2_b32 v[132:133], v172 offset0:12 offset1:77
	ds_read2_b32 v[142:143], v172 offset0:142 offset1:207
	s_waitcnt lgkmcnt(1)
	v_cvt_pk_bf16_f32 v132, v132, v133
	s_waitcnt lgkmcnt(0)
	v_cvt_pk_bf16_f32 v133, v142, v143
	v_cndmask_b32_e64 v143, 0, 1, s[90:91]
	v_add_u32_e32 v142, s15, v156
	s_mov_b64 s[96:97], -1
	v_cmp_ne_u32_e64 s[0:1], 1, v143
	s_andn2_b64 vcc, exec, s[90:91]
	s_cbranch_vccnz .LBB0_32
	v_and_b32_e32 v143, 0x7f, v142
	s_mov_b64 s[96:97], 0

.LBB0_34:
	v_ashrrev_i32_e32 v144, 8, v142
	v_lshlrev_b32_e32 v142, 7, v142
	v_mad_i64_i32 v[144:145], s[26:27], s2, v144, v[138:139]
	v_and_b32_e32 v146, 0x4000, v142
	v_lshrrev_b32_e32 v142, 3, v143
	v_lshlrev_b64 v[144:145], 15, v[144:145]
	v_and_or_b32 v142, v142, s12, v140
	v_lshlrev_b32_e32 v148, 6, v143
	v_lshlrev_b32_e32 v143, 2, v143
	v_mov_b32_e32 v147, v137
	v_and_or_b32 v148, v148, s13, v141
	v_lshlrev_b32_e32 v142, 10, v142
	v_and_b32_e32 v143, 32, v143
	v_lshl_add_u64 v[144:145], s[70:71], 0, v[144:145]
	v_bitop3_b32 v142, v148, v142, v143 bitop3:0xde
	v_mov_b32_e32 v143, v137
	v_lshl_add_u64 v[144:145], v[144:145], 0, v[146:147]
	v_lshl_add_u64 v[142:143], v[144:145], 0, v[142:143]
	global_store_dwordx4 v[142:143], v[130:133], off sc1
	ds_read2_b32 v[130:131], v155 offset0:16 offset1:81
	ds_read2_b32 v[132:133], v155 offset0:146 offset1:211
	s_waitcnt lgkmcnt(1)
	v_cvt_pk_bf16_f32 v130, v130, v131
	s_waitcnt lgkmcnt(0)
	v_cvt_pk_bf16_f32 v131, v132, v133
	ds_read2_b32 v[132:133], v172 offset0:20 offset1:85
	ds_read2_b32 v[142:143], v172 offset0:150 offset1:215
	s_waitcnt lgkmcnt(1)
	v_cvt_pk_bf16_f32 v132, v132, v133
	s_waitcnt lgkmcnt(0)
	v_cvt_pk_bf16_f32 v133, v142, v143
	v_add_u32_e32 v142, s15, v157
	s_mov_b64 s[96:97], -1
	s_and_b64 vcc, exec, s[0:1]
	s_cbranch_vccnz .LBB0_36
	v_and_b32_e32 v143, 0x7f, v142
	s_mov_b64 s[96:97], 0

.LBB0_38:
	v_ashrrev_i32_e32 v144, 8, v142
	v_lshlrev_b32_e32 v142, 7, v142
	v_mad_i64_i32 v[144:145], s[26:27], s2, v144, v[138:139]
	v_and_b32_e32 v146, 0x4000, v142
	v_lshrrev_b32_e32 v142, 3, v143
	v_lshlrev_b64 v[144:145], 15, v[144:145]
	v_and_or_b32 v142, v142, s12, v140
	v_lshlrev_b32_e32 v148, 6, v143
	v_lshlrev_b32_e32 v143, 2, v143
	v_mov_b32_e32 v147, v137
	v_and_or_b32 v148, v148, s13, v141
	v_lshlrev_b32_e32 v142, 10, v142
	v_and_b32_e32 v143, 32, v143
	v_lshl_add_u64 v[144:145], s[70:71], 0, v[144:145]
	v_bitop3_b32 v142, v148, v142, v143 bitop3:0xde
	v_mov_b32_e32 v143, v137
	v_lshl_add_u64 v[144:145], v[144:145], 0, v[146:147]
	v_lshl_add_u64 v[142:143], v[144:145], 0, v[142:143]
	global_store_dwordx4 v[142:143], v[130:133], off sc1
	ds_read2_b32 v[130:131], v155 offset0:24 offset1:89
	ds_read2_b32 v[132:133], v155 offset0:154 offset1:219
	s_waitcnt lgkmcnt(1)
	v_cvt_pk_bf16_f32 v130, v130, v131
	s_waitcnt lgkmcnt(0)
	v_cvt_pk_bf16_f32 v131, v132, v133
	ds_read2_b32 v[132:133], v172 offset0:28 offset1:93
	ds_read2_b32 v[142:143], v172 offset0:158 offset1:223
	s_waitcnt lgkmcnt(1)
	v_cvt_pk_bf16_f32 v132, v132, v133
	s_waitcnt lgkmcnt(0)
	v_cvt_pk_bf16_f32 v133, v142, v143
	v_add_u32_e32 v142, s15, v158
	s_mov_b64 s[96:97], -1
	s_and_b64 vcc, exec, s[0:1]
	s_cbranch_vccnz .LBB0_40
	v_and_b32_e32 v143, 0x7f, v142
	s_mov_b64 s[96:97], 0

.LBB0_42:
	v_ashrrev_i32_e32 v144, 8, v142
	v_lshlrev_b32_e32 v142, 7, v142
	v_mad_i64_i32 v[144:145], s[26:27], s2, v144, v[138:139]
	v_and_b32_e32 v146, 0x4000, v142
	v_lshrrev_b32_e32 v142, 3, v143
	v_lshlrev_b64 v[144:145], 15, v[144:145]
	v_and_or_b32 v142, v142, s12, v140
	v_lshlrev_b32_e32 v148, 6, v143
	v_lshlrev_b32_e32 v143, 2, v143
	v_mov_b32_e32 v147, v137
	v_and_or_b32 v148, v148, s13, v141
	v_lshlrev_b32_e32 v142, 10, v142
	v_and_b32_e32 v143, 32, v143
	v_lshl_add_u64 v[144:145], s[70:71], 0, v[144:145]
	v_bitop3_b32 v142, v148, v142, v143 bitop3:0xde
	v_mov_b32_e32 v143, v137
	v_lshl_add_u64 v[144:145], v[144:145], 0, v[146:147]
	v_lshl_add_u64 v[142:143], v[144:145], 0, v[142:143]
	global_store_dwordx4 v[142:143], v[130:133], off sc1
	ds_read2_b32 v[130:131], v155 offset0:32 offset1:97
	ds_read2_b32 v[132:133], v155 offset0:162 offset1:227
	s_waitcnt lgkmcnt(1)
	v_cvt_pk_bf16_f32 v130, v130, v131
	s_waitcnt lgkmcnt(0)
	v_cvt_pk_bf16_f32 v131, v132, v133
	ds_read2_b32 v[132:133], v172 offset0:36 offset1:101
	ds_read2_b32 v[142:143], v172 offset0:166 offset1:231
	s_waitcnt lgkmcnt(1)
	v_cvt_pk_bf16_f32 v132, v132, v133
	s_waitcnt lgkmcnt(0)
	v_cvt_pk_bf16_f32 v133, v142, v143
	v_add_u32_e32 v142, s15, v159
	s_mov_b64 s[96:97], -1
	s_and_b64 vcc, exec, s[0:1]
	s_cbranch_vccnz .LBB0_44
	v_and_b32_e32 v143, 0x7f, v142
	s_mov_b64 s[96:97], 0

.LBB0_46:
	v_ashrrev_i32_e32 v144, 8, v142
	v_lshlrev_b32_e32 v142, 7, v142
	v_mad_i64_i32 v[144:145], s[26:27], s2, v144, v[138:139]
	v_and_b32_e32 v146, 0x4000, v142
	v_lshrrev_b32_e32 v142, 3, v143
	v_lshlrev_b64 v[144:145], 15, v[144:145]
	v_and_or_b32 v142, v142, s12, v140
	v_lshlrev_b32_e32 v148, 6, v143
	v_lshlrev_b32_e32 v143, 2, v143
	v_mov_b32_e32 v147, v137
	v_and_or_b32 v148, v148, s13, v141
	v_lshlrev_b32_e32 v142, 10, v142
	v_and_b32_e32 v143, 32, v143
	v_lshl_add_u64 v[144:145], s[70:71], 0, v[144:145]
	v_bitop3_b32 v142, v148, v142, v143 bitop3:0xde
	v_mov_b32_e32 v143, v137
	v_lshl_add_u64 v[144:145], v[144:145], 0, v[146:147]
	v_lshl_add_u64 v[142:143], v[144:145], 0, v[142:143]
	global_store_dwordx4 v[142:143], v[130:133], off sc1
	ds_read2_b32 v[130:131], v155 offset0:40 offset1:105
	ds_read2_b32 v[132:133], v155 offset0:170 offset1:235
	s_waitcnt lgkmcnt(1)
	v_cvt_pk_bf16_f32 v130, v130, v131
	s_waitcnt lgkmcnt(0)
	v_cvt_pk_bf16_f32 v131, v132, v133
	ds_read2_b32 v[132:133], v172 offset0:44 offset1:109
	ds_read2_b32 v[142:143], v172 offset0:174 offset1:239
	s_waitcnt lgkmcnt(1)
	v_cvt_pk_bf16_f32 v132, v132, v133
	s_waitcnt lgkmcnt(0)
	v_cvt_pk_bf16_f32 v133, v142, v143
	v_add_u32_e32 v142, s15, v160
	s_mov_b64 s[96:97], -1
	s_and_b64 vcc, exec, s[0:1]
	s_cbranch_vccnz .LBB0_48
	v_and_b32_e32 v143, 0x7f, v142
	s_mov_b64 s[96:97], 0

.LBB0_50:
	v_ashrrev_i32_e32 v144, 8, v142
	v_lshlrev_b32_e32 v142, 7, v142
	v_mad_i64_i32 v[144:145], s[26:27], s2, v144, v[138:139]
	v_and_b32_e32 v146, 0x4000, v142
	v_lshrrev_b32_e32 v142, 3, v143
	v_lshlrev_b64 v[144:145], 15, v[144:145]
	v_and_or_b32 v142, v142, s12, v140
	v_lshlrev_b32_e32 v148, 6, v143
	v_lshlrev_b32_e32 v143, 2, v143
	v_mov_b32_e32 v147, v137
	v_and_or_b32 v148, v148, s13, v141
	v_lshlrev_b32_e32 v142, 10, v142
	v_and_b32_e32 v143, 32, v143
	v_lshl_add_u64 v[144:145], s[70:71], 0, v[144:145]
	v_bitop3_b32 v142, v148, v142, v143 bitop3:0xde
	v_mov_b32_e32 v143, v137
	v_lshl_add_u64 v[144:145], v[144:145], 0, v[146:147]
	v_lshl_add_u64 v[142:143], v[144:145], 0, v[142:143]
	global_store_dwordx4 v[142:143], v[130:133], off sc1
	ds_read2_b32 v[130:131], v155 offset0:48 offset1:113
	ds_read2_b32 v[132:133], v155 offset0:178 offset1:243
	s_waitcnt lgkmcnt(1)
	v_cvt_pk_bf16_f32 v130, v130, v131
	s_waitcnt lgkmcnt(0)
	v_cvt_pk_bf16_f32 v131, v132, v133
	ds_read2_b32 v[132:133], v172 offset0:52 offset1:117
	ds_read2_b32 v[142:143], v172 offset0:182 offset1:247
	s_waitcnt lgkmcnt(1)
	v_cvt_pk_bf16_f32 v132, v132, v133
	s_waitcnt lgkmcnt(0)
	v_cvt_pk_bf16_f32 v133, v142, v143
	v_add_u32_e32 v142, s15, v161
	s_mov_b64 s[96:97], -1
	s_and_b64 vcc, exec, s[0:1]
	s_cbranch_vccnz .LBB0_52
	v_and_b32_e32 v143, 0x7f, v142
	s_mov_b64 s[96:97], 0

.LBB0_54:
	v_ashrrev_i32_e32 v144, 8, v142
	v_lshlrev_b32_e32 v142, 7, v142
	v_mad_i64_i32 v[144:145], s[26:27], s2, v144, v[138:139]
	v_and_b32_e32 v146, 0x4000, v142
	v_lshrrev_b32_e32 v142, 3, v143
	v_lshlrev_b64 v[144:145], 15, v[144:145]
	v_and_or_b32 v142, v142, s12, v140
	v_lshlrev_b32_e32 v148, 6, v143
	v_lshlrev_b32_e32 v143, 2, v143
	v_mov_b32_e32 v147, v137
	v_and_or_b32 v148, v148, s13, v141
	v_lshlrev_b32_e32 v142, 10, v142
	v_and_b32_e32 v143, 32, v143
	v_lshl_add_u64 v[144:145], s[70:71], 0, v[144:145]
	v_bitop3_b32 v142, v148, v142, v143 bitop3:0xde
	v_mov_b32_e32 v143, v137
	v_lshl_add_u64 v[144:145], v[144:145], 0, v[146:147]
	v_lshl_add_u64 v[142:143], v[144:145], 0, v[142:143]
	global_store_dwordx4 v[142:143], v[130:133], off sc1
	ds_read2_b32 v[130:131], v155 offset0:56 offset1:121
	ds_read2_b32 v[132:133], v155 offset0:186 offset1:251
	s_waitcnt lgkmcnt(1)
	v_cvt_pk_bf16_f32 v130, v130, v131
	s_waitcnt lgkmcnt(0)
	v_cvt_pk_bf16_f32 v131, v132, v133
	ds_read2_b32 v[132:133], v172 offset0:60 offset1:125
	ds_read2_b32 v[142:143], v172 offset0:190 offset1:255
	s_waitcnt lgkmcnt(1)
	v_cvt_pk_bf16_f32 v132, v132, v133
	s_waitcnt lgkmcnt(0)
	v_cvt_pk_bf16_f32 v133, v142, v143
	v_add_u32_e32 v142, s15, v162
	s_mov_b64 s[96:97], -1
	s_and_b64 vcc, exec, s[0:1]
	s_cbranch_vccnz .LBB0_56
	v_and_b32_e32 v143, 0x7f, v142
	s_mov_b64 s[96:97], 0

.LBB0_58:
	v_ashrrev_i32_e32 v144, 8, v142
	v_lshlrev_b32_e32 v142, 7, v142
	v_mad_i64_i32 v[138:139], s[0:1], s2, v144, v[138:139]
	v_and_b32_e32 v144, 0x4000, v142
	v_lshrrev_b32_e32 v142, 3, v143
	v_and_or_b32 v140, v142, s12, v140
	v_lshlrev_b32_e32 v142, 6, v143
	v_lshlrev_b64 v[138:139], 15, v[138:139]
	v_and_or_b32 v141, v142, s13, v141
	v_lshlrev_b32_e32 v142, 2, v143
	v_mov_b32_e32 v145, v137
	v_lshlrev_b32_e32 v140, 10, v140
	v_and_b32_e32 v142, 32, v142
	v_lshl_add_u64 v[138:139], s[70:71], 0, v[138:139]
	v_bitop3_b32 v140, v141, v140, v142 bitop3:0xde
	v_mov_b32_e32 v141, v137
	v_lshl_add_u64 v[138:139], v[138:139], 0, v[144:145]
	v_lshl_add_u64 v[138:139], v[138:139], 0, v[140:141]
	global_store_dwordx4 v[138:139], v[130:133], off sc1
	s_waitcnt lgkmcnt(0)
	s_mov_b64 s[0:1], 0

.LBB0_64:
	s_waitcnt lgkmcnt(7)
	v_mul_f32_e32 v148, 0x42800000, v148
	v_mul_f32_e32 v149, 0x42800000, v149
	s_waitcnt lgkmcnt(6)
	v_mul_f32_e32 v151, 0x42800000, v146
	v_med3_f32 v148, v148, s20, v171
	v_med3_f32 v149, v149, s20, v171
	v_mov_b32_e32 v146, v137
	v_cvt_pk_fp8_f32 v146, v148, v149
	s_waitcnt lgkmcnt(1)
	v_mul_f32_e32 v132, 0x42800000, v132
	v_mul_f32_e32 v133, 0x42800000, v133
	v_mul_f32_e32 v147, 0x42800000, v147
	v_med3_f32 v132, v132, s20, v171
	v_med3_f32 v133, v133, s20, v171
	v_mov_b32_e32 v149, v137
	v_med3_f32 v148, v151, s20, v171
	v_med3_f32 v147, v147, s20, v171
	v_mul_f32_e32 v144, 0x42800000, v144
	v_mul_f32_e32 v145, 0x42800000, v145
	v_cvt_pk_fp8_f32 v149, v132, v133
	v_cvt_pk_fp8_f32 v146, v148, v147 op_sel:[0,0,1]
	v_med3_f32 v144, v144, s20, v171
	v_med3_f32 v145, v145, s20, v171
	v_mov_b32_e32 v147, v137
	v_mul_f32_e32 v140, 0x42800000, v140
	v_mul_f32_e32 v141, 0x42800000, v141
	v_cvt_pk_fp8_f32 v147, v144, v145
	v_med3_f32 v140, v140, s20, v171
	v_med3_f32 v141, v141, s20, v171
	v_mov_b32_e32 v148, v137
	s_waitcnt lgkmcnt(0)
	v_mul_f32_e32 v130, 0x42800000, v130
	v_mul_f32_e32 v131, 0x42800000, v131
	s_ashr_i32 s0, s4, 31
	v_cvt_pk_fp8_f32 v148, v140, v141
	v_med3_f32 v130, v130, s20, v171
	v_med3_f32 v131, v131, s20, v171
	v_add_u32_e32 v140, s35, v163
	s_lshr_b32 s0, s0, 25
	v_mul_f32_e32 v142, 0x42800000, v142
	v_mul_f32_e32 v143, 0x42800000, v143
	v_cvt_pk_fp8_f32 v149, v130, v131 op_sel:[0,0,1]
	s_add_i32 s0, s4, s0
	v_ashrrev_i32_e32 v130, 7, v140
	v_med3_f32 v142, v142, s20, v171
	v_med3_f32 v143, v143, s20, v171
	v_mul_f32_e32 v138, 0x42800000, v138
	v_mul_f32_e32 v139, 0x42800000, v139
	s_ashr_i32 s2, s0, 7
	v_ashrrev_i32_e32 v132, 8, v176
	v_ashrrev_i32_e32 v131, 31, v130
	v_cvt_pk_fp8_f32 v147, v142, v143 op_sel:[0,0,1]
	v_med3_f32 v138, v138, s20, v171
	v_med3_f32 v139, v139, s20, v171
	v_mad_i64_i32 v[132:133], s[0:1], s2, v132, v[130:131]
	v_lshrrev_b32_e32 v141, 3, v150
	v_bfe_u32 v208, v140, 6, 1
	v_lshlrev_b32_e32 v142, 6, v150
	v_and_b32_e32 v209, 62, v140
	v_cvt_pk_fp8_f32 v148, v138, v139 op_sel:[0,0,1]
	v_lshlrev_b64 v[132:133], 15, v[132:133]
	v_lshlrev_b32_e32 v138, 7, v176
	v_and_or_b32 v141, v141, s12, v208
	v_and_or_b32 v140, v142, s13, v209
	v_lshlrev_b32_e32 v142, 2, v150
	v_and_b32_e32 v138, 0x4000, v138
	v_mov_b32_e32 v139, v137
	v_lshlrev_b32_e32 v141, 10, v141
	v_and_b32_e32 v142, 32, v142
	v_lshl_add_u64 v[132:133], s[70:71], 0, v[132:133]
	v_bitop3_b32 v140, v140, v141, v142 bitop3:0xde
	v_mov_b32_e32 v141, v137
	v_lshl_add_u64 v[132:133], v[132:133], 0, v[138:139]
	v_lshl_add_u64 v[132:133], v[132:133], 0, v[140:141]
	global_store_dwordx4 v[132:133], v[146:149], off sc1
	ds_read2_b32 v[150:151], v164 offset0:16 offset1:81
	ds_read2_b32 v[148:149], v164 offset0:146 offset1:211
	ds_read2_b32 v[146:147], v175 offset0:20 offset1:85
	ds_read2_b32 v[144:145], v175 offset0:150 offset1:215
	ds_read2_b32 v[142:143], v174 offset0:24 offset1:89
	ds_read2_b32 v[140:141], v174 offset0:154 offset1:219
	ds_read2_b32 v[138:139], v173 offset0:28 offset1:93
	ds_read2_b32 v[132:133], v173 offset0:158 offset1:223
	v_cndmask_b32_e64 v211, 0, 1, s[90:91]
	v_add_u32_e32 v210, s15, v165
	v_cmp_ne_u32_e64 s[0:1], 1, v211
	s_andn2_b64 vcc, exec, s[90:91]
	s_mov_b64 s[96:97], -1
	s_cbranch_vccnz .LBB0_66
	v_and_b32_e32 v211, 0x7f, v210
	s_mov_b64 s[96:97], 0

.LBB0_68:
	s_waitcnt lgkmcnt(7)
	v_mul_f32_e32 v150, 0x42800000, v150
	v_mul_f32_e32 v151, 0x42800000, v151
	s_waitcnt lgkmcnt(6)
	v_mul_f32_e32 v212, 0x42800000, v148
	v_med3_f32 v150, v150, s20, v171
	v_med3_f32 v151, v151, s20, v171
	v_mov_b32_e32 v148, v137
	v_cvt_pk_fp8_f32 v148, v150, v151
	v_mul_f32_e32 v149, 0x42800000, v149
	s_waitcnt lgkmcnt(1)
	v_mul_f32_e32 v138, 0x42800000, v138
	v_mul_f32_e32 v139, 0x42800000, v139
	v_med3_f32 v150, v212, s20, v171
	v_med3_f32 v149, v149, s20, v171
	v_mul_f32_e32 v142, 0x42800000, v142
	v_mul_f32_e32 v143, 0x42800000, v143
	v_med3_f32 v138, v138, s20, v171
	v_med3_f32 v139, v139, s20, v171
	v_mov_b32_e32 v151, v137
	v_cvt_pk_fp8_f32 v148, v150, v149 op_sel:[0,0,1]
	v_mul_f32_e32 v146, 0x42800000, v146
	v_mul_f32_e32 v147, 0x42800000, v147
	v_med3_f32 v142, v142, s20, v171
	v_med3_f32 v143, v143, s20, v171
	v_mov_b32_e32 v150, v137
	v_cvt_pk_fp8_f32 v151, v138, v139
	v_med3_f32 v146, v146, s20, v171
	v_med3_f32 v147, v147, s20, v171
	v_mov_b32_e32 v149, v137
	v_cvt_pk_fp8_f32 v150, v142, v143
	v_cvt_pk_fp8_f32 v149, v146, v147
	s_waitcnt lgkmcnt(0)
	v_mul_f32_e32 v132, 0x42800000, v132
	v_mul_f32_e32 v133, 0x42800000, v133
	v_mul_f32_e32 v140, 0x42800000, v140
	v_mul_f32_e32 v141, 0x42800000, v141
	v_med3_f32 v132, v132, s20, v171
	v_med3_f32 v133, v133, s20, v171
	v_mul_f32_e32 v144, 0x42800000, v144
	v_mul_f32_e32 v145, 0x42800000, v145
	v_med3_f32 v140, v140, s20, v171
	v_med3_f32 v141, v141, s20, v171
	v_cvt_pk_fp8_f32 v151, v132, v133 op_sel:[0,0,1]
	v_ashrrev_i32_e32 v132, 8, v210
	v_med3_f32 v144, v144, s20, v171
	v_med3_f32 v145, v145, s20, v171
	v_cvt_pk_fp8_f32 v150, v140, v141 op_sel:[0,0,1]
	v_mad_i64_i32 v[132:133], s[26:27], s2, v132, v[130:131]
	v_lshrrev_b32_e32 v140, 3, v211
	v_cvt_pk_fp8_f32 v149, v144, v145 op_sel:[0,0,1]
	v_lshlrev_b64 v[132:133], 15, v[132:133]
	v_lshlrev_b32_e32 v138, 7, v210
	v_and_or_b32 v140, v140, s12, v208
	v_lshlrev_b32_e32 v141, 6, v211
	v_lshlrev_b32_e32 v142, 2, v211
	v_and_b32_e32 v138, 0x4000, v138
	v_mov_b32_e32 v139, v137
	v_and_or_b32 v141, v141, s13, v209
	v_lshlrev_b32_e32 v140, 10, v140
	v_and_b32_e32 v142, 32, v142
	v_lshl_add_u64 v[132:133], s[70:71], 0, v[132:133]
	v_bitop3_b32 v140, v141, v140, v142 bitop3:0xde
	v_mov_b32_e32 v141, v137
	v_lshl_add_u64 v[132:133], v[132:133], 0, v[138:139]
	v_lshl_add_u64 v[132:133], v[132:133], 0, v[140:141]
	global_store_dwordx4 v[132:133], v[148:151], off sc1
	ds_read2_b32 v[150:151], v164 offset0:32 offset1:97
	ds_read2_b32 v[148:149], v164 offset0:162 offset1:227
	ds_read2_b32 v[146:147], v175 offset0:36 offset1:101
	ds_read2_b32 v[144:145], v175 offset0:166 offset1:231
	ds_read2_b32 v[142:143], v174 offset0:40 offset1:105
	ds_read2_b32 v[140:141], v174 offset0:170 offset1:235
	ds_read2_b32 v[138:139], v173 offset0:44 offset1:109
	ds_read2_b32 v[132:133], v173 offset0:174 offset1:239
	v_add_u32_e32 v210, s15, v166
	s_mov_b64 s[96:97], -1
	s_and_b64 vcc, exec, s[0:1]
	s_cbranch_vccnz .LBB0_70
	v_and_b32_e32 v211, 0x7f, v210
	s_mov_b64 s[96:97], 0

.LBB0_72:
	s_waitcnt lgkmcnt(7)
	v_mul_f32_e32 v150, 0x42800000, v150
	v_mul_f32_e32 v151, 0x42800000, v151
	s_waitcnt lgkmcnt(6)
	v_mul_f32_e32 v212, 0x42800000, v148
	v_med3_f32 v150, v150, s20, v171
	v_med3_f32 v151, v151, s20, v171
	v_mov_b32_e32 v148, v137
	v_cvt_pk_fp8_f32 v148, v150, v151
	v_mul_f32_e32 v149, 0x42800000, v149
	s_waitcnt lgkmcnt(1)
	v_mul_f32_e32 v138, 0x42800000, v138
	v_mul_f32_e32 v139, 0x42800000, v139
	v_med3_f32 v150, v212, s20, v171
	v_med3_f32 v149, v149, s20, v171
	v_mul_f32_e32 v142, 0x42800000, v142
	v_mul_f32_e32 v143, 0x42800000, v143
	v_med3_f32 v138, v138, s20, v171
	v_med3_f32 v139, v139, s20, v171
	v_mov_b32_e32 v151, v137
	v_cvt_pk_fp8_f32 v148, v150, v149 op_sel:[0,0,1]
	v_mul_f32_e32 v146, 0x42800000, v146
	v_mul_f32_e32 v147, 0x42800000, v147
	v_med3_f32 v142, v142, s20, v171
	v_med3_f32 v143, v143, s20, v171
	v_mov_b32_e32 v150, v137
	v_cvt_pk_fp8_f32 v151, v138, v139
	v_med3_f32 v146, v146, s20, v171
	v_med3_f32 v147, v147, s20, v171
	v_mov_b32_e32 v149, v137
	v_cvt_pk_fp8_f32 v150, v142, v143
	v_cvt_pk_fp8_f32 v149, v146, v147
	s_waitcnt lgkmcnt(0)
	v_mul_f32_e32 v132, 0x42800000, v132
	v_mul_f32_e32 v133, 0x42800000, v133
	v_mul_f32_e32 v140, 0x42800000, v140
	v_mul_f32_e32 v141, 0x42800000, v141
	v_med3_f32 v132, v132, s20, v171
	v_med3_f32 v133, v133, s20, v171
	v_mul_f32_e32 v144, 0x42800000, v144
	v_mul_f32_e32 v145, 0x42800000, v145
	v_med3_f32 v140, v140, s20, v171
	v_med3_f32 v141, v141, s20, v171
	v_cvt_pk_fp8_f32 v151, v132, v133 op_sel:[0,0,1]
	v_ashrrev_i32_e32 v132, 8, v210
	v_med3_f32 v144, v144, s20, v171
	v_med3_f32 v145, v145, s20, v171
	v_cvt_pk_fp8_f32 v150, v140, v141 op_sel:[0,0,1]
	v_mad_i64_i32 v[132:133], s[26:27], s2, v132, v[130:131]
	v_lshrrev_b32_e32 v140, 3, v211
	v_cvt_pk_fp8_f32 v149, v144, v145 op_sel:[0,0,1]
	v_lshlrev_b64 v[132:133], 15, v[132:133]
	v_lshlrev_b32_e32 v138, 7, v210
	v_and_or_b32 v140, v140, s12, v208
	v_lshlrev_b32_e32 v141, 6, v211
	v_lshlrev_b32_e32 v142, 2, v211
	v_and_b32_e32 v138, 0x4000, v138
	v_mov_b32_e32 v139, v137
	v_and_or_b32 v141, v141, s13, v209
	v_lshlrev_b32_e32 v140, 10, v140
	v_and_b32_e32 v142, 32, v142
	v_lshl_add_u64 v[132:133], s[70:71], 0, v[132:133]
	v_bitop3_b32 v140, v141, v140, v142 bitop3:0xde
	v_mov_b32_e32 v141, v137
	v_lshl_add_u64 v[132:133], v[132:133], 0, v[138:139]
	v_lshl_add_u64 v[132:133], v[132:133], 0, v[140:141]
	global_store_dwordx4 v[132:133], v[148:151], off sc1
	ds_read2_b32 v[148:149], v164 offset0:48 offset1:113
	ds_read2_b32 v[150:151], v164 offset0:178 offset1:243
	ds_read2_b32 v[144:145], v175 offset0:52 offset1:117
	ds_read2_b32 v[146:147], v175 offset0:182 offset1:247
	ds_read2_b32 v[140:141], v174 offset0:56 offset1:121
	ds_read2_b32 v[142:143], v174 offset0:186 offset1:251
	ds_read2_b32 v[132:133], v173 offset0:60 offset1:125
	ds_read2_b32 v[138:139], v173 offset0:190 offset1:255
	v_add_u32_e32 v210, s15, v167
	s_mov_b64 s[96:97], -1
	s_and_b64 vcc, exec, s[0:1]
	s_cbranch_vccnz .LBB0_74
	v_and_b32_e32 v211, 0x7f, v210
	s_mov_b64 s[96:97], 0

.LBB0_76:
	s_waitcnt lgkmcnt(7)
	v_mul_f32_e32 v148, 0x42800000, v148
	v_med3_f32 v212, v148, s20, v171
	v_mul_f32_e32 v148, 0x42800000, v149
	v_med3_f32 v149, v148, s20, v171
	v_mov_b32_e32 v148, v137
	v_cvt_pk_fp8_f32 v148, v212, v149
	s_waitcnt lgkmcnt(6)
	v_mul_f32_e32 v150, 0x42800000, v150
	v_mul_f32_e32 v151, 0x42800000, v151
	v_med3_f32 v150, v150, s20, v171
	v_med3_f32 v151, v151, s20, v171
	s_waitcnt lgkmcnt(1)
	v_mul_f32_e32 v132, 0x42800000, v132
	v_mul_f32_e32 v133, 0x42800000, v133
	v_cvt_pk_fp8_f32 v148, v150, v151 op_sel:[0,0,1]
	v_mul_f32_e32 v144, 0x42800000, v144
	v_mul_f32_e32 v145, 0x42800000, v145
	v_mul_f32_e32 v140, 0x42800000, v140
	v_mul_f32_e32 v141, 0x42800000, v141
	v_med3_f32 v132, v132, s20, v171
	v_med3_f32 v133, v133, s20, v171
	v_mov_b32_e32 v151, v137
	v_med3_f32 v144, v144, s20, v171
	v_med3_f32 v145, v145, s20, v171
	v_mov_b32_e32 v149, v137
	v_med3_f32 v140, v140, s20, v171
	v_med3_f32 v141, v141, s20, v171
	v_mov_b32_e32 v150, v137
	v_cvt_pk_fp8_f32 v151, v132, v133
	v_cvt_pk_fp8_f32 v149, v144, v145
	v_cvt_pk_fp8_f32 v150, v140, v141
	s_waitcnt lgkmcnt(0)
	v_mul_f32_e32 v138, 0x42800000, v138
	v_mul_f32_e32 v139, 0x42800000, v139
	v_mul_f32_e32 v146, 0x42800000, v146
	v_mul_f32_e32 v147, 0x42800000, v147
	v_mul_f32_e32 v142, 0x42800000, v142
	v_mul_f32_e32 v143, 0x42800000, v143
	v_med3_f32 v138, v138, s20, v171
	v_med3_f32 v139, v139, s20, v171
	v_ashrrev_i32_e32 v132, 8, v210
	v_med3_f32 v146, v146, s20, v171
	v_med3_f32 v147, v147, s20, v171
	v_med3_f32 v142, v142, s20, v171
	v_med3_f32 v143, v143, s20, v171
	v_cvt_pk_fp8_f32 v151, v138, v139 op_sel:[0,0,1]
	v_mad_i64_i32 v[130:131], s[0:1], s2, v132, v[130:131]
	v_lshrrev_b32_e32 v138, 3, v211
	v_cvt_pk_fp8_f32 v149, v146, v147 op_sel:[0,0,1]
	v_cvt_pk_fp8_f32 v150, v142, v143 op_sel:[0,0,1]
	v_lshlrev_b64 v[130:131], 15, v[130:131]
	v_lshlrev_b32_e32 v132, 7, v210
	v_and_or_b32 v138, v138, s12, v208
	v_lshlrev_b32_e32 v139, 6, v211
	v_lshlrev_b32_e32 v140, 2, v211
	v_and_b32_e32 v132, 0x4000, v132
	v_mov_b32_e32 v133, v137
	v_and_or_b32 v139, v139, s13, v209
	v_lshlrev_b32_e32 v138, 10, v138
	v_and_b32_e32 v140, 32, v140
	v_lshl_add_u64 v[130:131], s[70:71], 0, v[130:131]
	v_bitop3_b32 v138, v139, v138, v140 bitop3:0xde
	v_mov_b32_e32 v139, v137
	v_lshl_add_u64 v[130:131], v[130:131], 0, v[132:133]
	v_lshl_add_u64 v[130:131], v[130:131], 0, v[138:139]
	global_store_dwordx4 v[130:131], v[148:151], off sc1
	s_waitcnt lgkmcnt(0)

.LBB0_135:
	s_ashr_i32 s0, s4, 31
	v_add_u32_e32 v75, s35, v168
	s_lshr_b32 s0, s0, 26
	s_add_i32 s0, s4, s0
	v_ashrrev_i32_e32 v70, 6, v75
	s_ashr_i32 s2, s0, 6
	v_ashrrev_i32_e32 v72, 8, v177
	v_ashrrev_i32_e32 v71, 31, v70
	v_mad_i64_i32 v[72:73], s[0:1], s2, v72, v[70:71]
	v_lshlrev_b64 v[76:77], 15, v[72:73]
	v_lshlrev_b32_e32 v72, 7, v177
	v_and_b32_e32 v78, 0x4000, v72
	v_lshrrev_b32_e32 v73, 3, v74
	v_bfe_u32 v72, v75, 5, 1
	v_and_or_b32 v80, v73, s12, v72
	v_lshlrev_b32_e32 v73, 1, v75
	v_lshlrev_b32_e32 v81, 6, v74
	v_and_b32_e32 v73, 62, v73
	v_lshlrev_b32_e32 v74, 2, v74
	v_mov_b32_e32 v79, v137
	v_and_or_b32 v75, v81, s13, v73
	v_lshlrev_b32_e32 v80, 10, v80
	v_and_b32_e32 v74, 32, v74
	v_lshl_add_u64 v[76:77], s[70:71], 0, v[76:77]
	v_bitop3_b32 v74, v75, v80, v74 bitop3:0xde
	v_mov_b32_e32 v75, v137
	v_lshl_add_u64 v[76:77], v[76:77], 0, v[78:79]
	v_lshl_add_u64 v[74:75], v[76:77], 0, v[74:75]
	global_store_dwordx4 v[74:75], v[66:69], off sc1
	ds_read2_b32 v[66:67], v155 offset0:8 offset1:73
	ds_read2_b32 v[68:69], v155 offset0:138 offset1:203
	s_waitcnt lgkmcnt(1)
	v_cvt_pk_bf16_f32 v66, v66, v67
	s_waitcnt lgkmcnt(0)
	v_cvt_pk_bf16_f32 v67, v68, v69
	ds_read2_b32 v[68:69], v172 offset0:12 offset1:77
	ds_read2_b32 v[74:75], v172 offset0:142 offset1:207
	s_waitcnt lgkmcnt(1)
	v_cvt_pk_bf16_f32 v68, v68, v69
	s_waitcnt lgkmcnt(0)
	v_cvt_pk_bf16_f32 v69, v74, v75
	v_cndmask_b32_e64 v75, 0, 1, s[90:91]
	v_add_u32_e32 v74, s15, v156
	s_mov_b64 s[94:95], -1
	v_cmp_ne_u32_e64 s[0:1], 1, v75
	s_andn2_b64 vcc, exec, s[90:91]
	s_cbranch_vccnz .LBB0_137
	v_and_b32_e32 v75, 0x7f, v74
	s_mov_b64 s[94:95], 0

.LBB0_139:
	v_ashrrev_i32_e32 v76, 8, v74
	v_lshlrev_b32_e32 v74, 7, v74
	v_mad_i64_i32 v[76:77], s[26:27], s2, v76, v[70:71]
	v_and_b32_e32 v78, 0x4000, v74
	v_lshrrev_b32_e32 v74, 3, v75
	v_lshlrev_b64 v[76:77], 15, v[76:77]
	v_and_or_b32 v74, v74, s12, v72
	v_lshlrev_b32_e32 v80, 6, v75
	v_lshlrev_b32_e32 v75, 2, v75
	v_mov_b32_e32 v79, v137
	v_and_or_b32 v80, v80, s13, v73
	v_lshlrev_b32_e32 v74, 10, v74
	v_and_b32_e32 v75, 32, v75
	v_lshl_add_u64 v[76:77], s[70:71], 0, v[76:77]
	v_bitop3_b32 v74, v80, v74, v75 bitop3:0xde
	v_mov_b32_e32 v75, v137
	v_lshl_add_u64 v[76:77], v[76:77], 0, v[78:79]
	v_lshl_add_u64 v[74:75], v[76:77], 0, v[74:75]
	global_store_dwordx4 v[74:75], v[66:69], off sc1
	ds_read2_b32 v[66:67], v155 offset0:16 offset1:81
	ds_read2_b32 v[68:69], v155 offset0:146 offset1:211
	s_waitcnt lgkmcnt(1)
	v_cvt_pk_bf16_f32 v66, v66, v67
	s_waitcnt lgkmcnt(0)
	v_cvt_pk_bf16_f32 v67, v68, v69
	ds_read2_b32 v[68:69], v172 offset0:20 offset1:85
	ds_read2_b32 v[74:75], v172 offset0:150 offset1:215
	s_waitcnt lgkmcnt(1)
	v_cvt_pk_bf16_f32 v68, v68, v69
	s_waitcnt lgkmcnt(0)
	v_cvt_pk_bf16_f32 v69, v74, v75
	v_add_u32_e32 v74, s15, v157
	s_mov_b64 s[94:95], -1
	s_and_b64 vcc, exec, s[0:1]
	s_cbranch_vccnz .LBB0_141
	v_and_b32_e32 v75, 0x7f, v74
	s_mov_b64 s[94:95], 0

.LBB0_143:
	v_ashrrev_i32_e32 v76, 8, v74
	v_lshlrev_b32_e32 v74, 7, v74
	v_mad_i64_i32 v[76:77], s[26:27], s2, v76, v[70:71]
	v_and_b32_e32 v78, 0x4000, v74
	v_lshrrev_b32_e32 v74, 3, v75
	v_lshlrev_b64 v[76:77], 15, v[76:77]
	v_and_or_b32 v74, v74, s12, v72
	v_lshlrev_b32_e32 v80, 6, v75
	v_lshlrev_b32_e32 v75, 2, v75
	v_mov_b32_e32 v79, v137
	v_and_or_b32 v80, v80, s13, v73
	v_lshlrev_b32_e32 v74, 10, v74
	v_and_b32_e32 v75, 32, v75
	v_lshl_add_u64 v[76:77], s[70:71], 0, v[76:77]
	v_bitop3_b32 v74, v80, v74, v75 bitop3:0xde
	v_mov_b32_e32 v75, v137
	v_lshl_add_u64 v[76:77], v[76:77], 0, v[78:79]
	v_lshl_add_u64 v[74:75], v[76:77], 0, v[74:75]
	global_store_dwordx4 v[74:75], v[66:69], off sc1
	ds_read2_b32 v[66:67], v155 offset0:24 offset1:89
	ds_read2_b32 v[68:69], v155 offset0:154 offset1:219
	s_waitcnt lgkmcnt(1)
	v_cvt_pk_bf16_f32 v66, v66, v67
	s_waitcnt lgkmcnt(0)
	v_cvt_pk_bf16_f32 v67, v68, v69
	ds_read2_b32 v[68:69], v172 offset0:28 offset1:93
	ds_read2_b32 v[74:75], v172 offset0:158 offset1:223
	s_waitcnt lgkmcnt(1)
	v_cvt_pk_bf16_f32 v68, v68, v69
	s_waitcnt lgkmcnt(0)
	v_cvt_pk_bf16_f32 v69, v74, v75
	v_add_u32_e32 v74, s15, v158
	s_mov_b64 s[94:95], -1
	s_and_b64 vcc, exec, s[0:1]
	s_cbranch_vccnz .LBB0_145
	v_and_b32_e32 v75, 0x7f, v74
	s_mov_b64 s[94:95], 0

.LBB0_147:
	v_ashrrev_i32_e32 v76, 8, v74
	v_lshlrev_b32_e32 v74, 7, v74
	v_mad_i64_i32 v[76:77], s[26:27], s2, v76, v[70:71]
	v_and_b32_e32 v78, 0x4000, v74
	v_lshrrev_b32_e32 v74, 3, v75
	v_lshlrev_b64 v[76:77], 15, v[76:77]
	v_and_or_b32 v74, v74, s12, v72
	v_lshlrev_b32_e32 v80, 6, v75
	v_lshlrev_b32_e32 v75, 2, v75
	v_mov_b32_e32 v79, v137
	v_and_or_b32 v80, v80, s13, v73
	v_lshlrev_b32_e32 v74, 10, v74
	v_and_b32_e32 v75, 32, v75
	v_lshl_add_u64 v[76:77], s[70:71], 0, v[76:77]
	v_bitop3_b32 v74, v80, v74, v75 bitop3:0xde
	v_mov_b32_e32 v75, v137
	v_lshl_add_u64 v[76:77], v[76:77], 0, v[78:79]
	v_lshl_add_u64 v[74:75], v[76:77], 0, v[74:75]
	global_store_dwordx4 v[74:75], v[66:69], off sc1
	ds_read2_b32 v[66:67], v155 offset0:32 offset1:97
	ds_read2_b32 v[68:69], v155 offset0:162 offset1:227
	s_waitcnt lgkmcnt(1)
	v_cvt_pk_bf16_f32 v66, v66, v67
	s_waitcnt lgkmcnt(0)
	v_cvt_pk_bf16_f32 v67, v68, v69
	ds_read2_b32 v[68:69], v172 offset0:36 offset1:101
	ds_read2_b32 v[74:75], v172 offset0:166 offset1:231
	s_waitcnt lgkmcnt(1)
	v_cvt_pk_bf16_f32 v68, v68, v69
	s_waitcnt lgkmcnt(0)
	v_cvt_pk_bf16_f32 v69, v74, v75
	v_add_u32_e32 v74, s15, v159
	s_mov_b64 s[94:95], -1
	s_and_b64 vcc, exec, s[0:1]
	s_cbranch_vccnz .LBB0_149
	v_and_b32_e32 v75, 0x7f, v74
	s_mov_b64 s[94:95], 0

.LBB0_151:
	v_ashrrev_i32_e32 v76, 8, v74
	v_lshlrev_b32_e32 v74, 7, v74
	v_mad_i64_i32 v[76:77], s[26:27], s2, v76, v[70:71]
	v_and_b32_e32 v78, 0x4000, v74
	v_lshrrev_b32_e32 v74, 3, v75
	v_lshlrev_b64 v[76:77], 15, v[76:77]
	v_and_or_b32 v74, v74, s12, v72
	v_lshlrev_b32_e32 v80, 6, v75
	v_lshlrev_b32_e32 v75, 2, v75
	v_mov_b32_e32 v79, v137
	v_and_or_b32 v80, v80, s13, v73
	v_lshlrev_b32_e32 v74, 10, v74
	v_and_b32_e32 v75, 32, v75
	v_lshl_add_u64 v[76:77], s[70:71], 0, v[76:77]
	v_bitop3_b32 v74, v80, v74, v75 bitop3:0xde
	v_mov_b32_e32 v75, v137
	v_lshl_add_u64 v[76:77], v[76:77], 0, v[78:79]
	v_lshl_add_u64 v[74:75], v[76:77], 0, v[74:75]
	global_store_dwordx4 v[74:75], v[66:69], off sc1
	ds_read2_b32 v[66:67], v155 offset0:40 offset1:105
	ds_read2_b32 v[68:69], v155 offset0:170 offset1:235
	s_waitcnt lgkmcnt(1)
	v_cvt_pk_bf16_f32 v66, v66, v67
	s_waitcnt lgkmcnt(0)
	v_cvt_pk_bf16_f32 v67, v68, v69
	ds_read2_b32 v[68:69], v172 offset0:44 offset1:109
	ds_read2_b32 v[74:75], v172 offset0:174 offset1:239
	s_waitcnt lgkmcnt(1)
	v_cvt_pk_bf16_f32 v68, v68, v69
	s_waitcnt lgkmcnt(0)
	v_cvt_pk_bf16_f32 v69, v74, v75
	v_add_u32_e32 v74, s15, v160
	s_mov_b64 s[94:95], -1
	s_and_b64 vcc, exec, s[0:1]
	s_cbranch_vccnz .LBB0_153
	v_and_b32_e32 v75, 0x7f, v74
	s_mov_b64 s[94:95], 0

.LBB0_155:
	v_ashrrev_i32_e32 v76, 8, v74
	v_lshlrev_b32_e32 v74, 7, v74
	v_mad_i64_i32 v[76:77], s[26:27], s2, v76, v[70:71]
	v_and_b32_e32 v78, 0x4000, v74
	v_lshrrev_b32_e32 v74, 3, v75
	v_lshlrev_b64 v[76:77], 15, v[76:77]
	v_and_or_b32 v74, v74, s12, v72
	v_lshlrev_b32_e32 v80, 6, v75
	v_lshlrev_b32_e32 v75, 2, v75
	v_mov_b32_e32 v79, v137
	v_and_or_b32 v80, v80, s13, v73
	v_lshlrev_b32_e32 v74, 10, v74
	v_and_b32_e32 v75, 32, v75
	v_lshl_add_u64 v[76:77], s[70:71], 0, v[76:77]
	v_bitop3_b32 v74, v80, v74, v75 bitop3:0xde
	v_mov_b32_e32 v75, v137
	v_lshl_add_u64 v[76:77], v[76:77], 0, v[78:79]
	v_lshl_add_u64 v[74:75], v[76:77], 0, v[74:75]
	global_store_dwordx4 v[74:75], v[66:69], off sc1
	ds_read2_b32 v[66:67], v155 offset0:48 offset1:113
	ds_read2_b32 v[68:69], v155 offset0:178 offset1:243
	s_waitcnt lgkmcnt(1)
	v_cvt_pk_bf16_f32 v66, v66, v67
	s_waitcnt lgkmcnt(0)
	v_cvt_pk_bf16_f32 v67, v68, v69
	ds_read2_b32 v[68:69], v172 offset0:52 offset1:117
	ds_read2_b32 v[74:75], v172 offset0:182 offset1:247
	s_waitcnt lgkmcnt(1)
	v_cvt_pk_bf16_f32 v68, v68, v69
	s_waitcnt lgkmcnt(0)
	v_cvt_pk_bf16_f32 v69, v74, v75
	v_add_u32_e32 v74, s15, v161
	s_mov_b64 s[94:95], -1
	s_and_b64 vcc, exec, s[0:1]
	s_cbranch_vccnz .LBB0_157
	v_and_b32_e32 v75, 0x7f, v74
	s_mov_b64 s[94:95], 0

.LBB0_159:
	v_ashrrev_i32_e32 v76, 8, v74
	v_lshlrev_b32_e32 v74, 7, v74
	v_mad_i64_i32 v[76:77], s[26:27], s2, v76, v[70:71]
	v_and_b32_e32 v78, 0x4000, v74
	v_lshrrev_b32_e32 v74, 3, v75
	v_lshlrev_b64 v[76:77], 15, v[76:77]
	v_and_or_b32 v74, v74, s12, v72
	v_lshlrev_b32_e32 v80, 6, v75
	v_lshlrev_b32_e32 v75, 2, v75
	v_mov_b32_e32 v79, v137
	v_and_or_b32 v80, v80, s13, v73
	v_lshlrev_b32_e32 v74, 10, v74
	v_and_b32_e32 v75, 32, v75
	v_lshl_add_u64 v[76:77], s[70:71], 0, v[76:77]
	v_bitop3_b32 v74, v80, v74, v75 bitop3:0xde
	v_mov_b32_e32 v75, v137
	v_lshl_add_u64 v[76:77], v[76:77], 0, v[78:79]
	v_lshl_add_u64 v[74:75], v[76:77], 0, v[74:75]
	global_store_dwordx4 v[74:75], v[66:69], off sc1
	ds_read2_b32 v[66:67], v155 offset0:56 offset1:121
	ds_read2_b32 v[68:69], v155 offset0:186 offset1:251
	s_waitcnt lgkmcnt(1)
	v_cvt_pk_bf16_f32 v66, v66, v67
	s_waitcnt lgkmcnt(0)
	v_cvt_pk_bf16_f32 v67, v68, v69
	ds_read2_b32 v[68:69], v172 offset0:60 offset1:125
	ds_read2_b32 v[74:75], v172 offset0:190 offset1:255
	s_waitcnt lgkmcnt(1)
	v_cvt_pk_bf16_f32 v68, v68, v69
	s_waitcnt lgkmcnt(0)
	v_cvt_pk_bf16_f32 v69, v74, v75
	v_add_u32_e32 v74, s15, v162
	s_mov_b64 s[94:95], -1
	s_and_b64 vcc, exec, s[0:1]
	s_cbranch_vccnz .LBB0_161
	v_and_b32_e32 v75, 0x7f, v74
	s_mov_b64 s[94:95], 0

.LBB0_163:
	v_ashrrev_i32_e32 v76, 8, v74
	v_lshlrev_b32_e32 v74, 7, v74
	v_mad_i64_i32 v[70:71], s[0:1], s2, v76, v[70:71]
	v_and_b32_e32 v76, 0x4000, v74
	v_lshrrev_b32_e32 v74, 3, v75
	v_and_or_b32 v72, v74, s12, v72
	v_lshlrev_b32_e32 v74, 6, v75
	v_lshlrev_b64 v[70:71], 15, v[70:71]
	v_and_or_b32 v73, v74, s13, v73
	v_lshlrev_b32_e32 v74, 2, v75
	v_mov_b32_e32 v77, v137
	v_lshlrev_b32_e32 v72, 10, v72
	v_and_b32_e32 v74, 32, v74
	v_lshl_add_u64 v[70:71], s[70:71], 0, v[70:71]
	v_bitop3_b32 v72, v73, v72, v74 bitop3:0xde
	v_mov_b32_e32 v73, v137
	v_lshl_add_u64 v[70:71], v[70:71], 0, v[76:77]
	v_lshl_add_u64 v[70:71], v[70:71], 0, v[72:73]
	global_store_dwordx4 v[70:71], v[66:69], off sc1
	s_waitcnt lgkmcnt(0)
	s_mov_b64 s[0:1], 0

.LBB0_169:
	s_waitcnt lgkmcnt(7)
	v_mul_f32_e32 v80, 0x42800000, v80
	v_mul_f32_e32 v81, 0x42800000, v81
	s_waitcnt lgkmcnt(6)
	v_mul_f32_e32 v83, 0x42800000, v78
	v_med3_f32 v80, v80, s20, v171
	v_med3_f32 v81, v81, s20, v171
	v_mov_b32_e32 v78, v137
	v_cvt_pk_fp8_f32 v78, v80, v81
	s_waitcnt lgkmcnt(1)
	v_mul_f32_e32 v68, 0x42800000, v68
	v_mul_f32_e32 v69, 0x42800000, v69
	v_mul_f32_e32 v79, 0x42800000, v79
	v_med3_f32 v68, v68, s20, v171
	v_med3_f32 v69, v69, s20, v171
	v_mov_b32_e32 v81, v137
	v_med3_f32 v80, v83, s20, v171
	v_med3_f32 v79, v79, s20, v171
	v_mul_f32_e32 v76, 0x42800000, v76
	v_mul_f32_e32 v77, 0x42800000, v77
	v_cvt_pk_fp8_f32 v81, v68, v69
	v_cvt_pk_fp8_f32 v78, v80, v79 op_sel:[0,0,1]
	v_med3_f32 v76, v76, s20, v171
	v_med3_f32 v77, v77, s20, v171
	v_mov_b32_e32 v79, v137
	v_mul_f32_e32 v72, 0x42800000, v72
	v_mul_f32_e32 v73, 0x42800000, v73
	v_cvt_pk_fp8_f32 v79, v76, v77
	v_med3_f32 v72, v72, s20, v171
	v_med3_f32 v73, v73, s20, v171
	v_mov_b32_e32 v80, v137
	s_waitcnt lgkmcnt(0)
	v_mul_f32_e32 v66, 0x42800000, v66
	v_mul_f32_e32 v67, 0x42800000, v67
	s_ashr_i32 s0, s4, 31
	v_cvt_pk_fp8_f32 v80, v72, v73
	v_med3_f32 v66, v66, s20, v171
	v_med3_f32 v67, v67, s20, v171
	v_add_u32_e32 v72, s35, v169
	s_lshr_b32 s0, s0, 25
	v_mul_f32_e32 v74, 0x42800000, v74
	v_mul_f32_e32 v75, 0x42800000, v75
	v_cvt_pk_fp8_f32 v81, v66, v67 op_sel:[0,0,1]
	s_add_i32 s0, s4, s0
	v_ashrrev_i32_e32 v66, 7, v72
	v_med3_f32 v74, v74, s20, v171
	v_med3_f32 v75, v75, s20, v171
	v_mul_f32_e32 v70, 0x42800000, v70
	v_mul_f32_e32 v71, 0x42800000, v71
	s_ashr_i32 s2, s0, 7
	v_ashrrev_i32_e32 v68, 8, v176
	v_ashrrev_i32_e32 v67, 31, v66
	v_cvt_pk_fp8_f32 v79, v74, v75 op_sel:[0,0,1]
	v_med3_f32 v70, v70, s20, v171
	v_med3_f32 v71, v71, s20, v171
	v_mad_i64_i32 v[68:69], s[0:1], s2, v68, v[66:67]
	v_lshrrev_b32_e32 v73, 3, v82
	v_bfe_u32 v84, v72, 6, 1
	v_lshlrev_b32_e32 v74, 6, v82
	v_and_b32_e32 v85, 62, v72
	v_cvt_pk_fp8_f32 v80, v70, v71 op_sel:[0,0,1]
	v_lshlrev_b64 v[68:69], 15, v[68:69]
	v_lshlrev_b32_e32 v70, 7, v176
	v_and_or_b32 v73, v73, s12, v84
	v_and_or_b32 v72, v74, s13, v85
	v_lshlrev_b32_e32 v74, 2, v82
	v_and_b32_e32 v70, 0x4000, v70
	v_mov_b32_e32 v71, v137
	v_lshlrev_b32_e32 v73, 10, v73
	v_and_b32_e32 v74, 32, v74
	v_lshl_add_u64 v[68:69], s[70:71], 0, v[68:69]
	v_bitop3_b32 v72, v72, v73, v74 bitop3:0xde
	v_mov_b32_e32 v73, v137
	v_lshl_add_u64 v[68:69], v[68:69], 0, v[70:71]
	v_lshl_add_u64 v[68:69], v[68:69], 0, v[72:73]
	global_store_dwordx4 v[68:69], v[78:81], off sc1
	ds_read2_b32 v[82:83], v164 offset0:16 offset1:81
	ds_read2_b32 v[80:81], v164 offset0:146 offset1:211
	ds_read2_b32 v[78:79], v175 offset0:20 offset1:85
	ds_read2_b32 v[76:77], v175 offset0:150 offset1:215
	ds_read2_b32 v[74:75], v174 offset0:24 offset1:89
	ds_read2_b32 v[72:73], v174 offset0:154 offset1:219
	ds_read2_b32 v[70:71], v173 offset0:28 offset1:93
	ds_read2_b32 v[68:69], v173 offset0:158 offset1:223
	v_cndmask_b32_e64 v87, 0, 1, s[90:91]
	v_add_u32_e32 v86, s15, v165
	v_cmp_ne_u32_e64 s[0:1], 1, v87
	s_andn2_b64 vcc, exec, s[90:91]
	s_mov_b64 s[90:91], -1
	s_cbranch_vccnz .LBB0_171
	v_and_b32_e32 v87, 0x7f, v86
	s_mov_b64 s[90:91], 0

.LBB0_173:
	s_waitcnt lgkmcnt(7)
	v_mul_f32_e32 v82, 0x42800000, v82
	v_mul_f32_e32 v83, 0x42800000, v83
	s_waitcnt lgkmcnt(6)
	v_mul_f32_e32 v88, 0x42800000, v80
	v_med3_f32 v82, v82, s20, v171
	v_med3_f32 v83, v83, s20, v171
	v_mov_b32_e32 v80, v137
	v_cvt_pk_fp8_f32 v80, v82, v83
	v_mul_f32_e32 v81, 0x42800000, v81
	s_waitcnt lgkmcnt(1)
	v_mul_f32_e32 v70, 0x42800000, v70
	v_mul_f32_e32 v71, 0x42800000, v71
	v_med3_f32 v82, v88, s20, v171
	v_med3_f32 v81, v81, s20, v171
	v_mul_f32_e32 v74, 0x42800000, v74
	v_mul_f32_e32 v75, 0x42800000, v75
	v_med3_f32 v70, v70, s20, v171
	v_med3_f32 v71, v71, s20, v171
	v_mov_b32_e32 v83, v137
	v_cvt_pk_fp8_f32 v80, v82, v81 op_sel:[0,0,1]
	v_mul_f32_e32 v78, 0x42800000, v78
	v_mul_f32_e32 v79, 0x42800000, v79
	v_med3_f32 v74, v74, s20, v171
	v_med3_f32 v75, v75, s20, v171
	v_mov_b32_e32 v82, v137
	v_cvt_pk_fp8_f32 v83, v70, v71
	v_med3_f32 v78, v78, s20, v171
	v_med3_f32 v79, v79, s20, v171
	v_mov_b32_e32 v81, v137
	v_cvt_pk_fp8_f32 v82, v74, v75
	v_cvt_pk_fp8_f32 v81, v78, v79
	s_waitcnt lgkmcnt(0)
	v_mul_f32_e32 v68, 0x42800000, v68
	v_mul_f32_e32 v69, 0x42800000, v69
	v_mul_f32_e32 v72, 0x42800000, v72
	v_mul_f32_e32 v73, 0x42800000, v73
	v_med3_f32 v68, v68, s20, v171
	v_med3_f32 v69, v69, s20, v171
	v_mul_f32_e32 v76, 0x42800000, v76
	v_mul_f32_e32 v77, 0x42800000, v77
	v_med3_f32 v72, v72, s20, v171
	v_med3_f32 v73, v73, s20, v171
	v_cvt_pk_fp8_f32 v83, v68, v69 op_sel:[0,0,1]
	v_ashrrev_i32_e32 v68, 8, v86
	v_med3_f32 v76, v76, s20, v171
	v_med3_f32 v77, v77, s20, v171
	v_cvt_pk_fp8_f32 v82, v72, v73 op_sel:[0,0,1]
	v_mad_i64_i32 v[68:69], s[26:27], s2, v68, v[66:67]
	v_lshrrev_b32_e32 v72, 3, v87
	v_cvt_pk_fp8_f32 v81, v76, v77 op_sel:[0,0,1]
	v_lshlrev_b64 v[68:69], 15, v[68:69]
	v_lshlrev_b32_e32 v70, 7, v86
	v_and_or_b32 v72, v72, s12, v84
	v_lshlrev_b32_e32 v73, 6, v87
	v_lshlrev_b32_e32 v74, 2, v87
	v_and_b32_e32 v70, 0x4000, v70
	v_mov_b32_e32 v71, v137
	v_and_or_b32 v73, v73, s13, v85
	v_lshlrev_b32_e32 v72, 10, v72
	v_and_b32_e32 v74, 32, v74
	v_lshl_add_u64 v[68:69], s[70:71], 0, v[68:69]
	v_bitop3_b32 v72, v73, v72, v74 bitop3:0xde
	v_mov_b32_e32 v73, v137
	v_lshl_add_u64 v[68:69], v[68:69], 0, v[70:71]
	v_lshl_add_u64 v[68:69], v[68:69], 0, v[72:73]
	global_store_dwordx4 v[68:69], v[80:83], off sc1
	ds_read2_b32 v[82:83], v164 offset0:32 offset1:97
	ds_read2_b32 v[80:81], v164 offset0:162 offset1:227
	ds_read2_b32 v[78:79], v175 offset0:36 offset1:101
	ds_read2_b32 v[76:77], v175 offset0:166 offset1:231
	ds_read2_b32 v[74:75], v174 offset0:40 offset1:105
	ds_read2_b32 v[72:73], v174 offset0:170 offset1:235
	ds_read2_b32 v[70:71], v173 offset0:44 offset1:109
	ds_read2_b32 v[68:69], v173 offset0:174 offset1:239
	v_add_u32_e32 v86, s15, v166
	s_mov_b64 s[90:91], -1
	s_and_b64 vcc, exec, s[0:1]
	s_cbranch_vccnz .LBB0_175
	v_and_b32_e32 v87, 0x7f, v86
	s_mov_b64 s[90:91], 0

.LBB0_177:
	s_waitcnt lgkmcnt(7)
	v_mul_f32_e32 v82, 0x42800000, v82
	v_mul_f32_e32 v83, 0x42800000, v83
	s_waitcnt lgkmcnt(6)
	v_mul_f32_e32 v88, 0x42800000, v80
	v_med3_f32 v82, v82, s20, v171
	v_med3_f32 v83, v83, s20, v171
	v_mov_b32_e32 v80, v137
	v_cvt_pk_fp8_f32 v80, v82, v83
	v_mul_f32_e32 v81, 0x42800000, v81
	s_waitcnt lgkmcnt(1)
	v_mul_f32_e32 v70, 0x42800000, v70
	v_mul_f32_e32 v71, 0x42800000, v71
	v_med3_f32 v82, v88, s20, v171
	v_med3_f32 v81, v81, s20, v171
	v_mul_f32_e32 v74, 0x42800000, v74
	v_mul_f32_e32 v75, 0x42800000, v75
	v_med3_f32 v70, v70, s20, v171
	v_med3_f32 v71, v71, s20, v171
	v_mov_b32_e32 v83, v137
	v_cvt_pk_fp8_f32 v80, v82, v81 op_sel:[0,0,1]
	v_mul_f32_e32 v78, 0x42800000, v78
	v_mul_f32_e32 v79, 0x42800000, v79
	v_med3_f32 v74, v74, s20, v171
	v_med3_f32 v75, v75, s20, v171
	v_mov_b32_e32 v82, v137
	v_cvt_pk_fp8_f32 v83, v70, v71
	v_med3_f32 v78, v78, s20, v171
	v_med3_f32 v79, v79, s20, v171
	v_mov_b32_e32 v81, v137
	v_cvt_pk_fp8_f32 v82, v74, v75
	v_cvt_pk_fp8_f32 v81, v78, v79
	s_waitcnt lgkmcnt(0)
	v_mul_f32_e32 v68, 0x42800000, v68
	v_mul_f32_e32 v69, 0x42800000, v69
	v_mul_f32_e32 v72, 0x42800000, v72
	v_mul_f32_e32 v73, 0x42800000, v73
	v_med3_f32 v68, v68, s20, v171
	v_med3_f32 v69, v69, s20, v171
	v_mul_f32_e32 v76, 0x42800000, v76
	v_mul_f32_e32 v77, 0x42800000, v77
	v_med3_f32 v72, v72, s20, v171
	v_med3_f32 v73, v73, s20, v171
	v_cvt_pk_fp8_f32 v83, v68, v69 op_sel:[0,0,1]
	v_ashrrev_i32_e32 v68, 8, v86
	v_med3_f32 v76, v76, s20, v171
	v_med3_f32 v77, v77, s20, v171
	v_cvt_pk_fp8_f32 v82, v72, v73 op_sel:[0,0,1]
	v_mad_i64_i32 v[68:69], s[26:27], s2, v68, v[66:67]
	v_lshrrev_b32_e32 v72, 3, v87
	v_cvt_pk_fp8_f32 v81, v76, v77 op_sel:[0,0,1]
	v_lshlrev_b64 v[68:69], 15, v[68:69]
	v_lshlrev_b32_e32 v70, 7, v86
	v_and_or_b32 v72, v72, s12, v84
	v_lshlrev_b32_e32 v73, 6, v87
	v_lshlrev_b32_e32 v74, 2, v87
	v_and_b32_e32 v70, 0x4000, v70
	v_mov_b32_e32 v71, v137
	v_and_or_b32 v73, v73, s13, v85
	v_lshlrev_b32_e32 v72, 10, v72
	v_and_b32_e32 v74, 32, v74
	v_lshl_add_u64 v[68:69], s[70:71], 0, v[68:69]
	v_bitop3_b32 v72, v73, v72, v74 bitop3:0xde
	v_mov_b32_e32 v73, v137
	v_lshl_add_u64 v[68:69], v[68:69], 0, v[70:71]
	v_lshl_add_u64 v[68:69], v[68:69], 0, v[72:73]
	global_store_dwordx4 v[68:69], v[80:83], off sc1
	ds_read2_b32 v[80:81], v164 offset0:48 offset1:113
	ds_read2_b32 v[82:83], v164 offset0:178 offset1:243
	ds_read2_b32 v[76:77], v175 offset0:52 offset1:117
	ds_read2_b32 v[78:79], v175 offset0:182 offset1:247
	ds_read2_b32 v[72:73], v174 offset0:56 offset1:121
	ds_read2_b32 v[74:75], v174 offset0:186 offset1:251
	ds_read2_b32 v[68:69], v173 offset0:60 offset1:125
	ds_read2_b32 v[70:71], v173 offset0:190 offset1:255
	v_add_u32_e32 v86, s15, v167
	s_mov_b64 s[90:91], -1
	s_and_b64 vcc, exec, s[0:1]
	s_cbranch_vccnz .LBB0_179
	v_and_b32_e32 v87, 0x7f, v86
	s_mov_b64 s[90:91], 0

.LBB0_264:
	v_lshl_add_u32 v144, s74, 8, v166
	s_cmp_gt_i32 s2, 7
	v_ashrrev_i32_e32 v145, 31, v144
	s_mov_b64 s[74:75], -1
	v_or_b32_e32 v150, 16, v144
	v_or_b32_e32 v148, 32, v144
	v_or_b32_e32 v146, 48, v144
	s_cbranch_scc0 .LBB0_267
	v_lshl_add_u32 v136, s2, 8, v169
	v_lshlrev_b64 v[152:153], 13, v[144:145]
	v_lshl_add_u64 v[152:153], s[6:7], 0, v[152:153]
	v_lshlrev_b64 v[178:179], 1, v[136:137]
	v_lshl_add_u64 v[152:153], v[152:153], 0, v[178:179]
	v_cvt_pk_bf16_f32 v174, v122, v123
	v_cvt_pk_bf16_f32 v175, v124, v125
	v_cvt_pk_bf16_f32 v176, v118, v119
	v_cvt_pk_bf16_f32 v177, v120, v121
	global_store_dwordx4 v[152:153], v[174:177], off sc1
	v_ashrrev_i32_e32 v151, 31, v150
	v_ashrrev_i32_e32 v149, 31, v148
	v_cvt_pk_bf16_f32 v174, v126, v127
	v_cvt_pk_bf16_f32 v175, v128, v129
	v_cvt_pk_bf16_f32 v176, v114, v115
	v_cvt_pk_bf16_f32 v177, v116, v117
	global_store_dwordx4 v[152:153], v[174:177], off offset:256 sc1
	v_ashrrev_i32_e32 v147, 31, v146
	s_mov_b32 s8, 0x100000
	v_lshlrev_b64 v[174:175], 13, v[150:151]
	v_lshl_add_u64 v[174:175], s[6:7], 0, v[174:175]
	v_lshl_add_u64 v[180:181], v[174:175], 0, v[178:179]
	v_cvt_pk_bf16_f32 v174, v106, v107
	v_cvt_pk_bf16_f32 v175, v108, v109
	v_cvt_pk_bf16_f32 v176, v102, v103
	v_cvt_pk_bf16_f32 v177, v104, v105
	global_store_dwordx4 v[180:181], v[174:177], off sc1
	s_mov_b64 s[26:27], 0x100000
	s_nop 0
	v_cvt_pk_bf16_f32 v174, v110, v111
	v_cvt_pk_bf16_f32 v175, v112, v113
	v_cvt_pk_bf16_f32 v176, v98, v99
	v_cvt_pk_bf16_f32 v177, v100, v101
	global_store_dwordx4 v[180:181], v[174:177], off offset:256 sc1
	s_nop 1
	v_lshlrev_b64 v[174:175], 13, v[148:149]
	v_lshl_add_u64 v[174:175], s[6:7], 0, v[174:175]
	v_lshl_add_u64 v[180:181], v[174:175], 0, v[178:179]
	v_cvt_pk_bf16_f32 v174, v90, v91
	v_cvt_pk_bf16_f32 v175, v92, v93
	v_cvt_pk_bf16_f32 v176, v86, v87
	v_cvt_pk_bf16_f32 v177, v88, v89
	global_store_dwordx4 v[180:181], v[174:177], off sc1
	s_nop 1
	v_cvt_pk_bf16_f32 v174, v94, v95
	v_cvt_pk_bf16_f32 v175, v96, v97
	v_cvt_pk_bf16_f32 v176, v82, v83
	v_cvt_pk_bf16_f32 v177, v84, v85
	global_store_dwordx4 v[180:181], v[174:177], off offset:256 sc1
	v_add_co_u32_e32 v180, vcc, s8, v152
	s_nop 0
	v_lshlrev_b64 v[174:175], 13, v[146:147]
	v_lshl_add_u64 v[174:175], s[6:7], 0, v[174:175]
	v_lshl_add_u64 v[178:179], v[174:175], 0, v[178:179]
	v_cvt_pk_bf16_f32 v174, v74, v75
	v_cvt_pk_bf16_f32 v175, v76, v77
	v_cvt_pk_bf16_f32 v176, v70, v71
	v_cvt_pk_bf16_f32 v177, v72, v73
	global_store_dwordx4 v[178:179], v[174:177], off sc1
	v_addc_co_u32_e32 v181, vcc, 0, v153, vcc
	s_nop 0
	v_cvt_pk_bf16_f32 v174, v78, v79
	v_cvt_pk_bf16_f32 v175, v80, v81
	v_cvt_pk_bf16_f32 v176, v66, v67
	v_cvt_pk_bf16_f32 v177, v68, v69
	global_store_dwordx4 v[178:179], v[174:177], off offset:256 sc1
	s_mov_b32 s8, 0x120000
	v_lshl_add_u64 v[178:179], v[152:153], 0, s[26:27]
	v_cvt_pk_bf16_f32 v174, v58, v59
	v_cvt_pk_bf16_f32 v175, v60, v61
	v_cvt_pk_bf16_f32 v176, v54, v55
	v_cvt_pk_bf16_f32 v177, v56, v57
	global_store_dwordx4 v[180:181], v[174:177], off sc1
	v_add_co_u32_e32 v180, vcc, s8, v152
	s_nop 0
	v_cvt_pk_bf16_f32 v174, v62, v63
	v_cvt_pk_bf16_f32 v175, v64, v65
	v_cvt_pk_bf16_f32 v176, v50, v51
	v_cvt_pk_bf16_f32 v177, v52, v53
	global_store_dwordx4 v[178:179], v[174:177], off offset:256 sc1
	s_mov_b64 s[26:27], 0x120000
	v_addc_co_u32_e32 v181, vcc, 0, v153, vcc
	v_cvt_pk_bf16_f32 v174, v42, v43
	v_cvt_pk_bf16_f32 v175, v44, v45
	v_cvt_pk_bf16_f32 v176, v38, v39
	v_cvt_pk_bf16_f32 v177, v40, v41
	s_mov_b32 s8, 0x140000
	v_lshl_add_u64 v[178:179], v[152:153], 0, s[26:27]
	global_store_dwordx4 v[180:181], v[174:177], off sc1
	s_mov_b64 s[26:27], 0x140000
	v_add_co_u32_e32 v180, vcc, s8, v152
	v_cvt_pk_bf16_f32 v174, v46, v47
	v_cvt_pk_bf16_f32 v175, v48, v49
	v_cvt_pk_bf16_f32 v176, v34, v35
	v_cvt_pk_bf16_f32 v177, v36, v37
	global_store_dwordx4 v[178:179], v[174:177], off offset:256 sc1
	v_lshl_add_u64 v[178:179], v[152:153], 0, s[26:27]
	v_addc_co_u32_e32 v181, vcc, 0, v153, vcc
	v_cvt_pk_bf16_f32 v174, v26, v27
	v_cvt_pk_bf16_f32 v175, v28, v29
	v_cvt_pk_bf16_f32 v176, v22, v23
	v_cvt_pk_bf16_f32 v177, v24, v25
	s_mov_b64 s[26:27], 0x160000
	s_mov_b32 s8, 0x160000
	global_store_dwordx4 v[180:181], v[174:177], off sc1
	s_nop 1
	v_cvt_pk_bf16_f32 v174, v30, v31
	v_cvt_pk_bf16_f32 v175, v32, v33
	v_cvt_pk_bf16_f32 v176, v18, v19
	v_cvt_pk_bf16_f32 v177, v20, v21
	global_store_dwordx4 v[178:179], v[174:177], off offset:256 sc1
	v_lshl_add_u64 v[178:179], v[152:153], 0, s[26:27]
	v_add_co_u32_e32 v152, vcc, s8, v152
	v_cvt_pk_bf16_f32 v174, v10, v11
	v_cvt_pk_bf16_f32 v175, v12, v13
	v_cvt_pk_bf16_f32 v176, v6, v7
	v_cvt_pk_bf16_f32 v177, v8, v9
	s_nop 1
	v_addc_co_u32_e32 v153, vcc, 0, v153, vcc
	global_store_dwordx4 v[152:153], v[174:177], off sc1
	s_nop 1
	v_cvt_pk_bf16_f32 v174, v14, v15
	v_cvt_pk_bf16_f32 v175, v16, v17
	v_cvt_pk_bf16_f32 v176, v2, v3
	v_cvt_pk_bf16_f32 v177, v4, v5
	global_store_dwordx4 v[178:179], v[174:177], off offset:256 sc1
	s_cbranch_execz .LBB0_268

.LBB0_268:
	v_pk_mul_f32 v[126:127], v[126:127], s[54:55] op_sel_hi:[1,0]
	v_pk_mul_f32 v[128:129], v[128:129], s[54:55] op_sel_hi:[1,0]
	v_pk_mul_f32 v[114:115], v[114:115], s[54:55] op_sel_hi:[1,0]
	v_exp_f32_e32 v126, v126
	v_exp_f32_e32 v127, v127
	v_exp_f32_e32 v128, v128
	v_exp_f32_e32 v129, v129
	v_exp_f32_e32 v114, v114
	v_exp_f32_e32 v115, v115
	v_pk_mul_f32 v[116:117], v[116:117], s[54:55] op_sel_hi:[1,0]
	v_pk_mul_f32 v[110:111], v[110:111], s[54:55] op_sel_hi:[1,0]
	v_exp_f32_e32 v116, v116
	v_exp_f32_e32 v117, v117
	v_pk_mul_f32 v[112:113], v[112:113], s[54:55] op_sel_hi:[1,0]
	v_pk_mul_f32 v[98:99], v[98:99], s[54:55] op_sel_hi:[1,0]
	v_exp_f32_e32 v110, v110
	v_exp_f32_e32 v111, v111
	v_exp_f32_e32 v112, v112
	v_exp_f32_e32 v113, v113
	v_exp_f32_e32 v98, v98
	v_exp_f32_e32 v99, v99
	v_pk_mul_f32 v[100:101], v[100:101], s[54:55] op_sel_hi:[1,0]
	v_pk_add_f32 v[126:127], v[126:127], 1.0 op_sel_hi:[1,0]
	v_pk_add_f32 v[128:129], v[128:129], 1.0 op_sel_hi:[1,0]
	v_pk_add_f32 v[114:115], v[114:115], 1.0 op_sel_hi:[1,0]
	v_exp_f32_e32 v100, v100
	v_exp_f32_e32 v101, v101
	v_rcp_f32_e32 v126, v126
	v_rcp_f32_e32 v127, v127
	v_rcp_f32_e32 v128, v128
	v_rcp_f32_e32 v129, v129
	v_rcp_f32_e32 v114, v114
	v_rcp_f32_e32 v115, v115
	v_pk_add_f32 v[116:117], v[116:117], 1.0 op_sel_hi:[1,0]
	v_pk_mul_f32 v[94:95], v[94:95], s[54:55] op_sel_hi:[1,0]
	v_pk_mul_f32 v[96:97], v[96:97], s[54:55] op_sel_hi:[1,0]
	v_pk_mul_f32 v[82:83], v[82:83], s[54:55] op_sel_hi:[1,0]
	v_lshl_or_b32 v152, s2, 7, v168
	v_rcp_f32_e32 v116, v116
	v_rcp_f32_e32 v117, v117
	v_exp_f32_e32 v94, v94
	v_exp_f32_e32 v95, v95
	v_exp_f32_e32 v96, v96
	v_exp_f32_e32 v97, v97
	v_exp_f32_e32 v82, v82
	v_exp_f32_e32 v83, v83
	v_pk_mul_f32 v[84:85], v[84:85], s[54:55] op_sel_hi:[1,0]
	v_ashrrev_i32_e32 v153, 31, v152
	v_lshlrev_b64 v[144:145], 11, v[144:145]
	v_pk_add_f32 v[110:111], v[110:111], 1.0 op_sel_hi:[1,0]
	v_pk_add_f32 v[112:113], v[112:113], 1.0 op_sel_hi:[1,0]
	v_pk_add_f32 v[98:99], v[98:99], 1.0 op_sel_hi:[1,0]
	v_exp_f32_e32 v84, v84
	v_exp_f32_e32 v85, v85
	v_lshl_add_u64 v[144:145], s[18:19], 0, v[144:145]
	v_lshlrev_b64 v[152:153], 1, v[152:153]
	v_rcp_f32_e32 v110, v110
	v_rcp_f32_e32 v111, v111
	v_rcp_f32_e32 v112, v112
	v_rcp_f32_e32 v113, v113
	v_rcp_f32_e32 v98, v98
	v_rcp_f32_e32 v99, v99
	v_pk_add_f32 v[100:101], v[100:101], 1.0 op_sel_hi:[1,0]
	v_pk_mul_f32 v[50:51], v[50:51], s[54:55] op_sel_hi:[1,0]
	v_lshl_add_u64 v[144:145], v[144:145], 0, v[152:153]
	v_pk_mul_f32 v[122:123], v[122:123], v[126:127]
	v_pk_mul_f32 v[124:125], v[124:125], v[128:129]
	v_pk_mul_f32 v[118:119], v[118:119], v[114:115]
	v_cvt_pk_bf16_f32 v114, v122, v123
	v_cvt_pk_bf16_f32 v115, v124, v125
	v_ashrrev_i32_e32 v151, 31, v150
	v_rcp_f32_e32 v100, v100
	v_rcp_f32_e32 v101, v101
	v_pk_mul_f32 v[78:79], v[78:79], s[54:55] op_sel_hi:[1,0]
	v_pk_mul_f32 v[80:81], v[80:81], s[54:55] op_sel_hi:[1,0]
	v_pk_mul_f32 v[66:67], v[66:67], s[54:55] op_sel_hi:[1,0]
	v_pk_mul_f32 v[68:69], v[68:69], s[54:55] op_sel_hi:[1,0]
	v_pk_mul_f32 v[62:63], v[62:63], s[54:55] op_sel_hi:[1,0]
	v_pk_mul_f32 v[64:65], v[64:65], s[54:55] op_sel_hi:[1,0]
	v_exp_f32_e32 v50, v50
	v_exp_f32_e32 v51, v51
	v_pk_mul_f32 v[52:53], v[52:53], s[54:55] op_sel_hi:[1,0]
	v_pk_mul_f32 v[120:121], v[120:121], v[116:117]
	v_cvt_pk_bf16_f32 v116, v118, v119
	v_pk_add_f32 v[94:95], v[94:95], 1.0 op_sel_hi:[1,0]
	v_cvt_pk_bf16_f32 v117, v120, v121
	global_store_dwordx4 v[144:145], v[114:117], off sc1
	v_pk_add_f32 v[96:97], v[96:97], 1.0 op_sel_hi:[1,0]
	v_pk_add_f32 v[82:83], v[82:83], 1.0 op_sel_hi:[1,0]
	v_lshlrev_b64 v[114:115], 11, v[150:151]
	v_exp_f32_e32 v78, v78
	v_exp_f32_e32 v79, v79
	v_exp_f32_e32 v80, v80
	v_exp_f32_e32 v81, v81
	v_exp_f32_e32 v66, v66
	v_exp_f32_e32 v67, v67
	v_exp_f32_e32 v68, v68
	v_exp_f32_e32 v69, v69
	v_exp_f32_e32 v62, v62
	v_exp_f32_e32 v63, v63
	v_exp_f32_e32 v64, v64
	v_exp_f32_e32 v65, v65
	v_exp_f32_e32 v52, v52
	v_exp_f32_e32 v53, v53
	v_pk_mul_f32 v[34:35], v[34:35], s[54:55] op_sel_hi:[1,0]
	v_lshl_add_u64 v[114:115], s[18:19], 0, v[114:115]
	v_rcp_f32_e32 v94, v94
	v_rcp_f32_e32 v95, v95
	v_rcp_f32_e32 v96, v96
	v_rcp_f32_e32 v97, v97
	v_rcp_f32_e32 v82, v82
	v_rcp_f32_e32 v83, v83
	v_pk_add_f32 v[84:85], v[84:85], 1.0 op_sel_hi:[1,0]
	v_pk_mul_f32 v[46:47], v[46:47], s[54:55] op_sel_hi:[1,0]
	v_pk_mul_f32 v[48:49], v[48:49], s[54:55] op_sel_hi:[1,0]
	v_exp_f32_e32 v34, v34
	v_exp_f32_e32 v35, v35
	v_pk_mul_f32 v[36:37], v[36:37], s[54:55] op_sel_hi:[1,0]
	v_lshl_add_u64 v[114:115], v[114:115], 0, v[152:153]
	v_pk_mul_f32 v[106:107], v[106:107], v[110:111]
	v_pk_mul_f32 v[108:109], v[108:109], v[112:113]
	v_pk_mul_f32 v[102:103], v[102:103], v[98:99]
	v_cvt_pk_bf16_f32 v98, v106, v107
	v_cvt_pk_bf16_f32 v99, v108, v109
	v_ashrrev_i32_e32 v149, 31, v148
	v_rcp_f32_e32 v84, v84
	v_rcp_f32_e32 v85, v85
	v_exp_f32_e32 v46, v46
	v_exp_f32_e32 v47, v47
	v_exp_f32_e32 v48, v48
	v_exp_f32_e32 v49, v49
	v_exp_f32_e32 v36, v36
	v_exp_f32_e32 v37, v37
	v_pk_mul_f32 v[18:19], v[18:19], s[54:55] op_sel_hi:[1,0]
	v_pk_mul_f32 v[104:105], v[104:105], v[100:101]
	v_cvt_pk_bf16_f32 v100, v102, v103
	v_pk_add_f32 v[50:51], v[50:51], 1.0 op_sel_hi:[1,0]
	v_cvt_pk_bf16_f32 v101, v104, v105
	global_store_dwordx4 v[114:115], v[98:101], off sc1
	v_pk_mul_f32 v[30:31], v[30:31], s[54:55] op_sel_hi:[1,0]
	v_pk_mul_f32 v[32:33], v[32:33], s[54:55] op_sel_hi:[1,0]
	v_lshlrev_b64 v[98:99], 11, v[148:149]
	v_exp_f32_e32 v18, v18
	v_exp_f32_e32 v19, v19
	v_pk_mul_f32 v[20:21], v[20:21], s[54:55] op_sel_hi:[1,0]
	v_lshl_add_u64 v[98:99], s[18:19], 0, v[98:99]
	v_pk_add_f32 v[78:79], v[78:79], 1.0 op_sel_hi:[1,0]
	v_pk_add_f32 v[80:81], v[80:81], 1.0 op_sel_hi:[1,0]
	v_pk_add_f32 v[66:67], v[66:67], 1.0 op_sel_hi:[1,0]
	v_pk_add_f32 v[68:69], v[68:69], 1.0 op_sel_hi:[1,0]
	v_pk_add_f32 v[62:63], v[62:63], 1.0 op_sel_hi:[1,0]
	v_pk_add_f32 v[64:65], v[64:65], 1.0 op_sel_hi:[1,0]
	v_rcp_f32_e32 v50, v50
	v_rcp_f32_e32 v51, v51
	v_pk_add_f32 v[52:53], v[52:53], 1.0 op_sel_hi:[1,0]
	v_exp_f32_e32 v30, v30
	v_exp_f32_e32 v31, v31
	v_exp_f32_e32 v32, v32
	v_exp_f32_e32 v33, v33
	v_exp_f32_e32 v20, v20
	v_exp_f32_e32 v21, v21
	v_pk_mul_f32 v[2:3], v[2:3], s[54:55] op_sel_hi:[1,0]
	v_lshl_add_u64 v[98:99], v[98:99], 0, v[152:153]
	v_pk_mul_f32 v[90:91], v[90:91], v[94:95]
	v_pk_mul_f32 v[92:93], v[92:93], v[96:97]
	v_pk_mul_f32 v[86:87], v[86:87], v[82:83]
	v_cvt_pk_bf16_f32 v82, v90, v91
	v_cvt_pk_bf16_f32 v83, v92, v93
	v_ashrrev_i32_e32 v147, 31, v146
	v_rcp_f32_e32 v78, v78
	v_rcp_f32_e32 v79, v79
	v_rcp_f32_e32 v80, v80
	v_rcp_f32_e32 v81, v81
	v_rcp_f32_e32 v66, v66
	v_rcp_f32_e32 v67, v67
	v_rcp_f32_e32 v68, v68
	v_rcp_f32_e32 v69, v69
	v_rcp_f32_e32 v62, v62
	v_rcp_f32_e32 v63, v63
	v_rcp_f32_e32 v64, v64
	v_rcp_f32_e32 v65, v65
	v_rcp_f32_e32 v52, v52
	v_rcp_f32_e32 v53, v53
	v_pk_add_f32 v[34:35], v[34:35], 1.0 op_sel_hi:[1,0]
	v_pk_mul_f32 v[14:15], v[14:15], s[54:55] op_sel_hi:[1,0]
	v_pk_mul_f32 v[16:17], v[16:17], s[54:55] op_sel_hi:[1,0]
	v_exp_f32_e32 v2, v2
	v_exp_f32_e32 v3, v3
	v_pk_mul_f32 v[4:5], v[4:5], s[54:55] op_sel_hi:[1,0]
	v_pk_mul_f32 v[88:89], v[88:89], v[84:85]
	v_cvt_pk_bf16_f32 v84, v86, v87
	v_pk_add_f32 v[46:47], v[46:47], 1.0 op_sel_hi:[1,0]
	v_cvt_pk_bf16_f32 v85, v88, v89
	global_store_dwordx4 v[98:99], v[82:85], off sc1
	v_pk_add_f32 v[48:49], v[48:49], 1.0 op_sel_hi:[1,0]
	v_rcp_f32_e32 v34, v34
	v_lshlrev_b64 v[82:83], 11, v[146:147]
	v_rcp_f32_e32 v35, v35
	v_pk_add_f32 v[36:37], v[36:37], 1.0 op_sel_hi:[1,0]
	v_exp_f32_e32 v14, v14
	v_exp_f32_e32 v15, v15
	v_exp_f32_e32 v16, v16
	v_exp_f32_e32 v17, v17
	v_exp_f32_e32 v4, v4
	v_exp_f32_e32 v5, v5
	v_lshl_add_u64 v[82:83], s[18:19], 0, v[82:83]
	v_rcp_f32_e32 v46, v46
	v_rcp_f32_e32 v47, v47
	v_rcp_f32_e32 v48, v48
	v_rcp_f32_e32 v49, v49
	v_rcp_f32_e32 v36, v36
	v_rcp_f32_e32 v37, v37
	v_pk_add_f32 v[18:19], v[18:19], 1.0 op_sel_hi:[1,0]
	v_lshl_add_u64 v[82:83], v[82:83], 0, v[152:153]
	v_pk_mul_f32 v[54:55], v[54:55], v[50:51]
	s_mov_b32 s2, 0x40000
	v_pk_add_f32 v[30:31], v[30:31], 1.0 op_sel_hi:[1,0]
	v_pk_add_f32 v[32:33], v[32:33], 1.0 op_sel_hi:[1,0]
	v_rcp_f32_e32 v18, v18
	v_rcp_f32_e32 v19, v19
	v_pk_add_f32 v[20:21], v[20:21], 1.0 op_sel_hi:[1,0]
	v_pk_mul_f32 v[74:75], v[74:75], v[78:79]
	v_pk_mul_f32 v[76:77], v[76:77], v[80:81]
	v_pk_mul_f32 v[70:71], v[70:71], v[66:67]
	v_pk_mul_f32 v[72:73], v[72:73], v[68:69]
	v_cvt_pk_bf16_f32 v66, v74, v75
	v_cvt_pk_bf16_f32 v67, v76, v77
	v_cvt_pk_bf16_f32 v68, v70, v71
	v_pk_mul_f32 v[58:59], v[58:59], v[62:63]
	v_cvt_pk_bf16_f32 v69, v72, v73
	global_store_dwordx4 v[82:83], v[66:69], off sc1
	v_pk_mul_f32 v[60:61], v[60:61], v[64:65]
	v_pk_mul_f32 v[56:57], v[56:57], v[52:53]
	v_cvt_pk_bf16_f32 v50, v58, v59
	v_cvt_pk_bf16_f32 v51, v60, v61
	v_cvt_pk_bf16_f32 v52, v54, v55
	v_add_co_u32_e32 v54, vcc, s2, v144
	v_rcp_f32_e32 v30, v30
	v_rcp_f32_e32 v31, v31
	v_rcp_f32_e32 v32, v32
	v_rcp_f32_e32 v33, v33
	v_rcp_f32_e32 v20, v20
	v_rcp_f32_e32 v21, v21
	v_pk_add_f32 v[2:3], v[2:3], 1.0 op_sel_hi:[1,0]
	v_addc_co_u32_e32 v55, vcc, 0, v145, vcc
	v_pk_mul_f32 v[38:39], v[38:39], v[34:35]
	s_mov_b32 s2, 0x48000
	v_pk_add_f32 v[14:15], v[14:15], 1.0 op_sel_hi:[1,0]
	v_pk_add_f32 v[16:17], v[16:17], 1.0 op_sel_hi:[1,0]
	v_rcp_f32_e32 v2, v2
	v_rcp_f32_e32 v3, v3
	v_pk_add_f32 v[4:5], v[4:5], 1.0 op_sel_hi:[1,0]
	v_cvt_pk_bf16_f32 v53, v56, v57
	global_store_dwordx4 v[54:55], v[50:53], off sc1
	v_pk_mul_f32 v[42:43], v[42:43], v[46:47]
	v_pk_mul_f32 v[44:45], v[44:45], v[48:49]
	v_pk_mul_f32 v[40:41], v[40:41], v[36:37]
	v_cvt_pk_bf16_f32 v34, v42, v43
	v_cvt_pk_bf16_f32 v35, v44, v45
	v_cvt_pk_bf16_f32 v36, v38, v39
	v_add_co_u32_e32 v38, vcc, s2, v144
	v_rcp_f32_e32 v14, v14
	v_rcp_f32_e32 v15, v15
	v_rcp_f32_e32 v16, v16
	v_rcp_f32_e32 v17, v17
	v_rcp_f32_e32 v4, v4
	v_rcp_f32_e32 v5, v5
	v_addc_co_u32_e32 v39, vcc, 0, v145, vcc
	v_pk_mul_f32 v[22:23], v[22:23], v[18:19]
	s_mov_b32 s2, 0x50000
	v_cvt_pk_bf16_f32 v37, v40, v41
	global_store_dwordx4 v[38:39], v[34:37], off sc1
	v_pk_mul_f32 v[26:27], v[26:27], v[30:31]
	v_pk_mul_f32 v[28:29], v[28:29], v[32:33]
	v_pk_mul_f32 v[24:25], v[24:25], v[20:21]
	v_cvt_pk_bf16_f32 v18, v26, v27
	v_cvt_pk_bf16_f32 v19, v28, v29
	v_cvt_pk_bf16_f32 v20, v22, v23
	v_add_co_u32_e32 v22, vcc, s2, v144
	v_pk_mul_f32 v[6:7], v[6:7], v[2:3]
	s_nop 0
	v_addc_co_u32_e32 v23, vcc, 0, v145, vcc
	v_cvt_pk_bf16_f32 v21, v24, v25
	global_store_dwordx4 v[22:23], v[18:21], off sc1
	v_pk_mul_f32 v[10:11], v[10:11], v[14:15]
	v_pk_mul_f32 v[12:13], v[12:13], v[16:17]
	v_pk_mul_f32 v[8:9], v[8:9], v[4:5]
	v_cvt_pk_bf16_f32 v2, v10, v11
	v_cvt_pk_bf16_f32 v3, v12, v13
	v_cvt_pk_bf16_f32 v4, v6, v7
	v_add_co_u32_e32 v6, vcc, 0x58000, v144
	v_cvt_pk_bf16_f32 v5, v8, v9
	s_nop 1
	v_addc_co_u32_e32 v7, vcc, 0, v145, vcc
	global_store_dwordx4 v[6:7], v[2:5], off sc1
	s_andn2_b64 vcc, exec, s[0:1]
	s_mov_b64 s[0:1], -1
	s_cbranch_vccnz .LBB0_253

.LBB0_288:
	v_lshl_add_u32 v8, s68, 8, v182
	v_lshl_or_b32 v2, s2, 8, v184
	v_ashrrev_i32_e32 v9, 31, v8
	v_ashrrev_i32_e32 v3, 31, v2
	v_lshlrev_b64 v[4:5], 13, v[8:9]
	v_lshl_add_u64 v[4:5], s[6:7], 0, v[4:5]
	v_lshlrev_b64 v[10:11], 1, v[2:3]
	s_nop 15
	s_nop 15
	v_lshl_add_u64 v[2:3], v[4:5], 0, v[10:11]
	v_cvt_pk_bf16_f32 v4, v158, v159
	v_cvt_pk_bf16_f32 v5, v160, v161
	v_cvt_pk_bf16_f32 v6, v154, v155
	v_cvt_pk_bf16_f32 v7, v156, v157
	global_store_dwordx4 v[2:3], v[4:7], off sc1
	s_mov_b32 s2, 0x100000
	s_mov_b64 s[26:27], 0x100000
	v_cvt_pk_bf16_f32 v4, v146, v147
	v_cvt_pk_bf16_f32 v5, v148, v149
	v_cvt_pk_bf16_f32 v6, v138, v139
	v_cvt_pk_bf16_f32 v7, v140, v141
	global_store_dwordx4 v[2:3], v[4:7], off offset:256 sc1
	v_readlane_b32 s96, v254, 60
	v_readlane_b32 s97, v254, 61
	v_or_b32_e32 v4, 16, v8
	v_ashrrev_i32_e32 v5, 31, v4
	v_lshlrev_b64 v[4:5], 13, v[4:5]
	v_lshl_add_u64 v[4:5], s[6:7], 0, v[4:5]
	v_lshl_add_u64 v[12:13], v[4:5], 0, v[10:11]
	v_cvt_pk_bf16_f32 v4, v150, v151
	v_cvt_pk_bf16_f32 v5, v152, v153
	v_cvt_pk_bf16_f32 v6, v142, v143
	v_cvt_pk_bf16_f32 v7, v144, v145
	global_store_dwordx4 v[12:13], v[4:7], off sc1
	s_nop 1
	v_cvt_pk_bf16_f32 v4, v130, v131
	v_cvt_pk_bf16_f32 v5, v132, v133
	v_cvt_pk_bf16_f32 v6, v122, v123
	v_cvt_pk_bf16_f32 v7, v124, v125
	global_store_dwordx4 v[12:13], v[4:7], off offset:256 sc1
	s_nop 1
	v_or_b32_e32 v4, 32, v8
	v_ashrrev_i32_e32 v5, 31, v4
	v_lshlrev_b64 v[4:5], 13, v[4:5]
	v_lshl_add_u64 v[4:5], s[6:7], 0, v[4:5]
	v_lshl_add_u64 v[12:13], v[4:5], 0, v[10:11]
	v_cvt_pk_bf16_f32 v4, v134, v135
	v_cvt_pk_bf16_f32 v5, v136, v137
	v_cvt_pk_bf16_f32 v6, v126, v127
	v_cvt_pk_bf16_f32 v7, v128, v129
	global_store_dwordx4 v[12:13], v[4:7], off sc1
	s_nop 1
	v_cvt_pk_bf16_f32 v4, v114, v115
	v_cvt_pk_bf16_f32 v5, v116, v117
	v_cvt_pk_bf16_f32 v6, v106, v107
	v_cvt_pk_bf16_f32 v7, v108, v109
	global_store_dwordx4 v[12:13], v[4:7], off offset:256 sc1
	s_nop 1
	v_or_b32_e32 v4, 48, v8
	v_ashrrev_i32_e32 v5, 31, v4
	v_lshlrev_b64 v[4:5], 13, v[4:5]
	v_lshl_add_u64 v[4:5], s[6:7], 0, v[4:5]
	v_lshl_add_u64 v[8:9], v[4:5], 0, v[10:11]
	v_cvt_pk_bf16_f32 v4, v118, v119
	v_cvt_pk_bf16_f32 v5, v120, v121
	v_cvt_pk_bf16_f32 v6, v110, v111
	v_cvt_pk_bf16_f32 v7, v112, v113
	global_store_dwordx4 v[8:9], v[4:7], off sc1
	v_add_co_u32_e32 v10, vcc, s2, v2
	s_nop 0
	v_cvt_pk_bf16_f32 v4, v102, v103
	v_cvt_pk_bf16_f32 v5, v104, v105
	v_cvt_pk_bf16_f32 v6, v98, v99
	v_cvt_pk_bf16_f32 v7, v100, v101
	global_store_dwordx4 v[8:9], v[4:7], off offset:256 sc1
	v_addc_co_u32_e32 v11, vcc, 0, v3, vcc
	s_nop 0
	v_cvt_pk_bf16_f32 v4, v94, v95
	v_cvt_pk_bf16_f32 v5, v96, v97
	v_cvt_pk_bf16_f32 v6, v90, v91
	v_cvt_pk_bf16_f32 v7, v92, v93
	s_mov_b32 s2, 0x120000
	v_lshl_add_u64 v[8:9], v[2:3], 0, s[26:27]
	global_store_dwordx4 v[10:11], v[4:7], off sc1
	v_add_co_u32_e32 v10, vcc, s2, v2
	s_nop 0
	v_cvt_pk_bf16_f32 v4, v82, v83
	v_cvt_pk_bf16_f32 v5, v84, v85
	v_cvt_pk_bf16_f32 v6, v74, v75
	v_cvt_pk_bf16_f32 v7, v76, v77
	global_store_dwordx4 v[8:9], v[4:7], off offset:256 sc1
	s_mov_b64 s[26:27], 0x120000
	v_addc_co_u32_e32 v11, vcc, 0, v3, vcc
	v_cvt_pk_bf16_f32 v4, v86, v87
	v_cvt_pk_bf16_f32 v5, v88, v89
	v_cvt_pk_bf16_f32 v6, v78, v79
	v_cvt_pk_bf16_f32 v7, v80, v81
	s_mov_b32 s2, 0x140000
	v_lshl_add_u64 v[8:9], v[2:3], 0, s[26:27]
	global_store_dwordx4 v[10:11], v[4:7], off sc1
	s_mov_b64 s[26:27], 0x140000
	v_add_co_u32_e32 v10, vcc, s2, v2
	v_cvt_pk_bf16_f32 v4, v66, v67
	v_cvt_pk_bf16_f32 v5, v68, v69
	v_cvt_pk_bf16_f32 v6, v58, v59
	v_cvt_pk_bf16_f32 v7, v60, v61
	global_store_dwordx4 v[8:9], v[4:7], off offset:256 sc1
	v_lshl_add_u64 v[8:9], v[2:3], 0, s[26:27]
	v_addc_co_u32_e32 v11, vcc, 0, v3, vcc
	v_cvt_pk_bf16_f32 v4, v70, v71
	v_cvt_pk_bf16_f32 v5, v72, v73
	v_cvt_pk_bf16_f32 v6, v62, v63
	v_cvt_pk_bf16_f32 v7, v64, v65
	s_mov_b64 s[26:27], 0x160000
	s_mov_b32 s2, 0x160000
	global_store_dwordx4 v[10:11], v[4:7], off sc1
	s_nop 1
	v_cvt_pk_bf16_f32 v4, v50, v51
	v_cvt_pk_bf16_f32 v5, v52, v53
	v_cvt_pk_bf16_f32 v6, v42, v43
	v_cvt_pk_bf16_f32 v7, v44, v45
	global_store_dwordx4 v[8:9], v[4:7], off offset:256 sc1
	v_lshl_add_u64 v[8:9], v[2:3], 0, s[26:27]
	v_add_co_u32_e32 v2, vcc, s2, v2
	v_cvt_pk_bf16_f32 v4, v54, v55
	v_cvt_pk_bf16_f32 v5, v56, v57
	v_cvt_pk_bf16_f32 v6, v46, v47
	v_cvt_pk_bf16_f32 v7, v48, v49
	s_nop 1
	v_addc_co_u32_e32 v3, vcc, 0, v3, vcc
	s_andn2_b64 vcc, exec, s[0:1]
	s_mov_b64 s[0:1], -1
	global_store_dwordx4 v[2:3], v[4:7], off sc1
	v_cvt_pk_bf16_f32 v2, v38, v39
	v_cvt_pk_bf16_f32 v3, v40, v41
	s_nop 1
	v_cvt_pk_bf16_f32 v4, v34, v35
	v_cvt_pk_bf16_f32 v5, v36, v37
	global_store_dwordx4 v[8:9], v[2:5], off offset:256 sc1
	s_cbranch_vccnz .LBB0_277
	s_andn2_b64 vcc, exec, s[14:15]
	s_cbranch_vccnz .LBB0_276
	s_barrier
	s_branch .LBB0_276

.LBB0_427:
	s_or_b64 exec, exec, s[74:75]
	v_lshl_add_u64 v[146:147], s[44:45], 0, v[28:29]
	s_lshl_b32 s50, s2, 1
	v_lshl_add_u64 v[42:43], v[26:27], 0, v[28:29]
	v_lshl_add_u64 v[28:29], v[146:147], 0, s[50:51]
	v_lshl_add_u64 v[28:29], v[28:29], 0, v[128:129]
	v_add_co_u32_e32 v28, vcc, s97, v28
	v_mov_b32_e32 v169, s71
	s_nop 0
	v_addc_co_u32_e32 v29, vcc, 0, v29, vcc
	global_load_dwordx4 v[122:125], v[42:43], off
	global_load_dwordx4 v[106:109], v[28:29], off
	v_or_b32_e32 v168, s70, v132
	v_lshlrev_b64 v[28:29], 13, v[168:169]
	v_lshl_add_u64 v[42:43], v[26:27], 0, v[28:29]
	v_add_co_u32_e32 v44, vcc, s94, v42
	s_waitcnt vmcnt(2)
	v_lshlrev_b32_e32 v161, 16, v114
	v_addc_co_u32_e32 v45, vcc, -1, v43, vcc
	v_add_co_u32_e32 v46, vcc, s95, v42
	v_lshlrev_b32_e32 v160, 16, v118
	s_nop 0
	v_addc_co_u32_e32 v47, vcc, -1, v43, vcc
	v_add_co_u32_e32 v48, vcc, s96, v42
	v_mov_b32_e32 v158, v38
	s_nop 0
	v_addc_co_u32_e32 v49, vcc, -1, v43, vcc
	global_load_dwordx4 v[98:101], v[46:47], off
	global_load_dwordx4 v[86:89], v[48:49], off
	global_load_dwordx4 v[102:105], v[44:45], off
	global_load_dwordx4 v[90:93], v[42:43], off
	v_mov_b32_e32 v159, v18
	v_pk_mul_f32 v[160:161], v[158:159], v[160:161]
	v_lshlrev_b32_e32 v162, 16, v119
	v_add_f32_e32 v18, v22, v160
	v_add_f32_e32 v38, v18, v161
	v_and_b32_e32 v161, 0xffff0000, v114
	v_and_b32_e32 v160, 0xffff0000, v118
	v_mov_b32_e32 v18, v39
	v_pk_mul_f32 v[160:161], v[18:19], v[160:161]
	v_lshlrev_b32_e32 v163, 16, v115
	v_add_f32_e32 v114, v23, v160
	v_add_f32_e32 v143, v114, v161
	v_mov_b32_e32 v160, v40
	v_mov_b32_e32 v161, v20
	v_pk_mul_f32 v[162:163], v[160:161], v[162:163]
	v_and_b32_e32 v165, 0xffff0000, v116
	v_add_f32_e32 v114, v24, v162
	v_add_f32_e32 v247, v114, v163
	v_and_b32_e32 v163, 0xffff0000, v115
	v_and_b32_e32 v162, 0xffff0000, v119
	v_mov_b32_e32 v114, v41
	v_mov_b32_e32 v115, v21
	v_pk_mul_f32 v[118:119], v[114:115], v[162:163]
	v_lshlrev_b32_e32 v163, 16, v116
	v_add_f32_e32 v118, v25, v118
	v_add_f32_e32 v248, v118, v119
	v_lshlrev_b32_e32 v162, 16, v120
	v_mov_b32_e32 v118, v30
	v_mov_b32_e32 v119, v34
	v_pk_mul_f32 v[162:163], v[118:119], v[162:163]
	v_and_b32_e32 v164, 0xffff0000, v120
	v_add_f32_e32 v162, v14, v162
	v_add_f32_e32 v249, v162, v163
	v_mov_b32_e32 v162, v31
	v_mov_b32_e32 v163, v35
	v_pk_mul_f32 v[164:165], v[162:163], v[164:165]
	v_lshlrev_b32_e32 v166, 16, v121
	v_add_f32_e32 v116, v15, v164
	v_add_f32_e32 v250, v116, v165
	v_lshlrev_b32_e32 v167, 16, v117
	v_mov_b32_e32 v164, v32
	v_mov_b32_e32 v165, v36
	v_pk_mul_f32 v[166:167], v[164:165], v[166:167]
	v_lshl_add_u64 v[148:149], s[44:45], 0, v[28:29]
	v_add_f32_e32 v116, v16, v166
	v_add_f32_e32 v251, v116, v167
	v_and_b32_e32 v167, 0xffff0000, v117
	v_and_b32_e32 v166, 0xffff0000, v121
	v_mov_b32_e32 v116, v33
	v_mov_b32_e32 v117, v37
	v_pk_mul_f32 v[120:121], v[116:117], v[166:167]
	v_mov_b32_e32 v166, v10
	v_add_f32_e32 v120, v17, v120
	v_add_f32_e32 v252, v120, v121
	v_lshlrev_b32_e32 v120, 16, v110
	v_mov_b32_e32 v167, v94
	v_lshl_add_u64 v[28:29], v[148:149], 0, s[50:51]
	v_lshl_add_u64 v[28:29], v[28:29], 0, v[128:129]
	v_mov_b32_e32 v157, s71
	s_waitcnt vmcnt(5)
	v_lshlrev_b32_e32 v121, 16, v122
	v_pk_mul_f32 v[120:121], v[166:167], v[120:121]
	v_or_b32_e32 v156, s70, v134
	v_add_f32_e32 v10, v38, v120
	v_add_f32_e32 v38, v10, v121
	v_and_b32_e32 v121, 0xffff0000, v110
	v_and_b32_e32 v120, 0xffff0000, v122
	v_mov_b32_e32 v10, v95
	v_pk_mul_f32 v[94:95], v[10:11], v[120:121]
	v_lshlrev_b32_e32 v121, 16, v111
	v_add_f32_e32 v95, v143, v95
	v_add_f32_e32 v122, v94, v95
	v_lshlrev_b32_e32 v120, 16, v123
	v_mov_b32_e32 v94, v96
	v_mov_b32_e32 v95, v12
	v_pk_mul_f32 v[120:121], v[94:95], v[120:121]
	v_and_b32_e32 v111, 0xffff0000, v111
	v_add_f32_e32 v12, v247, v121
	v_add_f32_e32 v120, v120, v12
	v_and_b32_e32 v110, 0xffff0000, v123
	v_mov_b32_e32 v12, v97
	v_pk_mul_f32 v[96:97], v[12:13], v[110:111]
	v_lshlrev_b32_e32 v111, 16, v112
	v_add_f32_e32 v97, v248, v97
	v_add_f32_e32 v121, v96, v97
	v_lshlrev_b32_e32 v110, 16, v124
	v_mov_b32_e32 v96, v82
	v_mov_b32_e32 v97, v6
	v_pk_mul_f32 v[110:111], v[96:97], v[110:111]
	v_add_co_u32_e32 v28, vcc, s97, v28
	v_add_f32_e32 v6, v249, v111
	v_add_f32_e32 v123, v110, v6
	v_and_b32_e32 v111, 0xffff0000, v112
	v_and_b32_e32 v110, 0xffff0000, v124
	v_mov_b32_e32 v6, v83
	v_pk_mul_f32 v[82:83], v[6:7], v[110:111]
	v_lshlrev_b32_e32 v111, 16, v113
	v_add_f32_e32 v83, v250, v83
	v_add_f32_e32 v112, v82, v83
	v_lshlrev_b32_e32 v110, 16, v125
	v_mov_b32_e32 v82, v84
	v_mov_b32_e32 v83, v8
	v_pk_mul_f32 v[110:111], v[82:83], v[110:111]
	v_mul_f32_e32 v84, 0xbfb8aa3b, v38
	v_add_f32_e32 v8, v251, v111
	v_add_f32_e32 v124, v110, v8
	v_and_b32_e32 v111, 0xffff0000, v113
	v_and_b32_e32 v110, 0xffff0000, v125
	v_mov_b32_e32 v8, v85
	v_exp_f32_e32 v113, v84
	v_pk_mul_f32 v[84:85], v[8:9], v[110:111]
	v_mul_f32_e32 v110, 0xbfb8aa3b, v122
	v_mul_f32_e32 v111, 0xbfb8aa3b, v120
	v_exp_f32_e32 v110, v110
	v_exp_f32_e32 v111, v111
	v_add_f32_e32 v85, v252, v85
	v_add_f32_e32 v84, v84, v85
	v_add_f32_e32 v85, 1.0, v113
	v_add_f32_e32 v110, 1.0, v110
	v_add_f32_e32 v111, 1.0, v111
	v_mul_f32_e32 v113, 0xbfb8aa3b, v121
	v_lshlrev_b64 v[42:43], 13, v[156:157]
	v_rcp_f32_e32 v85, v85
	v_rcp_f32_e32 v110, v110
	v_rcp_f32_e32 v111, v111
	v_exp_f32_e32 v113, v113
	v_addc_co_u32_e32 v29, vcc, 0, v29, vcc
	v_lshl_add_u64 v[44:45], v[26:27], 0, v[42:43]
	v_add_co_u32_e32 v46, vcc, s94, v44
	v_mul_f32_e32 v38, v38, v85
	s_nop 0
	v_addc_co_u32_e32 v47, vcc, -1, v45, vcc
	v_add_co_u32_e32 v48, vcc, s95, v44
	v_mul_f32_e32 v85, v122, v110
	v_mul_f32_e32 v111, v120, v111
	v_add_f32_e32 v110, 1.0, v113
	v_mul_f32_e32 v113, 0xbfb8aa3b, v123
	v_mul_f32_e32 v120, 0xbfb8aa3b, v112
	v_addc_co_u32_e32 v49, vcc, -1, v45, vcc
	v_lshl_add_u64 v[150:151], s[44:45], 0, v[42:43]
	v_rcp_f32_e32 v110, v110
	v_exp_f32_e32 v113, v113
	v_exp_f32_e32 v120, v120
	global_load_dwordx4 v[70:73], v[46:47], off
	global_load_dwordx4 v[74:77], v[48:49], off
	v_add_co_u32_e32 v46, vcc, s96, v44
	global_load_dwordx4 v[78:81], v[28:29], off
	global_load_dwordx4 v[62:65], v[44:45], off
	v_lshl_add_u64 v[28:29], v[150:151], 0, s[50:51]
	v_addc_co_u32_e32 v47, vcc, -1, v45, vcc
	v_lshl_add_u64 v[28:29], v[28:29], 0, v[128:129]
	v_add_co_u32_e32 v28, vcc, s97, v28
	v_lshl_add_u64 v[154:155], s[70:71], 0, v[136:137]
	s_nop 0
	v_addc_co_u32_e32 v29, vcc, 0, v29, vcc
	v_mul_f32_e32 v121, v121, v110
	v_add_f32_e32 v110, 1.0, v113
	v_add_f32_e32 v113, 1.0, v120
	v_mul_f32_e32 v120, 0xbfb8aa3b, v124
	v_mul_f32_e32 v122, 0xbfb8aa3b, v84
	global_load_dwordx4 v[66:69], v[46:47], off
	global_load_dwordx4 v[58:61], v[28:29], off
	v_lshlrev_b64 v[28:29], 13, v[154:155]
	v_exp_f32_e32 v120, v120
	v_exp_f32_e32 v122, v122
	v_lshl_add_u64 v[26:27], v[26:27], 0, v[28:29]
	v_add_co_u32_e32 v46, vcc, s94, v26
	v_add_f32_e32 v120, 1.0, v120
	s_nop 0
	v_addc_co_u32_e32 v47, vcc, -1, v27, vcc
	v_add_co_u32_e32 v42, vcc, s95, v26
	v_add_f32_e32 v122, 1.0, v122
	s_nop 0
	v_addc_co_u32_e32 v43, vcc, -1, v27, vcc
	v_rcp_f32_e32 v113, v113
	v_rcp_f32_e32 v120, v120
	v_rcp_f32_e32 v122, v122
	v_add_co_u32_e32 v44, vcc, s96, v26
	v_rcp_f32_e32 v110, v110
	s_nop 0
	v_addc_co_u32_e32 v45, vcc, -1, v27, vcc
	v_lshl_add_u64 v[152:153], s[44:45], 0, v[28:29]
	global_load_dwordx4 v[50:53], v[42:43], off
	s_nop 0
	global_load_dwordx4 v[42:45], v[44:45], off
	s_nop 0
	global_load_dwordx4 v[54:57], v[46:47], off
	s_nop 0
	global_load_dwordx4 v[46:49], v[26:27], off
	v_lshl_add_u64 v[26:27], v[152:153], 0, s[50:51]
	s_add_u32 s70, s80, s50
	v_lshl_add_u64 v[26:27], v[26:27], 0, v[128:129]
	s_addc_u32 s71, s81, 0
	v_mul_f32_e32 v112, v112, v113
	v_mul_f32_e32 v113, v124, v120
	v_mul_f32_e32 v84, v84, v122
	v_cvt_pk_bf16_f32 v111, v111, v121
	v_lshlrev_b64 v[120:121], 11, v[170:171]
	v_add_co_u32_e32 v26, vcc, s97, v26
	v_mul_f32_e32 v123, v123, v110
	v_cvt_pk_bf16_f32 v110, v38, v85
	v_cvt_pk_bf16_f32 v113, v113, v84
	v_lshl_add_u64 v[84:85], s[70:71], 0, v[120:121]
	v_mov_b32_e32 v143, v129
	v_addc_co_u32_e32 v27, vcc, 0, v27, vcc
	v_lshl_add_u64 v[84:85], v[84:85], 0, v[142:143]
	global_load_dwordx4 v[26:29], v[26:27], off
	v_cvt_pk_bf16_f32 v112, v123, v112
	global_store_dwordx4 v[84:85], v[110:113], off sc1
	s_waitcnt vmcnt(15)
	v_lshlrev_b32_e32 v85, 16, v98
	s_waitcnt vmcnt(13)
	v_lshlrev_b32_e32 v84, 16, v102
	v_pk_mul_f32 v[84:85], v[158:159], v[84:85]
	ds_write_b128 v242, v[106:109]
	v_add_f32_e32 v38, v22, v84
	v_add_f32_e32 v38, v38, v85
	v_and_b32_e32 v85, 0xffff0000, v98
	v_and_b32_e32 v84, 0xffff0000, v102
	v_pk_mul_f32 v[84:85], v[18:19], v[84:85]
	v_lshlrev_b64 v[106:107], 11, v[168:169]
	v_add_f32_e32 v84, v23, v84
	v_add_f32_e32 v98, v84, v85
	v_lshlrev_b32_e32 v85, 16, v99
	v_lshlrev_b32_e32 v84, 16, v103
	v_pk_mul_f32 v[84:85], v[160:161], v[84:85]
	v_lshlrev_b64 v[108:109], 11, v[156:157]
	v_add_f32_e32 v84, v24, v84
	v_add_f32_e32 v102, v84, v85
	v_and_b32_e32 v85, 0xffff0000, v99
	v_and_b32_e32 v84, 0xffff0000, v103
	v_pk_mul_f32 v[84:85], v[114:115], v[84:85]
	s_waitcnt vmcnt(9)
	ds_write_b128 v243, v[78:81]
	v_add_f32_e32 v84, v25, v84
	v_add_f32_e32 v99, v84, v85
	v_lshlrev_b32_e32 v85, 16, v100
	v_lshlrev_b32_e32 v84, 16, v104
	v_pk_mul_f32 v[84:85], v[118:119], v[84:85]
	v_lshlrev_b32_e32 v79, 16, v74
	v_add_f32_e32 v84, v14, v84
	v_add_f32_e32 v103, v84, v85
	v_and_b32_e32 v85, 0xffff0000, v100
	v_and_b32_e32 v84, 0xffff0000, v104
	v_pk_mul_f32 v[84:85], v[162:163], v[84:85]
	v_lshlrev_b32_e32 v78, 16, v70
	v_add_f32_e32 v84, v15, v84
	v_add_f32_e32 v100, v84, v85
	v_lshlrev_b32_e32 v85, 16, v101
	v_lshlrev_b32_e32 v84, 16, v105
	v_pk_mul_f32 v[84:85], v[164:165], v[84:85]
	v_pk_mul_f32 v[78:79], v[158:159], v[78:79]
	v_add_f32_e32 v84, v16, v84
	v_add_f32_e32 v104, v84, v85
	v_and_b32_e32 v85, 0xffff0000, v101
	v_and_b32_e32 v84, 0xffff0000, v105
	v_pk_mul_f32 v[84:85], v[116:117], v[84:85]
	v_lshlrev_b64 v[110:111], 11, v[154:155]
	v_add_f32_e32 v84, v17, v84
	v_add_f32_e32 v101, v84, v85
	v_lshlrev_b32_e32 v84, 16, v86
	v_lshlrev_b32_e32 v85, 16, v90
	v_pk_mul_f32 v[84:85], v[166:167], v[84:85]
	v_readlane_b32 s4, v254, 7
	v_add_f32_e32 v38, v38, v84
	v_add_f32_e32 v38, v38, v85
	v_and_b32_e32 v85, 0xffff0000, v86
	v_and_b32_e32 v84, 0xffff0000, v90
	v_pk_mul_f32 v[84:85], v[10:11], v[84:85]
	v_readlane_b32 s18, v254, 21
	v_add_f32_e32 v85, v98, v85
	v_add_f32_e32 v86, v84, v85
	v_lshlrev_b32_e32 v85, 16, v87
	v_lshlrev_b32_e32 v84, 16, v91
	v_pk_mul_f32 v[84:85], v[94:95], v[84:85]
	v_readlane_b32 s19, v254, 22
	v_add_f32_e32 v85, v102, v85
	v_add_f32_e32 v90, v84, v85
	v_and_b32_e32 v85, 0xffff0000, v87
	v_and_b32_e32 v84, 0xffff0000, v91
	v_pk_mul_f32 v[84:85], v[12:13], v[84:85]
	s_waitcnt vmcnt(6)
	ds_write_b128 v244, v[58:61]
	v_add_f32_e32 v85, v99, v85
	v_add_f32_e32 v87, v84, v85
	v_lshlrev_b32_e32 v85, 16, v88
	v_lshlrev_b32_e32 v84, 16, v92
	v_pk_mul_f32 v[84:85], v[96:97], v[84:85]
	v_mul_f32_e32 v98, 0xbfb8aa3b, v87
	v_add_f32_e32 v85, v103, v85
	v_add_f32_e32 v91, v84, v85
	v_and_b32_e32 v85, 0xffff0000, v88
	v_and_b32_e32 v84, 0xffff0000, v92
	v_pk_mul_f32 v[84:85], v[6:7], v[84:85]
	v_exp_f32_e32 v98, v98
	v_add_f32_e32 v85, v100, v85
	v_add_f32_e32 v88, v84, v85
	v_lshlrev_b32_e32 v85, 16, v89
	v_lshlrev_b32_e32 v84, 16, v93
	v_pk_mul_f32 v[84:85], v[82:83], v[84:85]
	s_waitcnt vmcnt(1)
	ds_write_b128 v245, v[26:29]
	v_add_f32_e32 v85, v104, v85
	v_add_f32_e32 v92, v84, v85
	v_and_b32_e32 v85, 0xffff0000, v89
	v_mul_f32_e32 v89, 0xbfb8aa3b, v38
	v_exp_f32_e32 v89, v89
	v_and_b32_e32 v84, 0xffff0000, v93
	v_pk_mul_f32 v[84:85], v[8:9], v[84:85]
	v_mul_f32_e32 v93, 0xbfb8aa3b, v90
	v_add_f32_e32 v85, v101, v85
	v_add_f32_e32 v84, v84, v85
	v_add_f32_e32 v85, 1.0, v89
	v_mul_f32_e32 v89, 0xbfb8aa3b, v86
	v_exp_f32_e32 v89, v89
	v_exp_f32_e32 v93, v93
	v_rcp_f32_e32 v85, v85
	v_readlane_b32 s5, v254, 8
	v_add_f32_e32 v89, 1.0, v89
	v_add_f32_e32 v93, 1.0, v93
	v_rcp_f32_e32 v89, v89
	v_rcp_f32_e32 v93, v93
	v_mul_f32_e32 v38, v38, v85
	v_readlane_b32 s6, v254, 9
	v_mul_f32_e32 v85, v86, v89
	v_mul_f32_e32 v86, v90, v93
	v_add_f32_e32 v89, 1.0, v98
	v_mul_f32_e32 v90, 0xbfb8aa3b, v91
	v_mul_f32_e32 v98, 0xbfb8aa3b, v84
	v_rcp_f32_e32 v89, v89
	v_exp_f32_e32 v90, v90
	v_exp_f32_e32 v98, v98
	v_mul_f32_e32 v93, 0xbfb8aa3b, v88
	v_mul_f32_e32 v87, v87, v89
	v_add_f32_e32 v89, 1.0, v90
	v_add_f32_e32 v98, 1.0, v98
	v_rcp_f32_e32 v89, v89
	v_rcp_f32_e32 v98, v98
	v_exp_f32_e32 v93, v93
	v_readlane_b32 s7, v254, 10
	v_mul_f32_e32 v89, v91, v89
	v_mul_f32_e32 v91, v84, v98
	v_cvt_pk_bf16_f32 v84, v38, v85
	v_add_f32_e32 v38, v22, v78
	v_add_f32_e32 v80, v38, v79
	v_and_b32_e32 v79, 0xffff0000, v70
	v_and_b32_e32 v78, 0xffff0000, v74
	v_mov_b32_e32 v38, v19
	v_pk_mul_f32 v[38:39], v[38:39], v[78:79]
	v_mov_b32_e32 v78, v20
	v_add_f32_e32 v39, v23, v39
	v_add_f32_e32 v70, v38, v39
	v_lshlrev_b32_e32 v39, 16, v71
	v_lshlrev_b32_e32 v38, 16, v75
	v_mov_b32_e32 v79, v40
	v_pk_mul_f32 v[38:39], v[78:79], v[38:39]
	v_mov_b32_e32 v40, v21
	v_add_f32_e32 v20, v24, v39
	v_add_f32_e32 v74, v38, v20
	v_and_b32_e32 v39, 0xffff0000, v71
	v_and_b32_e32 v38, 0xffff0000, v75
	v_pk_mul_f32 v[20:21], v[40:41], v[38:39]
	v_mov_b32_e32 v38, v34
	v_add_f32_e32 v21, v25, v21
	v_add_f32_e32 v40, v20, v21
	v_lshlrev_b32_e32 v21, 16, v72
	v_lshlrev_b32_e32 v20, 16, v76
	v_mov_b32_e32 v39, v30
	v_pk_mul_f32 v[20:21], v[38:39], v[20:21]
	v_mov_b32_e32 v30, v35
	v_add_f32_e32 v21, v14, v21
	v_add_f32_e32 v34, v20, v21
	v_and_b32_e32 v21, 0xffff0000, v72
	v_and_b32_e32 v20, 0xffff0000, v76
	v_pk_mul_f32 v[20:21], v[30:31], v[20:21]
	v_mov_b32_e32 v30, v36
	v_add_f32_e32 v21, v15, v21
	v_add_f32_e32 v35, v20, v21
	v_lshlrev_b32_e32 v21, 16, v73
	v_lshlrev_b32_e32 v20, 16, v77
	v_mov_b32_e32 v31, v32
	v_pk_mul_f32 v[20:21], v[30:31], v[20:21]
	v_mov_b32_e32 v32, v37
	v_add_f32_e32 v21, v16, v21
	v_add_f32_e32 v30, v20, v21
	v_and_b32_e32 v21, 0xffff0000, v73
	v_and_b32_e32 v20, 0xffff0000, v77
	v_pk_mul_f32 v[20:21], v[32:33], v[20:21]
	v_add_f32_e32 v90, 1.0, v93
	v_add_f32_e32 v21, v17, v21
	v_add_f32_e32 v31, v20, v21
	v_lshlrev_b32_e32 v20, 16, v66
	v_lshlrev_b32_e32 v21, 16, v62
	v_pk_mul_f32 v[20:21], v[166:167], v[20:21]
	v_mul_f32_e32 v93, 0xbfb8aa3b, v92
	v_add_f32_e32 v20, v80, v20
	v_add_f32_e32 v32, v20, v21
	v_and_b32_e32 v21, 0xffff0000, v66
	v_and_b32_e32 v20, 0xffff0000, v62
	v_pk_mul_f32 v[20:21], v[10:11], v[20:21]
	v_mul_f32_e32 v38, 0xbfb8aa3b, v32
	v_add_f32_e32 v21, v21, v70
	v_add_f32_e32 v33, v20, v21
	v_lshlrev_b32_e32 v21, 16, v67
	v_lshlrev_b32_e32 v20, 16, v63
	v_pk_mul_f32 v[20:21], v[94:95], v[20:21]
	v_exp_f32_e32 v38, v38
	v_add_f32_e32 v21, v21, v74
	v_add_f32_e32 v36, v20, v21
	v_and_b32_e32 v21, 0xffff0000, v67
	v_and_b32_e32 v20, 0xffff0000, v63
	v_pk_mul_f32 v[20:21], v[12:13], v[20:21]
	v_exp_f32_e32 v93, v93
	v_add_f32_e32 v21, v21, v40
	v_add_f32_e32 v37, v20, v21
	v_lshlrev_b32_e32 v21, 16, v68
	v_lshlrev_b32_e32 v20, 16, v64
	v_pk_mul_f32 v[20:21], v[96:97], v[20:21]
	v_mul_f32_e32 v39, 0xbfb8aa3b, v37
	v_add_f32_e32 v21, v21, v34
	v_add_f32_e32 v34, v20, v21
	v_and_b32_e32 v21, 0xffff0000, v68
	v_and_b32_e32 v20, 0xffff0000, v64
	v_pk_mul_f32 v[20:21], v[6:7], v[20:21]
	v_exp_f32_e32 v39, v39
	v_add_f32_e32 v21, v21, v35
	v_add_f32_e32 v35, v20, v21
	v_lshlrev_b32_e32 v21, 16, v69
	v_lshlrev_b32_e32 v20, 16, v65
	v_pk_mul_f32 v[20:21], v[82:83], v[20:21]
	v_rcp_f32_e32 v90, v90
	v_add_f32_e32 v21, v21, v30
	v_add_f32_e32 v30, v20, v21
	v_and_b32_e32 v21, 0xffff0000, v69
	v_and_b32_e32 v20, 0xffff0000, v65
	v_pk_mul_f32 v[20:21], v[8:9], v[20:21]
	v_add_f32_e32 v93, 1.0, v93
	v_add_f32_e32 v21, v21, v31
	v_add_f32_e32 v20, v20, v21
	v_add_f32_e32 v21, 1.0, v38
	v_mul_f32_e32 v31, 0xbfb8aa3b, v33
	v_mul_f32_e32 v38, 0xbfb8aa3b, v36
	v_exp_f32_e32 v31, v31
	v_exp_f32_e32 v38, v38
	v_rcp_f32_e32 v21, v21
	v_rcp_f32_e32 v93, v93
	v_add_f32_e32 v31, 1.0, v31
	v_add_f32_e32 v38, 1.0, v38
	v_rcp_f32_e32 v31, v31
	v_rcp_f32_e32 v38, v38
	v_mul_f32_e32 v21, v32, v21
	v_mul_f32_e32 v88, v88, v90
	v_mul_f32_e32 v31, v33, v31
	v_mul_f32_e32 v32, v36, v38
	v_add_f32_e32 v33, 1.0, v39
	v_mul_f32_e32 v38, 0xbfb8aa3b, v35
	v_rcp_f32_e32 v33, v33
	v_exp_f32_e32 v38, v38
	v_mul_f32_e32 v39, 0xbfb8aa3b, v20
	v_mul_f32_e32 v36, 0xbfb8aa3b, v34
	v_mul_f32_e32 v33, v37, v33
	v_add_f32_e32 v37, 1.0, v38
	v_mul_f32_e32 v38, 0xbfb8aa3b, v30
	v_exp_f32_e32 v39, v39
	v_exp_f32_e32 v36, v36
	v_exp_f32_e32 v38, v38
	v_rcp_f32_e32 v37, v37
	v_add_f32_e32 v39, 1.0, v39
	v_add_f32_e32 v36, 1.0, v36
	v_add_f32_e32 v38, 1.0, v38
	v_rcp_f32_e32 v39, v39
	v_rcp_f32_e32 v36, v36
	v_rcp_f32_e32 v38, v38
	v_cvt_pk_bf16_f32 v85, v86, v87
	v_mul_f32_e32 v20, v20, v39
	v_cvt_pk_bf16_f32 v86, v89, v88
	v_lshl_add_u64 v[88:89], s[70:71], 0, v[106:107]
	v_mul_f32_e32 v34, v34, v36
	v_mul_f32_e32 v36, v30, v38
	v_cvt_pk_bf16_f32 v30, v21, v31
	v_cvt_pk_bf16_f32 v31, v32, v33
	v_cvt_pk_bf16_f32 v33, v36, v20
	v_lshl_add_u64 v[20:21], s[70:71], 0, v[108:109]
	v_lshl_add_u64 v[88:89], v[88:89], 0, v[142:143]
	v_lshl_add_u64 v[20:21], v[20:21], 0, v[142:143]
	v_mul_f32_e32 v90, v92, v93
	v_cvt_pk_bf16_f32 v87, v90, v91
	global_store_dwordx4 v[88:89], v[84:87], off sc1
	v_mul_f32_e32 v35, v35, v37
	v_cvt_pk_bf16_f32 v32, v34, v35
	global_store_dwordx4 v[20:21], v[30:33], off sc1
	v_lshlrev_b32_e32 v21, 16, v50
	v_lshlrev_b32_e32 v20, 16, v54
	v_pk_mul_f32 v[20:21], v[158:159], v[20:21]
	v_or_b32_e32 v38, 0x400, v246
	v_add_f32_e32 v20, v22, v20
	v_add_f32_e32 v22, v20, v21
	v_and_b32_e32 v21, 0xffff0000, v50
	v_and_b32_e32 v20, 0xffff0000, v54
	v_pk_mul_f32 v[18:19], v[18:19], v[20:21]
	v_readlane_b32 s8, v254, 11
	v_add_f32_e32 v18, v23, v18
	v_add_f32_e32 v20, v18, v19
	v_lshlrev_b32_e32 v19, 16, v51
	v_lshlrev_b32_e32 v18, 16, v55
	v_pk_mul_f32 v[18:19], v[160:161], v[18:19]
	v_readlane_b32 s9, v254, 12
	v_add_f32_e32 v18, v24, v18
	v_add_f32_e32 v21, v18, v19
	v_and_b32_e32 v19, 0xffff0000, v51
	v_and_b32_e32 v18, 0xffff0000, v55
	v_pk_mul_f32 v[18:19], v[114:115], v[18:19]
	v_readlane_b32 s10, v254, 13
	v_add_f32_e32 v18, v25, v18
	v_add_f32_e32 v23, v18, v19
	v_lshlrev_b32_e32 v19, 16, v52
	v_lshlrev_b32_e32 v18, 16, v56
	v_pk_mul_f32 v[18:19], v[118:119], v[18:19]
	v_readlane_b32 s11, v254, 14
	v_add_f32_e32 v14, v14, v18
	v_add_f32_e32 v24, v14, v19
	v_and_b32_e32 v19, 0xffff0000, v52
	v_and_b32_e32 v18, 0xffff0000, v56
	v_pk_mul_f32 v[18:19], v[162:163], v[18:19]
	v_readlane_b32 s12, v254, 15
	v_add_f32_e32 v14, v15, v18
	v_add_f32_e32 v18, v14, v19
	v_lshlrev_b32_e32 v15, 16, v53
	v_lshlrev_b32_e32 v14, 16, v57
	v_pk_mul_f32 v[14:15], v[164:165], v[14:15]
	v_readlane_b32 s13, v254, 16
	v_add_f32_e32 v14, v16, v14
	v_add_f32_e32 v16, v14, v15
	v_and_b32_e32 v15, 0xffff0000, v53
	v_and_b32_e32 v14, 0xffff0000, v57
	v_pk_mul_f32 v[14:15], v[116:117], v[14:15]
	v_readlane_b32 s14, v254, 17
	v_add_f32_e32 v14, v17, v14
	v_add_f32_e32 v17, v14, v15
	v_lshlrev_b32_e32 v14, 16, v42
	v_lshlrev_b32_e32 v15, 16, v46
	v_pk_mul_f32 v[14:15], v[166:167], v[14:15]
	v_readlane_b32 s15, v254, 18
	v_add_f32_e32 v14, v22, v14
	v_add_f32_e32 v19, v14, v15
	v_and_b32_e32 v15, 0xffff0000, v42
	v_and_b32_e32 v14, 0xffff0000, v46
	v_pk_mul_f32 v[10:11], v[10:11], v[14:15]
	v_lshlrev_b32_e32 v22, 2, v38
	v_add_f32_e32 v11, v20, v11
	v_add_f32_e32 v14, v10, v11
	v_lshlrev_b32_e32 v11, 16, v43
	v_lshlrev_b32_e32 v10, 16, v47
	v_pk_mul_f32 v[10:11], v[94:95], v[10:11]
	v_readlane_b32 s16, v254, 19
	v_add_f32_e32 v11, v21, v11
	v_add_f32_e32 v15, v10, v11
	v_and_b32_e32 v11, 0xffff0000, v43
	v_and_b32_e32 v10, 0xffff0000, v47
	v_pk_mul_f32 v[10:11], v[12:13], v[10:11]
	v_readlane_b32 s17, v254, 20
	v_add_f32_e32 v11, v23, v11
	v_add_f32_e32 v12, v10, v11
	v_lshlrev_b32_e32 v11, 16, v44
	v_lshlrev_b32_e32 v10, 16, v48
	v_pk_mul_f32 v[10:11], v[96:97], v[10:11]
	v_mov_b32_e32 v23, v129
	v_add_f32_e32 v11, v24, v11
	v_add_f32_e32 v13, v10, v11
	v_and_b32_e32 v11, 0xffff0000, v44
	v_and_b32_e32 v10, 0xffff0000, v48
	v_pk_mul_f32 v[6:7], v[6:7], v[10:11]
	v_mov_b32_e32 v98, 0
	v_add_f32_e32 v7, v18, v7
	v_add_f32_e32 v10, v6, v7
	v_lshlrev_b32_e32 v7, 16, v45
	v_lshlrev_b32_e32 v6, 16, v49
	v_pk_mul_f32 v[6:7], v[82:83], v[6:7]
	v_lshlrev_b32_e32 v38, 1, v38
	v_add_f32_e32 v7, v16, v7
	v_add_f32_e32 v11, v6, v7
	v_and_b32_e32 v7, 0xffff0000, v45
	v_and_b32_e32 v6, 0xffff0000, v49
	v_mul_f32_e32 v16, 0xbfb8aa3b, v19
	v_pk_mul_f32 v[6:7], v[8:9], v[6:7]
	v_mul_f32_e32 v8, 0xbfb8aa3b, v14
	v_mul_f32_e32 v9, 0xbfb8aa3b, v15
	v_exp_f32_e32 v16, v16
	v_exp_f32_e32 v8, v8
	v_exp_f32_e32 v9, v9
	v_add_f32_e32 v7, v17, v7
	v_add_f32_e32 v6, v6, v7
	v_add_f32_e32 v7, 1.0, v16
	v_add_f32_e32 v8, 1.0, v8
	v_add_f32_e32 v9, 1.0, v9
	v_mul_f32_e32 v16, 0xbfb8aa3b, v12
	v_rcp_f32_e32 v8, v8
	v_rcp_f32_e32 v9, v9
	v_exp_f32_e32 v16, v16
	v_mul_f32_e32 v17, 0xbfb8aa3b, v6
	v_mul_f32_e32 v8, v14, v8
	v_mul_f32_e32 v9, v15, v9
	v_add_f32_e32 v14, 1.0, v16
	v_mul_f32_e32 v15, 0xbfb8aa3b, v13
	v_mul_f32_e32 v16, 0xbfb8aa3b, v10
	v_rcp_f32_e32 v14, v14
	v_exp_f32_e32 v15, v15
	v_exp_f32_e32 v16, v16
	v_exp_f32_e32 v17, v17
	v_mul_f32_e32 v12, v12, v14
	v_add_f32_e32 v14, 1.0, v15
	v_add_f32_e32 v15, 1.0, v16
	v_mul_f32_e32 v16, 0xbfb8aa3b, v11
	v_exp_f32_e32 v16, v16
	v_rcp_f32_e32 v7, v7
	v_rcp_f32_e32 v15, v15
	v_add_f32_e32 v17, 1.0, v17
	v_add_f32_e32 v16, 1.0, v16
	v_rcp_f32_e32 v16, v16
	v_rcp_f32_e32 v14, v14
	v_rcp_f32_e32 v17, v17
	v_mul_f32_e32 v7, v19, v7
	v_mul_f32_e32 v10, v10, v15
	v_mul_f32_e32 v11, v11, v16
	v_mul_f32_e32 v13, v13, v14
	v_mul_f32_e32 v14, v6, v17
	v_cvt_pk_bf16_f32 v6, v7, v8
	v_cvt_pk_bf16_f32 v7, v9, v12
	v_cvt_pk_bf16_f32 v8, v13, v10
	v_cvt_pk_bf16_f32 v9, v11, v14
	v_lshl_add_u64 v[10:11], s[70:71], 0, v[110:111]
	v_lshl_add_u64 v[10:11], v[10:11], 0, v[142:143]
	v_lshl_add_u64 v[18:19], s[18:19], 0, v[22:23]
	global_store_dwordx4 v[10:11], v[6:9], off sc1
	s_waitcnt lgkmcnt(0)
	s_barrier
	v_add_co_u32_e32 v8, vcc, 0x2000, v18
	s_nop 1
	v_addc_co_u32_e32 v9, vcc, 0, v19, vcc
	global_load_dwordx4 v[26:29], v22, s[18:19] offset:16
	global_load_dwordx4 v[34:37], v22, s[18:19]
	v_lshl_add_u64 v[6:7], v[18:19], 0, s[62:63]
	global_load_dwordx4 v[14:17], v[8:9], off
	global_load_dwordx4 v[30:33], v[6:7], off offset:16
	v_add_co_u32_e32 v8, vcc, 0x4000, v18
	v_lshl_add_u64 v[6:7], v[18:19], 0, s[64:65]
	s_nop 0
	v_addc_co_u32_e32 v9, vcc, 0, v19, vcc
	v_lshl_add_u64 v[20:21], v[18:19], 0, s[68:69]
	v_add_co_u32_e32 v18, vcc, 0x6000, v18
	v_readlane_b32 s4, v254, 23
	s_nop 0
	v_addc_co_u32_e32 v19, vcc, 0, v19, vcc
	v_readlane_b32 s5, v254, 24
	global_load_dwordx4 v[10:13], v[8:9], off
	s_nop 0
	global_load_dwordx4 v[6:9], v[6:7], off offset:16
	s_nop 0
	global_load_dwordx4 v[90:93], v[18:19], off
	global_load_dwordx4 v[86:89], v[20:21], off offset:16
	s_nop 0
	global_load_dwordx4 v[18:21], v22, s[4:5] offset:16
	s_nop 0
	global_load_dwordx4 v[22:25], v22, s[4:5]
	v_mov_b32_e32 v102, 0
	v_mov_b32_e32 v103, 0
	v_mov_b32_e32 v104, 0
	v_mov_b32_e32 v105, 0
	v_readlane_b32 s6, v254, 25
	v_readlane_b32 s7, v254, 26
	v_readlane_b32 s8, v254, 27
	v_readlane_b32 s9, v254, 28
	v_readlane_b32 s10, v254, 29
	v_readlane_b32 s11, v254, 30
	v_readlane_b32 s12, v254, 31
	v_readlane_b32 s13, v254, 32
	v_readlane_b32 s14, v254, 33
	v_readlane_b32 s15, v254, 34
	v_readlane_b32 s16, v254, 35
	v_readlane_b32 s17, v254, 36
	v_readlane_b32 s18, v254, 37
	v_readlane_b32 s19, v254, 38
	s_and_saveexec_b64 s[70:71], s[88:89]
	s_cbranch_execz .LBB0_429
	v_mov_b32_e32 v39, v129
	v_lshl_add_u64 v[40:41], v[146:147], 0, v[38:39]
	v_add_co_u32_e32 v40, vcc, 0xffffa000, v40
	s_nop 1
	v_addc_co_u32_e32 v41, vcc, -1, v41, vcc
	global_load_dwordx4 v[102:105], v[40:41], off

.LBB0_433:
	s_or_b64 exec, exec, s[16:17]
	v_mov_b32_e32 v39, v129
	v_lshl_add_u64 v[42:43], v[148:149], 0, v[38:39]
	v_add_co_u32_e32 v44, vcc, s94, v42
	v_lshl_add_u64 v[40:41], v[146:147], 0, v[38:39]
	s_nop 0
	v_addc_co_u32_e32 v45, vcc, -1, v43, vcc
	v_add_co_u32_e32 v46, vcc, s95, v42
	s_waitcnt vmcnt(0)
	v_lshlrev_b32_e32 v115, 16, v98
	v_addc_co_u32_e32 v47, vcc, -1, v43, vcc
	global_load_dwordx4 v[78:81], v[44:45], off
	global_load_dwordx4 v[82:85], v[46:47], off
	global_load_dwordx4 v[122:125], v[40:41], off
	global_load_dwordx4 v[70:73], v[42:43], off
	v_lshlrev_b32_e32 v114, 16, v102
	v_mov_b32_e32 v112, v34
	v_mov_b32_e32 v113, v14
	v_pk_mul_f32 v[114:115], v[112:113], v[114:115]
	v_lshlrev_b32_e32 v116, 16, v103
	v_add_f32_e32 v14, v22, v114
	v_add_f32_e32 v34, v14, v115
	v_and_b32_e32 v115, 0xffff0000, v98
	v_and_b32_e32 v114, 0xffff0000, v102
	v_mov_b32_e32 v14, v35
	v_pk_mul_f32 v[114:115], v[14:15], v[114:115]
	v_lshlrev_b32_e32 v117, 16, v99
	v_add_f32_e32 v98, v23, v114
	v_add_f32_e32 v143, v98, v115
	v_mov_b32_e32 v114, v36
	v_mov_b32_e32 v115, v16
	v_pk_mul_f32 v[116:117], v[114:115], v[116:117]
	v_lshl_add_u64 v[40:41], v[150:151], 0, v[38:39]
	v_add_f32_e32 v98, v24, v116
	v_add_f32_e32 v148, v98, v117
	v_and_b32_e32 v117, 0xffff0000, v99
	v_and_b32_e32 v116, 0xffff0000, v103
	v_mov_b32_e32 v98, v37
	v_mov_b32_e32 v99, v17
	v_pk_mul_f32 v[102:103], v[98:99], v[116:117]
	v_lshlrev_b32_e32 v117, 16, v100
	v_add_f32_e32 v102, v25, v102
	v_add_f32_e32 v149, v102, v103
	v_lshlrev_b32_e32 v116, 16, v104
	v_mov_b32_e32 v102, v26
	v_mov_b32_e32 v103, v30
	v_pk_mul_f32 v[116:117], v[102:103], v[116:117]
	v_and_b32_e32 v119, 0xffff0000, v100
	v_add_f32_e32 v116, v18, v116
	v_add_f32_e32 v150, v116, v117
	v_and_b32_e32 v118, 0xffff0000, v104
	v_mov_b32_e32 v116, v27
	v_mov_b32_e32 v117, v31
	v_add_co_u32_e32 v44, vcc, s96, v42
	v_pk_mul_f32 v[118:119], v[116:117], v[118:119]
	s_nop 0
	v_addc_co_u32_e32 v45, vcc, -1, v43, vcc
	v_add_f32_e32 v100, v19, v118
	v_add_co_u32_e32 v42, vcc, s94, v40
	v_add_f32_e32 v151, v100, v119
	v_lshlrev_b32_e32 v146, 16, v105
	v_lshlrev_b32_e32 v147, 16, v101
	v_mov_b32_e32 v118, v28
	v_mov_b32_e32 v119, v32
	v_addc_co_u32_e32 v43, vcc, -1, v41, vcc
	v_pk_mul_f32 v[146:147], v[118:119], v[146:147]
	v_add_co_u32_e32 v46, vcc, s95, v40
	v_add_f32_e32 v100, v20, v146
	s_nop 0
	v_addc_co_u32_e32 v47, vcc, -1, v41, vcc
	global_load_dwordx4 v[62:65], v[42:43], off
	global_load_dwordx4 v[66:69], v[46:47], off
	global_load_dwordx4 v[74:77], v[44:45], off
	global_load_dwordx4 v[54:57], v[40:41], off
	v_lshl_add_u64 v[44:45], v[152:153], 0, v[38:39]
	v_add_f32_e32 v152, v100, v147
	v_and_b32_e32 v147, 0xffff0000, v101
	v_and_b32_e32 v146, 0xffff0000, v105
	v_mov_b32_e32 v100, v29
	v_mov_b32_e32 v101, v33
	v_pk_mul_f32 v[104:105], v[100:101], v[146:147]
	v_lshlrev_b32_e32 v146, 16, v94
	v_add_f32_e32 v104, v21, v104
	v_add_f32_e32 v153, v104, v105
	v_mov_b32_e32 v104, v10
	v_mov_b32_e32 v105, v90
	v_add_co_u32_e32 v42, vcc, s96, v40
	s_add_u32 s16, s82, s50
	s_nop 0
	v_addc_co_u32_e32 v43, vcc, -1, v41, vcc
	s_waitcnt vmcnt(5)
	v_lshlrev_b32_e32 v147, 16, v122
	v_pk_mul_f32 v[146:147], v[104:105], v[146:147]
	v_add_co_u32_e32 v38, vcc, s94, v44
	v_add_f32_e32 v10, v34, v146
	v_add_f32_e32 v34, v10, v147
	v_and_b32_e32 v147, 0xffff0000, v94
	v_and_b32_e32 v146, 0xffff0000, v122
	v_mov_b32_e32 v10, v91
	v_pk_mul_f32 v[90:91], v[10:11], v[146:147]
	v_lshlrev_b32_e32 v147, 16, v95
	v_add_f32_e32 v91, v143, v91
	v_add_f32_e32 v122, v90, v91
	v_lshlrev_b32_e32 v146, 16, v123
	v_mov_b32_e32 v90, v92
	v_mov_b32_e32 v91, v12
	v_pk_mul_f32 v[146:147], v[90:91], v[146:147]
	v_and_b32_e32 v95, 0xffff0000, v95
	v_add_f32_e32 v12, v148, v147
	v_add_f32_e32 v143, v146, v12
	v_and_b32_e32 v94, 0xffff0000, v123
	v_mov_b32_e32 v12, v93
	v_pk_mul_f32 v[92:93], v[12:13], v[94:95]
	v_lshlrev_b32_e32 v95, 16, v96
	v_add_f32_e32 v93, v149, v93
	v_add_f32_e32 v123, v92, v93
	v_lshlrev_b32_e32 v94, 16, v124
	v_mov_b32_e32 v92, v86
	v_mov_b32_e32 v93, v6
	v_pk_mul_f32 v[94:95], v[92:93], v[94:95]
	v_addc_co_u32_e32 v39, vcc, -1, v45, vcc
	v_add_f32_e32 v6, v150, v95
	v_add_f32_e32 v146, v94, v6
	v_and_b32_e32 v95, 0xffff0000, v96
	v_and_b32_e32 v94, 0xffff0000, v124
	v_mov_b32_e32 v6, v87
	v_pk_mul_f32 v[86:87], v[6:7], v[94:95]
	v_lshlrev_b32_e32 v95, 16, v97
	v_add_f32_e32 v87, v151, v87
	v_add_f32_e32 v96, v86, v87
	v_lshlrev_b32_e32 v94, 16, v125
	v_mov_b32_e32 v86, v88
	v_mov_b32_e32 v87, v8
	v_pk_mul_f32 v[94:95], v[86:87], v[94:95]
	v_mul_f32_e32 v88, 0xbfb8aa3b, v34
	v_add_f32_e32 v8, v152, v95
	v_add_f32_e32 v124, v94, v8
	v_and_b32_e32 v95, 0xffff0000, v97
	v_and_b32_e32 v94, 0xffff0000, v125
	v_mov_b32_e32 v8, v89
	v_exp_f32_e32 v97, v88
	v_pk_mul_f32 v[88:89], v[8:9], v[94:95]
	v_mul_f32_e32 v94, 0xbfb8aa3b, v122
	v_mul_f32_e32 v95, 0xbfb8aa3b, v143
	v_exp_f32_e32 v94, v94
	v_exp_f32_e32 v95, v95
	v_add_f32_e32 v89, v153, v89
	v_add_f32_e32 v88, v88, v89
	v_add_f32_e32 v89, 1.0, v97
	v_add_f32_e32 v94, 1.0, v94
	v_add_f32_e32 v95, 1.0, v95
	v_mul_f32_e32 v97, 0xbfb8aa3b, v123
	v_rcp_f32_e32 v89, v89
	v_rcp_f32_e32 v94, v94
	v_rcp_f32_e32 v95, v95
	v_exp_f32_e32 v97, v97
	v_mul_f32_e32 v34, v34, v89
	v_mul_f32_e32 v89, v122, v94
	v_mul_f32_e32 v94, v143, v95
	v_add_f32_e32 v95, 1.0, v97
	v_mul_f32_e32 v97, 0xbfb8aa3b, v146
	v_mul_f32_e32 v122, 0xbfb8aa3b, v96
	v_rcp_f32_e32 v95, v95
	v_exp_f32_e32 v97, v97
	v_exp_f32_e32 v122, v122
	v_mul_f32_e32 v125, 0xbfb8aa3b, v88
	v_mul_f32_e32 v123, v123, v95
	v_add_f32_e32 v95, 1.0, v97
	v_add_f32_e32 v97, 1.0, v122
	v_mul_f32_e32 v122, 0xbfb8aa3b, v124
	v_exp_f32_e32 v122, v122
	v_exp_f32_e32 v125, v125
	v_rcp_f32_e32 v95, v95
	v_add_co_u32_e32 v40, vcc, s95, v44
	v_add_f32_e32 v122, 1.0, v122
	v_rcp_f32_e32 v122, v122
	v_add_f32_e32 v125, 1.0, v125
	v_rcp_f32_e32 v97, v97
	v_rcp_f32_e32 v125, v125
	v_addc_co_u32_e32 v41, vcc, -1, v45, vcc
	global_load_dwordx4 v[46:49], v[38:39], off
	global_load_dwordx4 v[50:53], v[40:41], off
	v_add_co_u32_e32 v38, vcc, s96, v44
	s_addc_u32 s17, s83, 0
	v_mul_f32_e32 v143, v146, v95
	v_addc_co_u32_e32 v39, vcc, -1, v45, vcc
	v_mul_f32_e32 v124, v124, v122
	v_mul_f32_e32 v122, 0x3db504f3, v89
	v_mul_f32_e32 v89, 0x3db504f3, v143
	v_lshl_add_u64 v[120:121], s[16:17], 0, v[120:121]
	v_mov_b32_e32 v143, v129
	global_load_dwordx4 v[38:41], v[38:39], off
	s_nop 0
	global_load_dwordx4 v[58:61], v[42:43], off
	s_nop 0
	global_load_dwordx4 v[42:45], v[44:45], off
	v_mul_f32_e32 v146, v96, v97
	v_mul_f32_e32 v88, v88, v125
	v_mul_f32_e32 v97, 0x3db504f3, v34
	v_mul_f32_e32 v34, 0x3db504f3, v124
	v_lshl_add_u64 v[124:125], v[120:121], 0, v[142:143]
	ds_read_b32 v120, v131
	v_mul_f32_e32 v88, 0x3db504f3, v88
	v_mul_f32_e32 v95, 0x3db504f3, v94
	v_mul_f32_e32 v94, 0x3db504f3, v146
	v_cvt_pk_bf16_f32 v148, v89, v94
	v_cvt_pk_bf16_f32 v149, v34, v88
	s_waitcnt lgkmcnt(0)
	v_mul_f32_e32 v89, v89, v120
	v_mul_f32_e32 v88, v88, v120
	v_mul_f32_e32 v96, 0x3db504f3, v123
	v_cvt_pk_bf16_f32 v146, v97, v122
	v_cvt_pk_bf16_f32 v147, v95, v96
	global_store_dwordx4 v[124:125], v[146:149], off sc1
	v_mul_f32_e32 v94, v94, v120
	v_cvt_pk_bf16_f32 v124, v89, v94
	v_mul_f32_e32 v34, v34, v120
	v_cvt_pk_bf16_f32 v125, v34, v88
	v_lshlrev_b32_e32 v89, 16, v82
	v_lshlrev_b32_e32 v88, 16, v78
	v_pk_mul_f32 v[88:89], v[112:113], v[88:89]
	ds_read_b32 v121, v133
	ds_read_b32 v146, v135
	ds_read_b32 v147, v145
	v_add_f32_e32 v34, v22, v88
	v_add_f32_e32 v34, v34, v89
	v_and_b32_e32 v89, 0xffff0000, v82
	v_and_b32_e32 v88, 0xffff0000, v78
	v_pk_mul_f32 v[88:89], v[14:15], v[88:89]
	v_and_b32_e32 v82, 0xffff0000, v79
	v_add_f32_e32 v78, v23, v88
	v_add_f32_e32 v94, v78, v89
	v_lshlrev_b32_e32 v89, 16, v83
	v_lshlrev_b32_e32 v88, 16, v79
	v_pk_mul_f32 v[88:89], v[114:115], v[88:89]
	v_and_b32_e32 v83, 0xffff0000, v83
	v_add_f32_e32 v78, v24, v88
	v_add_f32_e32 v88, v78, v89
	v_pk_mul_f32 v[78:79], v[98:99], v[82:83]
	v_mul_f32_e32 v122, v122, v120
	v_add_f32_e32 v78, v25, v78
	v_add_f32_e32 v82, v78, v79
	v_lshlrev_b32_e32 v79, 16, v84
	v_lshlrev_b32_e32 v78, 16, v80
	v_pk_mul_f32 v[78:79], v[102:103], v[78:79]
	v_mul_f32_e32 v97, v97, v120
	v_add_f32_e32 v78, v18, v78
	v_add_f32_e32 v83, v78, v79
	v_and_b32_e32 v79, 0xffff0000, v84
	v_and_b32_e32 v78, 0xffff0000, v80
	v_pk_mul_f32 v[78:79], v[116:117], v[78:79]
	v_cvt_pk_bf16_f32 v122, v97, v122
	v_mul_f32_e32 v95, v95, v120
	v_add_f32_e32 v78, v19, v78
	v_add_f32_e32 v80, v78, v79
	v_lshlrev_b32_e32 v79, 16, v85
	v_lshlrev_b32_e32 v78, 16, v81
	v_pk_mul_f32 v[78:79], v[118:119], v[78:79]
	v_mul_f32_e32 v96, v96, v120
	v_add_f32_e32 v78, v20, v78
	v_add_f32_e32 v84, v78, v79
	v_and_b32_e32 v79, 0xffff0000, v85
	v_and_b32_e32 v78, 0xffff0000, v81
	v_pk_mul_f32 v[78:79], v[100:101], v[78:79]
	v_cvt_pk_bf16_f32 v123, v95, v96
	ds_write_b128 v242, v[122:125] offset:32768
	v_add_f32_e32 v78, v21, v78
	v_add_f32_e32 v81, v78, v79
	s_waitcnt vmcnt(7)
	v_lshlrev_b32_e32 v78, 16, v74
	v_lshlrev_b32_e32 v79, 16, v70
	v_pk_mul_f32 v[78:79], v[104:105], v[78:79]
	s_nop 0
	v_add_f32_e32 v34, v34, v78
	v_add_f32_e32 v34, v34, v79
	v_and_b32_e32 v79, 0xffff0000, v74
	v_and_b32_e32 v78, 0xffff0000, v70
	v_pk_mul_f32 v[78:79], v[10:11], v[78:79]
	v_and_b32_e32 v74, 0xffff0000, v71
	v_add_f32_e32 v70, v94, v79
	v_add_f32_e32 v85, v78, v70
	v_lshlrev_b32_e32 v79, 16, v75
	v_lshlrev_b32_e32 v78, 16, v71
	v_pk_mul_f32 v[78:79], v[90:91], v[78:79]
	v_and_b32_e32 v75, 0xffff0000, v75
	v_add_f32_e32 v70, v88, v79
	v_add_f32_e32 v78, v78, v70
	v_pk_mul_f32 v[70:71], v[12:13], v[74:75]
	s_nop 0
	v_add_f32_e32 v71, v82, v71
	v_add_f32_e32 v74, v70, v71
	v_lshlrev_b32_e32 v71, 16, v76
	v_lshlrev_b32_e32 v70, 16, v72
	v_pk_mul_f32 v[70:71], v[92:93], v[70:71]
	v_mul_f32_e32 v79, 0xbfb8aa3b, v74
	v_add_f32_e32 v71, v83, v71
	v_add_f32_e32 v75, v70, v71
	v_and_b32_e32 v71, 0xffff0000, v76
	v_and_b32_e32 v70, 0xffff0000, v72
	v_pk_mul_f32 v[70:71], v[6:7], v[70:71]
	v_exp_f32_e32 v79, v79
	v_add_f32_e32 v71, v80, v71
	v_add_f32_e32 v72, v70, v71
	v_lshlrev_b32_e32 v71, 16, v77
	v_lshlrev_b32_e32 v70, 16, v73
	v_pk_mul_f32 v[70:71], v[86:87], v[70:71]
	s_nop 0
	v_add_f32_e32 v71, v84, v71
	v_add_f32_e32 v76, v70, v71
	v_and_b32_e32 v70, 0xffff0000, v73
	v_mul_f32_e32 v73, 0xbfb8aa3b, v34
	v_exp_f32_e32 v73, v73
	v_and_b32_e32 v71, 0xffff0000, v77
	v_pk_mul_f32 v[70:71], v[8:9], v[70:71]
	v_mul_f32_e32 v77, 0xbfb8aa3b, v78
	v_add_f32_e32 v71, v81, v71
	v_add_f32_e32 v70, v70, v71
	v_add_f32_e32 v71, 1.0, v73
	v_mul_f32_e32 v73, 0xbfb8aa3b, v85
	v_exp_f32_e32 v73, v73
	v_exp_f32_e32 v77, v77
	v_rcp_f32_e32 v71, v71
	v_mul_f32_e32 v80, 0xbfb8aa3b, v70
	v_add_f32_e32 v73, 1.0, v73
	v_add_f32_e32 v77, 1.0, v77
	v_rcp_f32_e32 v73, v73
	v_rcp_f32_e32 v77, v77
	v_mul_f32_e32 v34, v34, v71
	v_exp_f32_e32 v80, v80
	v_mul_f32_e32 v71, v85, v73
	v_mul_f32_e32 v73, v78, v77
	v_add_f32_e32 v77, 1.0, v79
	v_mul_f32_e32 v78, 0xbfb8aa3b, v75
	v_mul_f32_e32 v79, 0xbfb8aa3b, v72
	v_rcp_f32_e32 v77, v77
	v_exp_f32_e32 v78, v78
	v_exp_f32_e32 v79, v79
	v_add_f32_e32 v80, 1.0, v80
	v_mul_f32_e32 v74, v74, v77
	v_add_f32_e32 v77, 1.0, v78
	v_add_f32_e32 v78, 1.0, v79
	v_mul_f32_e32 v79, 0xbfb8aa3b, v76
	v_exp_f32_e32 v79, v79
	v_rcp_f32_e32 v77, v77
	v_rcp_f32_e32 v80, v80
	v_rcp_f32_e32 v78, v78
	v_add_f32_e32 v79, 1.0, v79
	v_rcp_f32_e32 v79, v79
	v_mul_f32_e32 v75, v75, v77
	v_mul_f32_e32 v70, v70, v80
	v_mul_f32_e32 v80, 0x3db504f3, v75
	v_mul_f32_e32 v76, v76, v79
	v_mul_f32_e32 v79, 0x3db504f3, v74
	v_lshl_add_u64 v[74:75], s[16:17], 0, v[106:107]
	v_mul_f32_e32 v72, v72, v78
	v_mul_f32_e32 v34, 0x3db504f3, v34
	v_mul_f32_e32 v77, 0x3db504f3, v71
	v_mul_f32_e32 v82, 0x3db504f3, v70
	v_cvt_pk_bf16_f32 v70, v34, v77
	v_lshl_add_u64 v[74:75], v[74:75], 0, v[142:143]
	v_mul_f32_e32 v78, 0x3db504f3, v73
	v_mul_f32_e32 v81, 0x3db504f3, v72
	v_mul_f32_e32 v76, 0x3db504f3, v76
	v_cvt_pk_bf16_f32 v71, v78, v79
	v_cvt_pk_bf16_f32 v72, v80, v81
	v_cvt_pk_bf16_f32 v73, v76, v82
	global_store_dwordx4 v[74:75], v[70:73], off sc1
	s_waitcnt lgkmcnt(3)
	v_mul_f32_e32 v34, v34, v121
	v_mul_f32_e32 v70, v77, v121
	v_cvt_pk_bf16_f32 v70, v34, v70
	v_mul_f32_e32 v34, v78, v121
	v_mul_f32_e32 v71, v79, v121
	v_cvt_pk_bf16_f32 v71, v34, v71
	v_mul_f32_e32 v34, v80, v121
	v_mul_f32_e32 v72, v81, v121
	v_mul_f32_e32 v73, v82, v121
	v_cvt_pk_bf16_f32 v72, v34, v72
	v_mul_f32_e32 v34, v76, v121
	v_cvt_pk_bf16_f32 v73, v34, v73
	ds_write_b128 v243, v[70:73] offset:32768
	v_lshlrev_b32_e32 v71, 16, v66
	v_lshlrev_b32_e32 v70, 16, v62
	v_pk_mul_f32 v[70:71], v[112:113], v[70:71]
	s_nop 0
	v_add_f32_e32 v34, v22, v70
	v_add_f32_e32 v72, v34, v71
	v_and_b32_e32 v71, 0xffff0000, v62
	v_and_b32_e32 v70, 0xffff0000, v66
	v_mov_b32_e32 v34, v15
	v_pk_mul_f32 v[34:35], v[34:35], v[70:71]
	v_mov_b32_e32 v70, v16
	v_add_f32_e32 v35, v23, v35
	v_add_f32_e32 v62, v34, v35
	v_lshlrev_b32_e32 v35, 16, v63
	v_lshlrev_b32_e32 v34, 16, v67
	v_mov_b32_e32 v71, v36
	v_pk_mul_f32 v[34:35], v[70:71], v[34:35]
	v_mov_b32_e32 v36, v17
	v_add_f32_e32 v16, v24, v35
	v_add_f32_e32 v66, v34, v16
	v_and_b32_e32 v35, 0xffff0000, v63
	v_and_b32_e32 v34, 0xffff0000, v67
	v_pk_mul_f32 v[16:17], v[36:37], v[34:35]
	v_mov_b32_e32 v34, v30
	v_add_f32_e32 v17, v25, v17
	v_add_f32_e32 v36, v16, v17
	v_lshlrev_b32_e32 v17, 16, v64
	v_lshlrev_b32_e32 v16, 16, v68
	v_mov_b32_e32 v35, v26
	v_pk_mul_f32 v[16:17], v[34:35], v[16:17]
	v_mov_b32_e32 v26, v31
	v_add_f32_e32 v17, v18, v17
	v_add_f32_e32 v30, v16, v17
	v_and_b32_e32 v17, 0xffff0000, v64
	v_and_b32_e32 v16, 0xffff0000, v68
	v_pk_mul_f32 v[16:17], v[26:27], v[16:17]
	v_mov_b32_e32 v26, v32
	v_add_f32_e32 v17, v19, v17
	v_add_f32_e32 v31, v16, v17
	v_lshlrev_b32_e32 v17, 16, v65
	v_lshlrev_b32_e32 v16, 16, v69
	v_mov_b32_e32 v27, v28
	v_pk_mul_f32 v[16:17], v[26:27], v[16:17]
	v_mov_b32_e32 v28, v33
	v_add_f32_e32 v17, v20, v17
	v_add_f32_e32 v26, v16, v17
	v_and_b32_e32 v17, 0xffff0000, v65
	v_and_b32_e32 v16, 0xffff0000, v69
	v_pk_mul_f32 v[16:17], v[28:29], v[16:17]
	s_nop 0
	v_add_f32_e32 v17, v21, v17
	v_add_f32_e32 v27, v16, v17
	s_waitcnt vmcnt(3)
	v_lshlrev_b32_e32 v16, 16, v58
	v_lshlrev_b32_e32 v17, 16, v54
	v_pk_mul_f32 v[16:17], v[104:105], v[16:17]
	s_nop 0
	v_add_f32_e32 v16, v72, v16
	v_add_f32_e32 v28, v16, v17
	v_and_b32_e32 v17, 0xffff0000, v58
	v_and_b32_e32 v16, 0xffff0000, v54
	v_pk_mul_f32 v[16:17], v[10:11], v[16:17]
	v_mul_f32_e32 v34, 0xbfb8aa3b, v28
	v_add_f32_e32 v17, v17, v62
	v_add_f32_e32 v29, v16, v17
	v_lshlrev_b32_e32 v17, 16, v59
	v_lshlrev_b32_e32 v16, 16, v55
	v_pk_mul_f32 v[16:17], v[90:91], v[16:17]
	v_exp_f32_e32 v34, v34
	v_add_f32_e32 v17, v17, v66
	v_add_f32_e32 v32, v16, v17
	v_and_b32_e32 v17, 0xffff0000, v59
	v_and_b32_e32 v16, 0xffff0000, v55
	v_pk_mul_f32 v[16:17], v[12:13], v[16:17]
	s_nop 0
	v_add_f32_e32 v17, v17, v36
	v_add_f32_e32 v33, v16, v17
	v_lshlrev_b32_e32 v17, 16, v60
	v_lshlrev_b32_e32 v16, 16, v56
	v_pk_mul_f32 v[16:17], v[92:93], v[16:17]
	v_mul_f32_e32 v35, 0xbfb8aa3b, v33
	v_add_f32_e32 v17, v17, v30
	v_add_f32_e32 v30, v16, v17
	v_and_b32_e32 v17, 0xffff0000, v60
	v_and_b32_e32 v16, 0xffff0000, v56
	v_pk_mul_f32 v[16:17], v[6:7], v[16:17]
	v_exp_f32_e32 v35, v35
	v_add_f32_e32 v17, v17, v31
	v_add_f32_e32 v31, v16, v17
	v_lshlrev_b32_e32 v17, 16, v61
	v_lshlrev_b32_e32 v16, 16, v57
	v_pk_mul_f32 v[16:17], v[86:87], v[16:17]
	s_nop 0
	v_add_f32_e32 v17, v17, v26
	v_add_f32_e32 v26, v16, v17
	v_and_b32_e32 v17, 0xffff0000, v61
	v_and_b32_e32 v16, 0xffff0000, v57
	v_pk_mul_f32 v[16:17], v[8:9], v[16:17]
	s_nop 0
	v_add_f32_e32 v17, v17, v27
	v_add_f32_e32 v16, v16, v17
	v_add_f32_e32 v17, 1.0, v34
	v_mul_f32_e32 v27, 0xbfb8aa3b, v29
	v_mul_f32_e32 v34, 0xbfb8aa3b, v32
	v_exp_f32_e32 v27, v27
	v_exp_f32_e32 v34, v34
	v_rcp_f32_e32 v17, v17
	v_add_f32_e32 v27, 1.0, v27
	v_add_f32_e32 v34, 1.0, v34
	v_rcp_f32_e32 v27, v27
	v_rcp_f32_e32 v34, v34
	v_mul_f32_e32 v17, v28, v17
	v_mul_f32_e32 v27, v29, v27
	v_mul_f32_e32 v28, v32, v34
	v_add_f32_e32 v29, 1.0, v35
	v_mul_f32_e32 v34, 0xbfb8aa3b, v31
	v_rcp_f32_e32 v29, v29
	v_exp_f32_e32 v34, v34
	v_mul_f32_e32 v35, 0xbfb8aa3b, v16
	v_mul_f32_e32 v32, 0xbfb8aa3b, v30
	v_exp_f32_e32 v35, v35
	v_exp_f32_e32 v32, v32
	v_mul_f32_e32 v29, v33, v29
	v_add_f32_e32 v33, 1.0, v34
	v_mul_f32_e32 v34, 0xbfb8aa3b, v26
	v_exp_f32_e32 v34, v34
	v_add_f32_e32 v35, 1.0, v35
	v_add_f32_e32 v32, 1.0, v32
	v_rcp_f32_e32 v35, v35
	v_rcp_f32_e32 v32, v32
	v_add_f32_e32 v34, 1.0, v34
	v_rcp_f32_e32 v33, v33
	v_rcp_f32_e32 v34, v34
	v_mul_f32_e32 v16, v16, v35
	v_mul_f32_e32 v30, v30, v32
	v_mul_f32_e32 v32, 0x3db504f3, v17
	v_mul_f32_e32 v37, 0x3db504f3, v16
	v_lshl_add_u64 v[16:17], s[16:17], 0, v[108:109]
	v_mul_f32_e32 v31, v31, v33
	v_mul_f32_e32 v26, v26, v34
	v_mul_f32_e32 v33, 0x3db504f3, v27
	v_lshl_add_u64 v[16:17], v[16:17], 0, v[142:143]
	v_mul_f32_e32 v34, 0x3db504f3, v28
	v_mul_f32_e32 v35, 0x3db504f3, v29
	v_mul_f32_e32 v30, 0x3db504f3, v30
	v_mul_f32_e32 v31, 0x3db504f3, v31
	v_mul_f32_e32 v36, 0x3db504f3, v26
	v_cvt_pk_bf16_f32 v26, v32, v33
	v_cvt_pk_bf16_f32 v27, v34, v35
	v_cvt_pk_bf16_f32 v28, v30, v31
	v_cvt_pk_bf16_f32 v29, v36, v37
	global_store_dwordx4 v[16:17], v[26:29], off sc1
	s_waitcnt lgkmcnt(3)
	v_mul_f32_e32 v16, v32, v146
	v_mul_f32_e32 v17, v33, v146
	v_cvt_pk_bf16_f32 v26, v16, v17
	v_mul_f32_e32 v16, v34, v146
	v_mul_f32_e32 v17, v35, v146
	v_cvt_pk_bf16_f32 v27, v16, v17
	v_mul_f32_e32 v16, v30, v146
	v_mul_f32_e32 v17, v31, v146
	v_cvt_pk_bf16_f32 v28, v16, v17
	v_mul_f32_e32 v16, v36, v146
	v_mul_f32_e32 v17, v37, v146
	v_cvt_pk_bf16_f32 v29, v16, v17
	v_lshlrev_b32_e32 v17, 16, v50
	v_lshlrev_b32_e32 v16, 16, v46
	v_pk_mul_f32 v[16:17], v[112:113], v[16:17]
	ds_write_b128 v244, v[26:29] offset:32768
	v_add_f32_e32 v16, v22, v16
	v_add_f32_e32 v22, v16, v17
	v_and_b32_e32 v17, 0xffff0000, v50
	v_and_b32_e32 v16, 0xffff0000, v46
	v_pk_mul_f32 v[14:15], v[14:15], v[16:17]
	s_nop 0
	v_add_f32_e32 v14, v23, v14
	v_add_f32_e32 v16, v14, v15
	v_lshlrev_b32_e32 v15, 16, v51
	v_lshlrev_b32_e32 v14, 16, v47
	v_pk_mul_f32 v[14:15], v[114:115], v[14:15]
	s_nop 0
	v_add_f32_e32 v14, v24, v14
	v_add_f32_e32 v17, v14, v15
	v_and_b32_e32 v15, 0xffff0000, v51
	v_and_b32_e32 v14, 0xffff0000, v47
	v_pk_mul_f32 v[14:15], v[98:99], v[14:15]
	s_nop 0
	v_add_f32_e32 v14, v25, v14
	v_add_f32_e32 v23, v14, v15
	v_lshlrev_b32_e32 v15, 16, v52
	v_lshlrev_b32_e32 v14, 16, v48
	v_pk_mul_f32 v[14:15], v[102:103], v[14:15]
	s_nop 0
	v_add_f32_e32 v14, v18, v14
	v_add_f32_e32 v18, v14, v15
	v_and_b32_e32 v15, 0xffff0000, v52
	v_and_b32_e32 v14, 0xffff0000, v48
	v_pk_mul_f32 v[14:15], v[116:117], v[14:15]
	s_nop 0
	v_add_f32_e32 v14, v19, v14
	v_add_f32_e32 v19, v14, v15
	v_lshlrev_b32_e32 v15, 16, v53
	v_lshlrev_b32_e32 v14, 16, v49
	v_pk_mul_f32 v[14:15], v[118:119], v[14:15]
	s_nop 0
	v_add_f32_e32 v14, v20, v14
	v_add_f32_e32 v20, v14, v15
	v_and_b32_e32 v15, 0xffff0000, v53
	v_and_b32_e32 v14, 0xffff0000, v49
	v_pk_mul_f32 v[14:15], v[100:101], v[14:15]
	s_nop 0
	v_add_f32_e32 v14, v21, v14
	v_add_f32_e32 v21, v14, v15
	v_lshlrev_b32_e32 v14, 16, v38
	s_waitcnt vmcnt(3)
	v_lshlrev_b32_e32 v15, 16, v42
	v_pk_mul_f32 v[14:15], v[104:105], v[14:15]
	s_nop 0
	v_add_f32_e32 v14, v22, v14
	v_add_f32_e32 v22, v14, v15
	v_and_b32_e32 v15, 0xffff0000, v38
	v_and_b32_e32 v14, 0xffff0000, v42
	v_pk_mul_f32 v[10:11], v[10:11], v[14:15]
	s_nop 0
	v_add_f32_e32 v11, v16, v11
	v_add_f32_e32 v14, v10, v11
	v_lshlrev_b32_e32 v11, 16, v39
	v_lshlrev_b32_e32 v10, 16, v43
	v_pk_mul_f32 v[10:11], v[90:91], v[10:11]
	v_mul_f32_e32 v16, 0xbfb8aa3b, v22
	v_add_f32_e32 v11, v17, v11
	v_add_f32_e32 v15, v10, v11
	v_and_b32_e32 v11, 0xffff0000, v39
	v_and_b32_e32 v10, 0xffff0000, v43
	v_pk_mul_f32 v[10:11], v[12:13], v[10:11]
	v_exp_f32_e32 v16, v16
	v_add_f32_e32 v11, v23, v11
	v_add_f32_e32 v12, v10, v11
	v_lshlrev_b32_e32 v11, 16, v40
	v_lshlrev_b32_e32 v10, 16, v44
	v_pk_mul_f32 v[10:11], v[92:93], v[10:11]
	s_nop 0
	v_add_f32_e32 v11, v18, v11
	v_add_f32_e32 v13, v10, v11
	v_and_b32_e32 v11, 0xffff0000, v40
	v_and_b32_e32 v10, 0xffff0000, v44
	v_pk_mul_f32 v[6:7], v[6:7], v[10:11]
	s_nop 0
	v_add_f32_e32 v7, v19, v7
	v_add_f32_e32 v10, v6, v7
	v_lshlrev_b32_e32 v7, 16, v41
	v_lshlrev_b32_e32 v6, 16, v45
	v_pk_mul_f32 v[6:7], v[86:87], v[6:7]
	s_nop 0
	v_add_f32_e32 v7, v20, v7
	v_add_f32_e32 v11, v6, v7
	v_and_b32_e32 v7, 0xffff0000, v41
	v_and_b32_e32 v6, 0xffff0000, v45
	v_pk_mul_f32 v[6:7], v[8:9], v[6:7]
	v_mul_f32_e32 v8, 0xbfb8aa3b, v14
	v_mul_f32_e32 v9, 0xbfb8aa3b, v15
	v_exp_f32_e32 v8, v8
	v_exp_f32_e32 v9, v9
	v_add_f32_e32 v7, v21, v7
	v_add_f32_e32 v6, v6, v7
	v_add_f32_e32 v7, 1.0, v16
	v_add_f32_e32 v8, 1.0, v8
	v_add_f32_e32 v9, 1.0, v9
	v_mul_f32_e32 v16, 0xbfb8aa3b, v12
	v_rcp_f32_e32 v8, v8
	v_rcp_f32_e32 v9, v9
	v_exp_f32_e32 v16, v16
	v_mul_f32_e32 v17, 0xbfb8aa3b, v6
	v_mul_f32_e32 v8, v14, v8
	v_mul_f32_e32 v9, v15, v9
	v_add_f32_e32 v14, 1.0, v16
	v_mul_f32_e32 v15, 0xbfb8aa3b, v13
	v_mul_f32_e32 v16, 0xbfb8aa3b, v10
	v_rcp_f32_e32 v14, v14
	v_exp_f32_e32 v15, v15
	v_exp_f32_e32 v16, v16
	v_exp_f32_e32 v17, v17
	v_mul_f32_e32 v12, v12, v14
	v_add_f32_e32 v14, 1.0, v15
	v_add_f32_e32 v15, 1.0, v16
	v_mul_f32_e32 v16, 0xbfb8aa3b, v11
	v_exp_f32_e32 v16, v16
	v_rcp_f32_e32 v15, v15
	v_add_f32_e32 v17, 1.0, v17
	v_rcp_f32_e32 v7, v7
	v_add_f32_e32 v16, 1.0, v16
	v_rcp_f32_e32 v16, v16
	v_rcp_f32_e32 v17, v17
	v_rcp_f32_e32 v14, v14
	v_mul_f32_e32 v10, v10, v15
	v_mul_f32_e32 v11, v11, v16
	v_mul_f32_e32 v7, v22, v7
	v_mul_f32_e32 v6, v6, v17
	v_mul_f32_e32 v17, 0x3db504f3, v10
	v_mul_f32_e32 v18, 0x3db504f3, v11
	v_lshl_add_u64 v[10:11], s[16:17], 0, v[110:111]
	v_mul_f32_e32 v13, v13, v14
	v_mul_f32_e32 v14, 0x3db504f3, v7
	v_mul_f32_e32 v15, 0x3db504f3, v8
	v_mul_f32_e32 v16, 0x3db504f3, v9
	v_mul_f32_e32 v12, 0x3db504f3, v12
	v_mul_f32_e32 v19, 0x3db504f3, v6
	v_cvt_pk_bf16_f32 v6, v14, v15
	v_cvt_pk_bf16_f32 v7, v16, v12
	v_lshl_add_u64 v[10:11], v[10:11], 0, v[142:143]
	v_mul_f32_e32 v13, 0x3db504f3, v13
	v_cvt_pk_bf16_f32 v8, v13, v17
	v_cvt_pk_bf16_f32 v9, v18, v19
	global_store_dwordx4 v[10:11], v[6:9], off sc1
	s_waitcnt lgkmcnt(3)
	v_mul_f32_e32 v10, v19, v147
	v_mul_f32_e32 v6, v14, v147
	v_mul_f32_e32 v7, v15, v147
	v_cvt_pk_bf16_f32 v6, v6, v7
	v_mul_f32_e32 v7, v16, v147
	v_mul_f32_e32 v8, v12, v147
	v_cvt_pk_bf16_f32 v7, v7, v8
	v_mul_f32_e32 v8, v13, v147
	v_mul_f32_e32 v9, v17, v147
	v_cvt_pk_bf16_f32 v8, v8, v9
	v_mul_f32_e32 v9, v18, v147
	v_cvt_pk_bf16_f32 v9, v9, v10
	ds_write_b128 v245, v[6:9] offset:32768
	s_waitcnt lgkmcnt(0)
	s_barrier
	ds_read_b64_tr_b16 v[6:7], v174
	ds_read_b64_tr_b16 v[10:11], v174 offset:8192
	ds_read_b64_tr_b16 v[14:15], v174 offset:16384
	ds_read_b64_tr_b16 v[18:19], v174 offset:24576
	ds_read_b64_tr_b16 v[8:9], v175
	ds_read_b64_tr_b16 v[12:13], v176
	ds_read_b64_tr_b16 v[16:17], v177
	ds_read_b64_tr_b16 v[20:21], v178
	ds_read_b64_tr_b16 v[22:23], v179 offset:32768
	ds_read_b64_tr_b16 v[26:27], v179 offset:40960
	ds_read_b64_tr_b16 v[30:31], v179 offset:49152
	ds_read_b64_tr_b16 v[34:35], v179 offset:57344
	ds_read_b64_tr_b16 v[24:25], v180 offset:32768
	ds_read_b64_tr_b16 v[28:29], v181 offset:32768
	ds_read_b64_tr_b16 v[32:33], v182 offset:32768
	ds_read_b64_tr_b16 v[36:37], v183 offset:32768
	ds_read_b64_tr_b16 v[38:39], v184 offset:32768
	ds_read_b64_tr_b16 v[42:43], v184 offset:40960
	ds_read_b64_tr_b16 v[46:47], v184 offset:49152
	ds_read_b64_tr_b16 v[50:51], v184 offset:57344
	ds_read_b64_tr_b16 v[40:41], v185 offset:32768
	ds_read_b64_tr_b16 v[44:45], v186 offset:32768
	ds_read_b64_tr_b16 v[48:49], v187 offset:32768
	ds_read_b64_tr_b16 v[52:53], v188 offset:32768
	s_waitcnt lgkmcnt(11)
	v_mfma_f32_16x16x32_bf16 v[22:25], v[22:25], v[6:9], 0
	s_waitcnt lgkmcnt(10)
	v_mfma_f32_16x16x32_bf16 v[22:25], v[26:29], v[10:13], v[22:25]
	s_waitcnt lgkmcnt(9)
	v_mfma_f32_16x16x32_bf16 v[22:25], v[30:33], v[14:17], v[22:25]
	s_waitcnt lgkmcnt(8)
	v_mfma_f32_16x16x32_bf16 v[22:25], v[34:37], v[18:21], v[22:25]
	s_nop 7
	global_store_dwordx4 v[140:141], v[22:25], off offset:-256 sc1
	ds_read_b64_tr_b16 v[22:23], v189 offset:32768
	ds_read_b64_tr_b16 v[26:27], v189 offset:40960
	ds_read_b64_tr_b16 v[30:31], v189 offset:49152
	ds_read_b64_tr_b16 v[34:35], v189 offset:57344
	ds_read_b64_tr_b16 v[24:25], v190 offset:32768
	ds_read_b64_tr_b16 v[28:29], v191 offset:32768
	ds_read_b64_tr_b16 v[32:33], v192 offset:32768
	ds_read_b64_tr_b16 v[36:37], v193 offset:32768
	s_waitcnt lgkmcnt(11)
	v_mfma_f32_16x16x32_bf16 v[38:41], v[38:41], v[6:9], 0
	s_waitcnt lgkmcnt(10)
	v_mfma_f32_16x16x32_bf16 v[38:41], v[42:45], v[10:13], v[38:41]
	s_waitcnt lgkmcnt(9)
	v_mfma_f32_16x16x32_bf16 v[38:41], v[46:49], v[14:17], v[38:41]
	s_waitcnt lgkmcnt(8)
	v_mfma_f32_16x16x32_bf16 v[38:41], v[50:53], v[18:21], v[38:41]
	s_nop 7
	global_store_dwordx4 v[140:141], v[38:41], off offset:-192 sc1
	ds_read_b64_tr_b16 v[38:39], v194 offset:32768
	ds_read_b64_tr_b16 v[42:43], v194 offset:40960
	ds_read_b64_tr_b16 v[46:47], v194 offset:49152
	ds_read_b64_tr_b16 v[50:51], v194 offset:57344
	ds_read_b64_tr_b16 v[40:41], v195 offset:32768
	ds_read_b64_tr_b16 v[44:45], v196 offset:32768
	ds_read_b64_tr_b16 v[48:49], v197 offset:32768
	ds_read_b64_tr_b16 v[52:53], v198 offset:32768
	s_waitcnt lgkmcnt(11)
	v_mfma_f32_16x16x32_bf16 v[22:25], v[22:25], v[6:9], 0
	s_waitcnt lgkmcnt(10)
	v_mfma_f32_16x16x32_bf16 v[22:25], v[26:29], v[10:13], v[22:25]
	s_waitcnt lgkmcnt(9)
	v_mfma_f32_16x16x32_bf16 v[22:25], v[30:33], v[14:17], v[22:25]
	s_waitcnt lgkmcnt(8)
	v_mfma_f32_16x16x32_bf16 v[22:25], v[34:37], v[18:21], v[22:25]
	s_nop 7
	global_store_dwordx4 v[140:141], v[22:25], off offset:-128 sc1
	ds_read_b64_tr_b16 v[22:23], v199 offset:32768
	ds_read_b64_tr_b16 v[26:27], v199 offset:40960
	ds_read_b64_tr_b16 v[30:31], v199 offset:49152
	ds_read_b64_tr_b16 v[34:35], v199 offset:57344
	ds_read_b64_tr_b16 v[24:25], v200 offset:32768
	ds_read_b64_tr_b16 v[28:29], v201 offset:32768
	ds_read_b64_tr_b16 v[32:33], v202 offset:32768
	ds_read_b64_tr_b16 v[36:37], v203 offset:32768
	s_waitcnt lgkmcnt(11)
	v_mfma_f32_16x16x32_bf16 v[38:41], v[38:41], v[6:9], 0
	s_waitcnt lgkmcnt(10)
	v_mfma_f32_16x16x32_bf16 v[38:41], v[42:45], v[10:13], v[38:41]
	s_waitcnt lgkmcnt(9)
	v_mfma_f32_16x16x32_bf16 v[38:41], v[46:49], v[14:17], v[38:41]
	s_waitcnt lgkmcnt(8)
	v_mfma_f32_16x16x32_bf16 v[38:41], v[50:53], v[18:21], v[38:41]
	s_nop 7
	global_store_dwordx4 v[140:141], v[38:41], off offset:-64 sc1
	ds_read_b64_tr_b16 v[38:39], v204 offset:32768
	ds_read_b64_tr_b16 v[42:43], v204 offset:40960
	ds_read_b64_tr_b16 v[46:47], v204 offset:49152
	ds_read_b64_tr_b16 v[50:51], v204 offset:57344
	ds_read_b64_tr_b16 v[40:41], v205 offset:32768
	ds_read_b64_tr_b16 v[44:45], v206 offset:32768
	ds_read_b64_tr_b16 v[48:49], v207 offset:32768
	ds_read_b64_tr_b16 v[52:53], v208 offset:32768
	s_waitcnt lgkmcnt(11)
	v_mfma_f32_16x16x32_bf16 v[22:25], v[22:25], v[6:9], 0
	s_waitcnt lgkmcnt(10)
	v_mfma_f32_16x16x32_bf16 v[22:25], v[26:29], v[10:13], v[22:25]
	s_waitcnt lgkmcnt(9)
	v_mfma_f32_16x16x32_bf16 v[22:25], v[30:33], v[14:17], v[22:25]
	s_waitcnt lgkmcnt(8)
	v_mfma_f32_16x16x32_bf16 v[22:25], v[34:37], v[18:21], v[22:25]
	s_nop 7
	global_store_dwordx4 v[140:141], v[22:25], off sc1
	ds_read_b64_tr_b16 v[22:23], v209 offset:32768
	ds_read_b64_tr_b16 v[26:27], v209 offset:40960
	ds_read_b64_tr_b16 v[30:31], v209 offset:49152
	ds_read_b64_tr_b16 v[34:35], v209 offset:57344
	ds_read_b64_tr_b16 v[24:25], v210 offset:32768
	ds_read_b64_tr_b16 v[28:29], v211 offset:32768
	ds_read_b64_tr_b16 v[32:33], v212 offset:32768
	ds_read_b64_tr_b16 v[36:37], v213 offset:32768
	s_waitcnt lgkmcnt(11)
	v_mfma_f32_16x16x32_bf16 v[38:41], v[38:41], v[6:9], 0
	s_waitcnt lgkmcnt(10)
	v_mfma_f32_16x16x32_bf16 v[38:41], v[42:45], v[10:13], v[38:41]
	s_waitcnt lgkmcnt(9)
	v_mfma_f32_16x16x32_bf16 v[38:41], v[46:49], v[14:17], v[38:41]
	s_waitcnt lgkmcnt(8)
	v_mfma_f32_16x16x32_bf16 v[38:41], v[50:53], v[18:21], v[38:41]
	s_nop 7
	global_store_dwordx4 v[140:141], v[38:41], off offset:64 sc1
	ds_read_b64_tr_b16 v[38:39], v214 offset:32768
	ds_read_b64_tr_b16 v[42:43], v214 offset:40960
	ds_read_b64_tr_b16 v[46:47], v214 offset:49152
	ds_read_b64_tr_b16 v[50:51], v214 offset:57344
	ds_read_b64_tr_b16 v[40:41], v215 offset:32768
	ds_read_b64_tr_b16 v[44:45], v216 offset:32768
	ds_read_b64_tr_b16 v[48:49], v217 offset:32768
	ds_read_b64_tr_b16 v[52:53], v219 offset:32768
	s_waitcnt lgkmcnt(11)
	v_mfma_f32_16x16x32_bf16 v[22:25], v[22:25], v[6:9], 0
	s_waitcnt lgkmcnt(10)
	v_mfma_f32_16x16x32_bf16 v[22:25], v[26:29], v[10:13], v[22:25]
	s_waitcnt lgkmcnt(9)
	v_mfma_f32_16x16x32_bf16 v[22:25], v[30:33], v[14:17], v[22:25]
	s_waitcnt lgkmcnt(8)
	v_mfma_f32_16x16x32_bf16 v[22:25], v[34:37], v[18:21], v[22:25]
	s_nop 7
	global_store_dwordx4 v[140:141], v[22:25], off offset:128 sc1
	s_waitcnt lgkmcnt(3)
	v_mfma_f32_16x16x32_bf16 v[6:9], v[38:41], v[6:9], 0
	s_waitcnt lgkmcnt(2)
	v_mfma_f32_16x16x32_bf16 v[6:9], v[42:45], v[10:13], v[6:9]
	s_waitcnt lgkmcnt(1)
	v_mfma_f32_16x16x32_bf16 v[6:9], v[46:49], v[14:17], v[6:9]
	s_waitcnt lgkmcnt(0)
	v_mfma_f32_16x16x32_bf16 v[6:9], v[50:53], v[18:21], v[6:9]
	s_nop 7
	global_store_dwordx4 v[140:141], v[6:9], off offset:192 sc1
	ds_read_u16 v6, v220 offset:32768
	ds_read_u16 v7, v221 offset:33024
	ds_read_u16 v8, v222 offset:33280
	ds_read_u16 v9, v223 offset:33536
	s_waitcnt lgkmcnt(3)
	v_lshlrev_b32_e32 v6, 16, v6
	s_waitcnt lgkmcnt(2)
	v_lshlrev_b32_e32 v7, 16, v7
	v_pk_add_f32 v[6:7], v[6:7], 0 op_sel_hi:[1,0]
	s_waitcnt lgkmcnt(0)
	v_lshlrev_b32_e32 v9, 16, v9
	v_lshlrev_b32_e32 v8, 16, v8
	v_pk_add_f32 v[6:7], v[6:7], v[8:9]
	ds_read_u16 v8, v224 offset:33792
	ds_read_u16 v9, v225 offset:34048
	s_waitcnt lgkmcnt(1)
	v_lshlrev_b32_e32 v8, 16, v8
	s_waitcnt lgkmcnt(0)
	v_lshlrev_b32_e32 v9, 16, v9
	v_pk_add_f32 v[6:7], v[6:7], v[8:9]
	ds_read_u16 v8, v226 offset:34304
	ds_read_u16 v9, v227 offset:34560
	s_waitcnt lgkmcnt(1)
	v_lshlrev_b32_e32 v8, 16, v8
	s_waitcnt lgkmcnt(0)
	v_lshlrev_b32_e32 v9, 16, v9
	v_pk_add_f32 v[6:7], v[6:7], v[8:9]
	ds_read_u16 v8, v228 offset:34816
	ds_read_u16 v9, v229 offset:35072
	ds_read_u16 v10, v230 offset:35328
	ds_read_u16 v11, v231 offset:35584
	ds_read_u16 v12, v232 offset:35840
	ds_read_u16 v13, v233 offset:36096
	s_waitcnt lgkmcnt(5)
	v_lshlrev_b32_e32 v8, 16, v8
	s_waitcnt lgkmcnt(4)
	v_lshlrev_b32_e32 v9, 16, v9
	s_waitcnt lgkmcnt(3)
	v_lshlrev_b32_e32 v10, 16, v10
	s_waitcnt lgkmcnt(2)
	v_lshlrev_b32_e32 v11, 16, v11
	v_pk_add_f32 v[6:7], v[6:7], v[8:9]
	s_waitcnt lgkmcnt(0)
	v_lshlrev_b32_e32 v9, 16, v13
	v_pk_add_f32 v[6:7], v[6:7], v[10:11]
	v_lshlrev_b32_e32 v8, 16, v12
	v_pk_add_f32 v[6:7], v[6:7], v[8:9]
	ds_read_u16 v8, v234 offset:36352
	ds_read_u16 v9, v235 offset:36608
	s_waitcnt lgkmcnt(1)
	v_lshlrev_b32_e32 v8, 16, v8
	s_waitcnt lgkmcnt(0)
	v_lshlrev_b32_e32 v9, 16, v9
	v_pk_add_f32 v[6:7], v[6:7], v[8:9]
	ds_read_u16 v8, v220 offset:36864
	ds_read_u16 v9, v221 offset:37120
	s_waitcnt lgkmcnt(1)
	v_lshlrev_b32_e32 v8, 16, v8
	s_waitcnt lgkmcnt(0)
	v_lshlrev_b32_e32 v9, 16, v9
	v_pk_add_f32 v[6:7], v[6:7], v[8:9]
	ds_read_u16 v8, v222 offset:37376
	ds_read_u16 v9, v223 offset:37632
	s_waitcnt lgkmcnt(1)
	v_lshlrev_b32_e32 v8, 16, v8
	s_waitcnt lgkmcnt(0)
	v_lshlrev_b32_e32 v9, 16, v9
	v_pk_add_f32 v[6:7], v[6:7], v[8:9]
	ds_read_u16 v8, v224 offset:37888
	ds_read_u16 v9, v225 offset:38144
	s_waitcnt lgkmcnt(1)
	v_lshlrev_b32_e32 v8, 16, v8
	s_waitcnt lgkmcnt(0)
	v_lshlrev_b32_e32 v9, 16, v9
	v_pk_add_f32 v[6:7], v[6:7], v[8:9]
	ds_read_u16 v8, v226 offset:38400
	ds_read_u16 v9, v227 offset:38656
	s_waitcnt lgkmcnt(1)
	v_lshlrev_b32_e32 v8, 16, v8
	s_waitcnt lgkmcnt(0)
	v_lshlrev_b32_e32 v9, 16, v9
	v_pk_add_f32 v[6:7], v[6:7], v[8:9]
	ds_read_u16 v8, v228 offset:38912
	ds_read_u16 v9, v229 offset:39168
	s_waitcnt lgkmcnt(1)
	v_lshlrev_b32_e32 v8, 16, v8
	s_waitcnt lgkmcnt(0)
	v_lshlrev_b32_e32 v9, 16, v9
	v_pk_add_f32 v[6:7], v[6:7], v[8:9]
	ds_read_u16 v8, v230 offset:39424
	ds_read_u16 v9, v231 offset:39680
	s_waitcnt lgkmcnt(1)
	v_lshlrev_b32_e32 v8, 16, v8
	s_waitcnt lgkmcnt(0)
	v_lshlrev_b32_e32 v9, 16, v9
	v_pk_add_f32 v[6:7], v[6:7], v[8:9]
	ds_read_u16 v8, v232 offset:39936
	ds_read_u16 v9, v233 offset:40192
	s_waitcnt lgkmcnt(1)
	v_lshlrev_b32_e32 v8, 16, v8
	s_waitcnt lgkmcnt(0)
	v_lshlrev_b32_e32 v9, 16, v9
	v_pk_add_f32 v[6:7], v[6:7], v[8:9]
	ds_read_u16 v8, v234 offset:40448
	ds_read_u16 v9, v236 offset:32768
	s_waitcnt lgkmcnt(1)
	v_lshlrev_b32_e32 v8, 16, v8
	s_waitcnt lgkmcnt(0)
	v_lshlrev_b32_e32 v9, 16, v9
	v_pk_add_f32 v[6:7], v[6:7], v[8:9]
	s_nop 0
	v_add_f32_e32 v6, v6, v7
	ds_write_b32 v172, v6 offset:512
	s_waitcnt lgkmcnt(0)
	s_barrier
	s_and_saveexec_b64 s[16:17], s[52:53]
	s_cbranch_execz .LBB0_412
	ds_read2st64_b32 v[6:7], v173 offset0:2 offset1:4
	ds_read2st64_b32 v[8:9], v173 offset0:6 offset1:8
	s_waitcnt lgkmcnt(1)
	v_mov_b32_e32 v10, v6
	s_waitcnt lgkmcnt(0)
	v_mov_b32_e32 v11, v8
	v_mov_b32_e32 v8, v7
	v_pk_add_f32 v[6:7], v[10:11], v[8:9]
	s_nop 0
	v_add_f32_e32 v6, v6, v7
	global_store_dword v[138:139], v6, off
	s_branch .LBB0_412

.LBB0_663:
	v_lshl_or_b32 v132, s2, 8, v221
	v_lshl_add_u32 v130, s56, 8, v219
	v_ashrrev_i32_e32 v133, 31, v132
	v_readlane_b32 s80, v254, 7
	v_lshlrev_b64 v[208:209], 2, v[132:133]
	v_readlane_b32 s81, v254, 8
	v_ashrrev_i32_e32 v131, 31, v130
	v_lshlrev_b64 v[212:213], 13, v[130:131]
	v_lshl_add_u64 v[210:211], s[80:81], 0, v[208:209]
	v_lshl_add_u64 v[132:133], v[210:211], 0, v[212:213]
	global_load_dwordx4 v[158:161], v[132:133], off
	global_load_dwordx4 v[150:153], v[132:133], off offset:64
	global_load_dwordx4 v[146:149], v[132:133], off offset:512
	global_load_dwordx4 v[142:145], v[132:133], off offset:576
	v_or_b32_e32 v132, 16, v130
	v_ashrrev_i32_e32 v133, 31, v132
	v_lshlrev_b64 v[226:227], 13, v[132:133]
	v_lshl_add_u64 v[132:133], v[210:211], 0, v[226:227]
	global_load_dwordx4 v[174:177], v[132:133], off
	global_load_dwordx4 v[166:169], v[132:133], off offset:64
	global_load_dwordx4 v[162:165], v[132:133], off offset:512
	global_load_dwordx4 v[154:157], v[132:133], off offset:576
	v_or_b32_e32 v132, 32, v130
	v_or_b32_e32 v130, 48, v130
	v_ashrrev_i32_e32 v133, 31, v132
	v_ashrrev_i32_e32 v131, 31, v130
	v_lshlrev_b64 v[228:229], 13, v[132:133]
	v_lshlrev_b64 v[216:217], 13, v[130:131]
	v_lshl_add_u64 v[132:133], v[210:211], 0, v[228:229]
	v_lshl_add_u64 v[130:131], v[210:211], 0, v[216:217]
	global_load_dwordx4 v[186:189], v[132:133], off
	global_load_dwordx4 v[182:185], v[132:133], off offset:64
	global_load_dwordx4 v[178:181], v[132:133], off offset:512
	global_load_dwordx4 v[170:173], v[132:133], off offset:576
	global_load_dwordx4 v[190:193], v[130:131], off
	global_load_dwordx4 v[138:141], v[130:131], off offset:64
	global_load_dwordx4 v[134:137], v[130:131], off offset:512
	s_nop 0
	global_load_dwordx4 v[130:133], v[130:131], off offset:576
	v_lshl_add_u64 v[214:215], s[78:79], 0, v[212:213]
	v_lshl_add_u64 v[216:217], s[78:79], 0, v[216:217]
	s_mov_b64 s[26:27], 0x100000
	v_lshl_add_u64 v[214:215], v[214:215], 0, v[208:209]
	v_lshl_add_u64 v[226:227], s[78:79], 0, v[226:227]
	v_lshl_add_u64 v[228:229], s[78:79], 0, v[228:229]
	v_lshl_add_u64 v[216:217], v[216:217], 0, v[208:209]
	v_lshl_add_u64 v[226:227], v[226:227], 0, v[208:209]
	v_lshl_add_u64 v[228:229], v[228:229], 0, v[208:209]
	s_andn2_b64 vcc, exec, s[0:1]
	s_mov_b64 s[0:1], -1
	v_readlane_b32 s82, v254, 9
	v_readlane_b32 s83, v254, 10
	v_readlane_b32 s84, v254, 11
	v_readlane_b32 s85, v254, 12
	v_readlane_b32 s86, v254, 13
	v_readlane_b32 s87, v254, 14
	v_readlane_b32 s88, v254, 15
	v_readlane_b32 s89, v254, 16
	v_readlane_b32 s90, v254, 17
	v_readlane_b32 s91, v254, 18
	v_readlane_b32 s92, v254, 19
	v_readlane_b32 s93, v254, 20
	v_readlane_b32 s94, v254, 21
	v_readlane_b32 s95, v254, 22
	s_waitcnt vmcnt(0)
	v_pk_add_f32 v[128:129], v[128:129], v[160:161]
	v_pk_add_f32 v[126:127], v[126:127], v[158:159]
	v_pk_add_f32 v[124:125], v[124:125], v[152:153]
	v_pk_add_f32 v[122:123], v[122:123], v[150:151]
	v_pk_add_f32 v[108:109], v[108:109], v[148:149]
	v_pk_add_f32 v[106:107], v[106:107], v[146:147]
	v_pk_add_f32 v[100:101], v[100:101], v[144:145]
	v_pk_add_f32 v[98:99], v[98:99], v[142:143]
	v_pk_add_f32 v[120:121], v[120:121], v[176:177]
	v_pk_add_f32 v[118:119], v[118:119], v[174:175]
	v_pk_add_f32 v[116:117], v[116:117], v[168:169]
	v_pk_add_f32 v[114:115], v[114:115], v[166:167]
	v_pk_add_f32 v[92:93], v[92:93], v[164:165]
	v_pk_add_f32 v[90:91], v[90:91], v[162:163]
	v_pk_add_f32 v[88:89], v[88:89], v[156:157]
	v_pk_add_f32 v[86:87], v[86:87], v[154:155]
	v_pk_add_f32 v[112:113], v[112:113], v[188:189]
	v_pk_add_f32 v[72:73], v[72:73], v[136:137]
	v_pk_add_f32 v[70:71], v[70:71], v[134:135]
	v_pk_add_f32 v[68:69], v[68:69], v[132:133]
	v_pk_add_f32 v[66:67], v[66:67], v[130:131]
	v_lshl_add_u64 v[132:133], v[212:213], 0, s[26:27]
	s_mov_b64 s[26:27], 0x120000
	v_pk_add_f32 v[110:111], v[110:111], v[186:187]
	v_pk_add_f32 v[104:105], v[104:105], v[184:185]
	v_pk_add_f32 v[102:103], v[102:103], v[182:183]
	v_pk_add_f32 v[84:85], v[84:85], v[180:181]
	v_pk_add_f32 v[82:83], v[82:83], v[178:179]
	v_pk_add_f32 v[80:81], v[80:81], v[172:173]
	v_pk_add_f32 v[78:79], v[78:79], v[170:171]
	v_pk_add_f32 v[96:97], v[96:97], v[192:193]
	v_pk_add_f32 v[94:95], v[94:95], v[190:191]
	v_pk_add_f32 v[76:77], v[76:77], v[140:141]
	v_pk_add_f32 v[74:75], v[74:75], v[138:139]
	global_store_dwordx4 v[214:215], v[126:129], off sc1
	global_store_dwordx4 v[214:215], v[122:125], off offset:64 sc1
	global_store_dwordx4 v[214:215], v[106:109], off offset:512 sc1
	global_store_dwordx4 v[214:215], v[98:101], off offset:576 sc1
	global_store_dwordx4 v[226:227], v[118:121], off sc1
	global_store_dwordx4 v[226:227], v[114:117], off offset:64 sc1
	global_store_dwordx4 v[226:227], v[90:93], off offset:512 sc1
	global_store_dwordx4 v[226:227], v[86:89], off offset:576 sc1
	global_store_dwordx4 v[228:229], v[110:113], off sc1
	global_store_dwordx4 v[228:229], v[102:105], off offset:64 sc1
	global_store_dwordx4 v[228:229], v[82:85], off offset:512 sc1
	global_store_dwordx4 v[228:229], v[78:81], off offset:576 sc1
	global_store_dwordx4 v[216:217], v[94:97], off sc1
	global_store_dwordx4 v[216:217], v[74:77], off offset:64 sc1
	global_store_dwordx4 v[216:217], v[70:73], off offset:512 sc1
	global_store_dwordx4 v[216:217], v[66:69], off offset:576 sc1
	v_lshl_add_u64 v[134:135], v[212:213], 0, s[26:27]
	s_mov_b64 s[26:27], 0x140000
	v_lshl_add_u64 v[66:67], v[210:211], 0, v[132:133]
	global_load_dwordx4 v[126:129], v[66:67], off
	global_load_dwordx4 v[118:121], v[66:67], off offset:64
	global_load_dwordx4 v[106:109], v[66:67], off offset:512
	global_load_dwordx4 v[90:93], v[66:67], off offset:576
	v_lshl_add_u64 v[66:67], v[210:211], 0, v[134:135]
	v_lshl_add_u64 v[136:137], v[212:213], 0, s[26:27]
	s_mov_b64 s[26:27], 0x160000
	global_load_dwordx4 v[122:125], v[66:67], off
	global_load_dwordx4 v[110:113], v[66:67], off offset:64
	global_load_dwordx4 v[94:97], v[66:67], off offset:512
	global_load_dwordx4 v[82:85], v[66:67], off offset:576
	v_lshl_add_u64 v[66:67], v[210:211], 0, v[136:137]
	v_lshl_add_u64 v[130:131], v[212:213], 0, s[26:27]
	global_load_dwordx4 v[114:117], v[66:67], off
	global_load_dwordx4 v[98:101], v[66:67], off offset:64
	global_load_dwordx4 v[86:89], v[66:67], off offset:512
	global_load_dwordx4 v[78:81], v[66:67], off offset:576
	v_lshl_add_u64 v[66:67], v[210:211], 0, v[130:131]
	global_load_dwordx4 v[102:105], v[66:67], off
	global_load_dwordx4 v[74:77], v[66:67], off offset:64
	global_load_dwordx4 v[70:73], v[66:67], off offset:512
	s_nop 0
	global_load_dwordx4 v[66:69], v[66:67], off offset:576
	v_lshl_add_u64 v[132:133], s[78:79], 0, v[132:133]
	v_lshl_add_u64 v[134:135], s[78:79], 0, v[134:135]
	v_lshl_add_u64 v[136:137], s[78:79], 0, v[136:137]
	v_lshl_add_u64 v[130:131], s[78:79], 0, v[130:131]
	v_lshl_add_u64 v[132:133], v[132:133], 0, v[208:209]
	v_lshl_add_u64 v[134:135], v[134:135], 0, v[208:209]
	v_lshl_add_u64 v[136:137], v[136:137], 0, v[208:209]
	s_waitcnt vmcnt(15)
	v_pk_add_f32 v[64:65], v[64:65], v[128:129]
	v_pk_add_f32 v[62:63], v[62:63], v[126:127]
	s_waitcnt vmcnt(14)
	v_pk_add_f32 v[60:61], v[60:61], v[120:121]
	v_pk_add_f32 v[58:59], v[58:59], v[118:119]
	s_waitcnt vmcnt(13)
	v_pk_add_f32 v[44:45], v[44:45], v[108:109]
	v_pk_add_f32 v[42:43], v[42:43], v[106:107]
	s_waitcnt vmcnt(12)
	v_pk_add_f32 v[36:37], v[36:37], v[92:93]
	v_pk_add_f32 v[34:35], v[34:35], v[90:91]
	s_waitcnt vmcnt(11)
	v_pk_add_f32 v[56:57], v[56:57], v[124:125]
	v_pk_add_f32 v[54:55], v[54:55], v[122:123]
	s_waitcnt vmcnt(4)
	v_pk_add_f32 v[14:15], v[14:15], v[78:79]
	v_pk_add_f32 v[52:53], v[52:53], v[112:113]
	v_pk_add_f32 v[50:51], v[50:51], v[110:111]
	v_pk_add_f32 v[28:29], v[28:29], v[96:97]
	v_pk_add_f32 v[26:27], v[26:27], v[94:95]
	v_pk_add_f32 v[24:25], v[24:25], v[84:85]
	v_pk_add_f32 v[22:23], v[22:23], v[82:83]
	v_pk_add_f32 v[48:49], v[48:49], v[116:117]
	v_pk_add_f32 v[46:47], v[46:47], v[114:115]
	v_pk_add_f32 v[40:41], v[40:41], v[100:101]
	v_pk_add_f32 v[38:39], v[38:39], v[98:99]
	v_pk_add_f32 v[20:21], v[20:21], v[88:89]
	v_pk_add_f32 v[18:19], v[18:19], v[86:87]
	v_pk_add_f32 v[16:17], v[16:17], v[80:81]
	s_waitcnt vmcnt(3)
	v_pk_add_f32 v[32:33], v[32:33], v[104:105]
	v_pk_add_f32 v[30:31], v[30:31], v[102:103]
	global_store_dwordx4 v[132:133], v[62:65], off sc1
	global_store_dwordx4 v[132:133], v[58:61], off offset:64 sc1
	global_store_dwordx4 v[132:133], v[42:45], off offset:512 sc1
	global_store_dwordx4 v[132:133], v[34:37], off offset:576 sc1
	global_store_dwordx4 v[134:135], v[54:57], off sc1
	global_store_dwordx4 v[134:135], v[50:53], off offset:64 sc1
	global_store_dwordx4 v[134:135], v[26:29], off offset:512 sc1
	global_store_dwordx4 v[134:135], v[22:25], off offset:576 sc1
	global_store_dwordx4 v[136:137], v[46:49], off sc1
	global_store_dwordx4 v[136:137], v[38:41], off offset:64 sc1
	global_store_dwordx4 v[136:137], v[18:21], off offset:512 sc1
	global_store_dwordx4 v[136:137], v[14:17], off offset:576 sc1
	s_waitcnt vmcnt(14)
	v_pk_add_f32 v[12:13], v[12:13], v[76:77]
	v_pk_add_f32 v[10:11], v[10:11], v[74:75]
	v_lshl_add_u64 v[14:15], v[130:131], 0, v[208:209]
	s_waitcnt vmcnt(13)
	v_pk_add_f32 v[8:9], v[8:9], v[72:73]
	v_pk_add_f32 v[6:7], v[6:7], v[70:71]
	s_waitcnt vmcnt(12)
	v_pk_add_f32 v[4:5], v[4:5], v[68:69]
	v_pk_add_f32 v[2:3], v[2:3], v[66:67]
	global_store_dwordx4 v[14:15], v[30:33], off sc1
	global_store_dwordx4 v[14:15], v[10:13], off offset:64 sc1
	global_store_dwordx4 v[14:15], v[6:9], off offset:512 sc1
	global_store_dwordx4 v[14:15], v[2:5], off offset:576 sc1
	s_cbranch_vccnz .LBB0_652
	s_andn2_b64 vcc, exec, s[12:13]
	s_cbranch_vccnz .LBB0_651
	s_barrier
	s_branch .LBB0_651

.LBB0_861:
	v_lshl_or_b32 v2, s71, 8, v184
	v_lshl_add_u32 v206, s2, 8, v182
	v_ashrrev_i32_e32 v3, 31, v2
	v_lshlrev_b64 v[176:177], 2, v[2:3]
	v_ashrrev_i32_e32 v207, 31, v206
	v_lshl_add_u64 v[178:179], s[78:79], 0, v[176:177]
	v_lshlrev_b64 v[180:181], 13, v[206:207]
	s_nop 15
	s_nop 15
	v_lshl_add_u64 v[14:15], v[178:179], 0, v[180:181]
	global_load_dwordx4 v[2:5], v[14:15], off
	global_load_dwordx4 v[6:9], v[14:15], off offset:64
	global_load_dwordx4 v[10:13], v[14:15], off offset:512
	s_nop 0
	global_load_dwordx4 v[14:17], v[14:15], off offset:576
	v_or_b32_e32 v18, 16, v206
	v_ashrrev_i32_e32 v19, 31, v18
	v_lshlrev_b64 v[224:225], 13, v[18:19]
	v_lshl_add_u64 v[30:31], v[178:179], 0, v[224:225]
	global_load_dwordx4 v[18:21], v[30:31], off
	global_load_dwordx4 v[22:25], v[30:31], off offset:64
	global_load_dwordx4 v[26:29], v[30:31], off offset:512
	s_nop 0
	global_load_dwordx4 v[30:33], v[30:31], off offset:576
	v_or_b32_e32 v190, 32, v206
	v_ashrrev_i32_e32 v191, 31, v190
	v_lshlrev_b64 v[226:227], 13, v[190:191]
	v_lshl_add_u64 v[202:203], v[178:179], 0, v[226:227]
	global_load_dwordx4 v[190:193], v[202:203], off
	global_load_dwordx4 v[194:197], v[202:203], off offset:64
	global_load_dwordx4 v[198:201], v[202:203], off offset:512
	s_nop 0
	global_load_dwordx4 v[202:205], v[202:203], off offset:576
	v_or_b32_e32 v206, 48, v206
	v_ashrrev_i32_e32 v207, 31, v206
	v_lshlrev_b64 v[228:229], 13, v[206:207]
	v_lshl_add_u64 v[220:221], v[178:179], 0, v[228:229]
	global_load_dwordx4 v[206:209], v[220:221], off
	global_load_dwordx4 v[210:213], v[220:221], off offset:64
	global_load_dwordx4 v[214:217], v[220:221], off offset:512
	s_nop 0
	global_load_dwordx4 v[220:223], v[220:221], off offset:576
	s_mov_b64 s[26:27], 0x100000
	s_mov_b64 s[50:51], -1
	s_and_b64 vcc, exec, s[0:1]
	s_waitcnt vmcnt(0)
	v_pk_add_f32 v[2:3], v[158:159], v[2:3]
	v_lshl_add_u64 v[158:159], s[78:79], 0, v[180:181]
	v_pk_add_f32 v[4:5], v[160:161], v[4:5]
	v_lshl_add_u64 v[158:159], v[158:159], 0, v[176:177]
	global_store_dwordx4 v[158:159], v[2:5], off sc1
	s_nop 1
	v_pk_add_f32 v[4:5], v[156:157], v[8:9]
	v_pk_add_f32 v[2:3], v[154:155], v[6:7]
	global_store_dwordx4 v[158:159], v[2:5], off offset:64 sc1
	v_lshl_add_u64 v[6:7], s[78:79], 0, v[224:225]
	v_lshl_add_u64 v[6:7], v[6:7], 0, v[176:177]
	v_pk_add_f32 v[4:5], v[144:145], v[12:13]
	v_pk_add_f32 v[2:3], v[142:143], v[10:11]
	global_store_dwordx4 v[158:159], v[2:5], off offset:512 sc1
	s_nop 1
	v_pk_add_f32 v[4:5], v[136:137], v[16:17]
	v_pk_add_f32 v[2:3], v[134:135], v[14:15]
	global_store_dwordx4 v[158:159], v[2:5], off offset:576 sc1
	s_nop 1
	v_pk_add_f32 v[4:5], v[152:153], v[20:21]
	v_pk_add_f32 v[2:3], v[150:151], v[18:19]
	global_store_dwordx4 v[6:7], v[2:5], off sc1
	s_nop 1
	v_pk_add_f32 v[4:5], v[148:149], v[24:25]
	v_pk_add_f32 v[2:3], v[146:147], v[22:23]
	global_store_dwordx4 v[6:7], v[2:5], off offset:64 sc1
	s_nop 1
	v_pk_add_f32 v[4:5], v[128:129], v[28:29]
	v_pk_add_f32 v[2:3], v[126:127], v[26:27]
	global_store_dwordx4 v[6:7], v[2:5], off offset:512 sc1
	s_nop 1
	v_pk_add_f32 v[4:5], v[120:121], v[32:33]
	v_pk_add_f32 v[2:3], v[118:119], v[30:31]
	global_store_dwordx4 v[6:7], v[2:5], off offset:576 sc1
	v_lshl_add_u64 v[6:7], s[78:79], 0, v[226:227]
	v_lshl_add_u64 v[6:7], v[6:7], 0, v[176:177]
	v_pk_add_f32 v[4:5], v[140:141], v[192:193]
	v_pk_add_f32 v[2:3], v[138:139], v[190:191]
	global_store_dwordx4 v[6:7], v[2:5], off sc1
	s_nop 1
	v_pk_add_f32 v[4:5], v[132:133], v[196:197]
	v_pk_add_f32 v[2:3], v[130:131], v[194:195]
	global_store_dwordx4 v[6:7], v[2:5], off offset:64 sc1
	v_lshl_add_u64 v[130:131], v[180:181], 0, s[26:27]
	s_mov_b64 s[26:27], 0x120000
	v_pk_add_f32 v[4:5], v[112:113], v[200:201]
	v_pk_add_f32 v[2:3], v[110:111], v[198:199]
	global_store_dwordx4 v[6:7], v[2:5], off offset:512 sc1
	v_lshl_add_u64 v[136:137], v[180:181], 0, s[26:27]
	v_lshl_add_u64 v[18:19], v[178:179], 0, v[136:137]
	v_pk_add_f32 v[4:5], v[108:109], v[204:205]
	v_pk_add_f32 v[2:3], v[106:107], v[202:203]
	global_store_dwordx4 v[6:7], v[2:5], off offset:576 sc1
	v_lshl_add_u64 v[6:7], s[78:79], 0, v[228:229]
	v_lshl_add_u64 v[6:7], v[6:7], 0, v[176:177]
	v_pk_add_f32 v[4:5], v[124:125], v[208:209]
	v_pk_add_f32 v[2:3], v[122:123], v[206:207]
	global_store_dwordx4 v[6:7], v[2:5], off sc1
	s_mov_b64 s[26:27], 0x140000
	v_lshl_add_u64 v[132:133], v[180:181], 0, s[26:27]
	v_pk_add_f32 v[4:5], v[116:117], v[212:213]
	v_pk_add_f32 v[2:3], v[114:115], v[210:211]
	global_store_dwordx4 v[6:7], v[2:5], off offset:64 sc1
	s_mov_b64 s[26:27], 0x160000
	v_lshl_add_u64 v[134:135], v[180:181], 0, s[26:27]
	v_pk_add_f32 v[4:5], v[104:105], v[216:217]
	v_pk_add_f32 v[2:3], v[102:103], v[214:215]
	global_store_dwordx4 v[6:7], v[2:5], off offset:512 sc1
	v_lshl_add_u64 v[122:123], v[178:179], 0, v[134:135]
	s_nop 0
	v_pk_add_f32 v[4:5], v[100:101], v[222:223]
	v_pk_add_f32 v[2:3], v[98:99], v[220:221]
	global_store_dwordx4 v[6:7], v[2:5], off offset:576 sc1
	s_nop 1
	v_lshl_add_u64 v[2:3], v[178:179], 0, v[130:131]
	global_load_dwordx4 v[14:17], v[2:3], off
	global_load_dwordx4 v[10:13], v[2:3], off offset:64
	global_load_dwordx4 v[6:9], v[2:3], off offset:512
	s_nop 0
	global_load_dwordx4 v[2:5], v[2:3], off offset:576
	s_nop 0
	global_load_dwordx4 v[110:113], v[18:19], off
	global_load_dwordx4 v[106:109], v[18:19], off offset:64
	global_load_dwordx4 v[98:101], v[18:19], off offset:512
	global_load_dwordx4 v[26:29], v[18:19], off offset:576
	v_lshl_add_u64 v[18:19], v[178:179], 0, v[132:133]
	global_load_dwordx4 v[102:105], v[18:19], off
	global_load_dwordx4 v[30:33], v[18:19], off offset:64
	global_load_dwordx4 v[22:25], v[18:19], off offset:512
	s_nop 0
	global_load_dwordx4 v[18:21], v[18:19], off offset:576
	s_nop 0
	global_load_dwordx4 v[118:121], v[122:123], off
	global_load_dwordx4 v[114:117], v[122:123], off offset:64
	global_load_dwordx4 v[126:129], v[122:123], off offset:512
	s_nop 0
	global_load_dwordx4 v[122:125], v[122:123], off offset:576
	s_waitcnt vmcnt(15)
	v_pk_add_f32 v[14:15], v[94:95], v[14:15]
	v_lshl_add_u64 v[94:95], s[78:79], 0, v[130:131]
	v_lshl_add_u64 v[94:95], v[94:95], 0, v[176:177]
	s_waitcnt vmcnt(13)
	v_pk_add_f32 v[8:9], v[84:85], v[8:9]
	v_pk_add_f32 v[6:7], v[82:83], v[6:7]
	global_store_dwordx4 v[94:95], v[6:9], off offset:512 sc1
	s_waitcnt vmcnt(13)
	v_pk_add_f32 v[4:5], v[76:77], v[4:5]
	v_pk_add_f32 v[2:3], v[74:75], v[2:3]
	v_lshl_add_u64 v[6:7], s[78:79], 0, v[136:137]
	global_store_dwordx4 v[94:95], v[2:5], off offset:576 sc1
	v_lshl_add_u64 v[6:7], v[6:7], 0, v[176:177]
	v_pk_add_f32 v[16:17], v[96:97], v[16:17]
	s_waitcnt vmcnt(13)
	v_pk_add_f32 v[4:5], v[88:89], v[112:113]
	v_pk_add_f32 v[2:3], v[86:87], v[110:111]
	global_store_dwordx4 v[6:7], v[2:5], off sc1
	v_pk_add_f32 v[12:13], v[92:93], v[12:13]
	v_pk_add_f32 v[10:11], v[90:91], v[10:11]
	s_waitcnt vmcnt(13)
	v_pk_add_f32 v[4:5], v[80:81], v[108:109]
	v_pk_add_f32 v[2:3], v[78:79], v[106:107]
	global_store_dwordx4 v[6:7], v[2:5], off offset:64 sc1
	global_store_dwordx4 v[94:95], v[14:17], off sc1
	global_store_dwordx4 v[94:95], v[10:13], off offset:64 sc1
	s_waitcnt vmcnt(15)
	v_pk_add_f32 v[4:5], v[68:69], v[100:101]
	v_pk_add_f32 v[2:3], v[66:67], v[98:99]
	global_store_dwordx4 v[6:7], v[2:5], off offset:512 sc1
	s_waitcnt vmcnt(15)
	s_nop 0
	v_pk_add_f32 v[4:5], v[60:61], v[28:29]
	v_pk_add_f32 v[2:3], v[58:59], v[26:27]
	global_store_dwordx4 v[6:7], v[2:5], off offset:576 sc1
	v_lshl_add_u64 v[6:7], s[78:79], 0, v[132:133]
	v_lshl_add_u64 v[6:7], v[6:7], 0, v[176:177]
	s_waitcnt vmcnt(15)
	v_pk_add_f32 v[4:5], v[72:73], v[104:105]
	v_pk_add_f32 v[2:3], v[70:71], v[102:103]
	global_store_dwordx4 v[6:7], v[2:5], off sc1
	s_waitcnt vmcnt(15)
	s_nop 0
	v_pk_add_f32 v[4:5], v[64:65], v[32:33]
	v_pk_add_f32 v[2:3], v[62:63], v[30:31]
	global_store_dwordx4 v[6:7], v[2:5], off offset:64 sc1
	s_waitcnt vmcnt(15)
	s_nop 0
	v_pk_add_f32 v[4:5], v[52:53], v[24:25]
	v_pk_add_f32 v[2:3], v[50:51], v[22:23]
	global_store_dwordx4 v[6:7], v[2:5], off offset:512 sc1
	s_waitcnt vmcnt(15)
	s_nop 0
	v_pk_add_f32 v[4:5], v[44:45], v[20:21]
	v_pk_add_f32 v[2:3], v[42:43], v[18:19]
	global_store_dwordx4 v[6:7], v[2:5], off offset:576 sc1
	v_lshl_add_u64 v[6:7], s[78:79], 0, v[134:135]
	v_lshl_add_u64 v[6:7], v[6:7], 0, v[176:177]
	s_waitcnt vmcnt(15)
	v_pk_add_f32 v[4:5], v[56:57], v[120:121]
	v_pk_add_f32 v[2:3], v[54:55], v[118:119]
	global_store_dwordx4 v[6:7], v[2:5], off sc1
	s_waitcnt vmcnt(15)
	s_nop 0
	v_pk_add_f32 v[4:5], v[48:49], v[116:117]
	v_pk_add_f32 v[2:3], v[46:47], v[114:115]
	global_store_dwordx4 v[6:7], v[2:5], off offset:64 sc1
	s_waitcnt vmcnt(15)
	s_nop 0
	v_pk_add_f32 v[4:5], v[40:41], v[128:129]
	v_pk_add_f32 v[2:3], v[38:39], v[126:127]
	global_store_dwordx4 v[6:7], v[2:5], off offset:512 sc1
	s_waitcnt vmcnt(15)
	s_nop 0
	v_pk_add_f32 v[4:5], v[36:37], v[124:125]
	v_pk_add_f32 v[2:3], v[34:35], v[122:123]
	global_store_dwordx4 v[6:7], v[2:5], off offset:576 sc1
	s_cbranch_vccnz .LBB0_846
	s_andn2_b64 vcc, exec, s[14:15]
	s_cbranch_vccnz .LBB0_845
	s_barrier
	s_branch .LBB0_845

.LBB0_988:
	s_lshl_b32 s27, s2, 8
	s_add_i32 s41, s27, 0xfffff400
	s_cmp_gt_i32 s2, 11
	s_mov_b32 s45, 0x37400000
	s_movk_i32 s26, 0x400
	s_cselect_b32 s45, s45, 0x31400000
	s_cselect_b32 s26, s26, 0xc00
	s_cselect_b32 s27, s41, s27
	s_add_u32 s56, s28, s45
	s_addc_u32 s57, s29, 0
	v_or_b32_e32 v4, s27, v184
	s_cmp_lt_i32 s2, 4
	v_lshl_add_u32 v3, s54, 8, v182
	s_cselect_b64 vcc, -1, 0
	v_ashrrev_i32_e32 v5, 31, v4
	v_cndmask_b32_e32 v2, 1.0, v190, vcc
	v_lshl_add_u64 v[4:5], v[4:5], 1, s[56:57]
	v_mad_i64_i32 v[6:7], s[56:57], s26, v3, 0
	v_lshl_add_u64 v[10:11], v[6:7], 1, v[4:5]
	v_pk_mul_f32 v[6:7], v[2:3], v[158:159] op_sel_hi:[0,1]
	s_nop 15
	s_nop 15
	v_pk_mul_f32 v[8:9], v[2:3], v[160:161] op_sel_hi:[0,1]
	v_cvt_pk_bf16_f32 v6, v6, v7
	v_cvt_pk_bf16_f32 v7, v8, v9
	v_pk_mul_f32 v[12:13], v[2:3], v[156:157] op_sel_hi:[0,1]
	v_pk_mul_f32 v[14:15], v[2:3], v[154:155] op_sel_hi:[0,1]
	v_cvt_pk_bf16_f32 v8, v14, v15
	v_cvt_pk_bf16_f32 v9, v12, v13
	global_store_dwordx4 v[10:11], v[6:9], off sc1
	v_pk_mul_f32 v[12:13], v[2:3], v[144:145] op_sel_hi:[0,1]
	v_pk_mul_f32 v[14:15], v[2:3], v[142:143] op_sel_hi:[0,1]
	v_pk_mul_f32 v[6:7], v[2:3], v[150:151] op_sel_hi:[0,1]
	v_pk_mul_f32 v[8:9], v[2:3], v[152:153] op_sel_hi:[0,1]
	v_cvt_pk_bf16_f32 v6, v6, v7
	v_cvt_pk_bf16_f32 v7, v8, v9
	v_cvt_pk_bf16_f32 v8, v14, v15
	v_cvt_pk_bf16_f32 v9, v12, v13
	global_store_dwordx4 v[10:11], v[6:9], off offset:256 sc1
	v_pk_mul_f32 v[12:13], v[2:3], v[140:141] op_sel_hi:[0,1]
	v_pk_mul_f32 v[14:15], v[2:3], v[138:139] op_sel_hi:[0,1]
	v_or_b32_e32 v6, 16, v3
	v_mad_i64_i32 v[6:7], s[56:57], s26, v6, 0
	v_lshl_add_u64 v[10:11], v[6:7], 1, v[4:5]
	v_pk_mul_f32 v[6:7], v[2:3], v[146:147] op_sel_hi:[0,1]
	v_pk_mul_f32 v[8:9], v[2:3], v[148:149] op_sel_hi:[0,1]
	v_cvt_pk_bf16_f32 v6, v6, v7
	v_cvt_pk_bf16_f32 v7, v8, v9
	v_cvt_pk_bf16_f32 v8, v14, v15
	v_cvt_pk_bf16_f32 v9, v12, v13
	global_store_dwordx4 v[10:11], v[6:9], off sc1
	v_pk_mul_f32 v[12:13], v[2:3], v[128:129] op_sel_hi:[0,1]
	v_pk_mul_f32 v[14:15], v[2:3], v[126:127] op_sel_hi:[0,1]
	v_pk_mul_f32 v[6:7], v[2:3], v[134:135] op_sel_hi:[0,1]
	v_pk_mul_f32 v[8:9], v[2:3], v[136:137] op_sel_hi:[0,1]
	v_cvt_pk_bf16_f32 v6, v6, v7
	v_cvt_pk_bf16_f32 v7, v8, v9
	v_cvt_pk_bf16_f32 v8, v14, v15
	v_cvt_pk_bf16_f32 v9, v12, v13
	global_store_dwordx4 v[10:11], v[6:9], off offset:256 sc1
	v_pk_mul_f32 v[12:13], v[2:3], v[124:125] op_sel_hi:[0,1]
	v_pk_mul_f32 v[14:15], v[2:3], v[122:123] op_sel_hi:[0,1]
	v_or_b32_e32 v6, 32, v3
	v_mad_i64_i32 v[6:7], s[56:57], s26, v6, 0
	v_lshl_add_u64 v[10:11], v[6:7], 1, v[4:5]
	v_pk_mul_f32 v[6:7], v[2:3], v[130:131] op_sel_hi:[0,1]
	v_pk_mul_f32 v[8:9], v[2:3], v[132:133] op_sel_hi:[0,1]
	v_cvt_pk_bf16_f32 v6, v6, v7
	v_cvt_pk_bf16_f32 v7, v8, v9
	v_cvt_pk_bf16_f32 v8, v14, v15
	v_cvt_pk_bf16_f32 v9, v12, v13
	global_store_dwordx4 v[10:11], v[6:9], off sc1
	v_pk_mul_f32 v[12:13], v[2:3], v[112:113] op_sel_hi:[0,1]
	v_pk_mul_f32 v[14:15], v[2:3], v[110:111] op_sel_hi:[0,1]
	v_pk_mul_f32 v[6:7], v[2:3], v[118:119] op_sel_hi:[0,1]
	v_pk_mul_f32 v[8:9], v[2:3], v[120:121] op_sel_hi:[0,1]
	v_cvt_pk_bf16_f32 v6, v6, v7
	v_cvt_pk_bf16_f32 v7, v8, v9
	v_cvt_pk_bf16_f32 v8, v14, v15
	v_cvt_pk_bf16_f32 v9, v12, v13
	global_store_dwordx4 v[10:11], v[6:9], off offset:256 sc1
	v_pk_mul_f32 v[12:13], v[2:3], v[108:109] op_sel_hi:[0,1]
	v_pk_mul_f32 v[14:15], v[2:3], v[106:107] op_sel_hi:[0,1]
	v_or_b32_e32 v6, 48, v3
	v_mad_i64_i32 v[6:7], s[56:57], s26, v6, 0
	v_lshl_add_u64 v[10:11], v[6:7], 1, v[4:5]
	v_pk_mul_f32 v[6:7], v[2:3], v[114:115] op_sel_hi:[0,1]
	v_pk_mul_f32 v[8:9], v[2:3], v[116:117] op_sel_hi:[0,1]
	v_cvt_pk_bf16_f32 v6, v6, v7
	v_cvt_pk_bf16_f32 v7, v8, v9
	v_cvt_pk_bf16_f32 v8, v14, v15
	v_cvt_pk_bf16_f32 v9, v12, v13
	global_store_dwordx4 v[10:11], v[6:9], off sc1
	v_pk_mul_f32 v[12:13], v[2:3], v[100:101] op_sel_hi:[0,1]
	v_pk_mul_f32 v[14:15], v[2:3], v[98:99] op_sel_hi:[0,1]
	v_pk_mul_f32 v[6:7], v[2:3], v[102:103] op_sel_hi:[0,1]
	v_pk_mul_f32 v[8:9], v[2:3], v[104:105] op_sel_hi:[0,1]
	v_cvt_pk_bf16_f32 v6, v6, v7
	v_cvt_pk_bf16_f32 v7, v8, v9
	v_cvt_pk_bf16_f32 v8, v14, v15
	v_cvt_pk_bf16_f32 v9, v12, v13
	global_store_dwordx4 v[10:11], v[6:9], off offset:256 sc1
	v_pk_mul_f32 v[12:13], v[2:3], v[92:93] op_sel_hi:[0,1]
	v_pk_mul_f32 v[14:15], v[2:3], v[90:91] op_sel_hi:[0,1]
	v_add_u32_e32 v6, 0x80, v3
	v_mad_i64_i32 v[6:7], s[56:57], s26, v6, 0
	v_lshl_add_u64 v[10:11], v[6:7], 1, v[4:5]
	v_pk_mul_f32 v[6:7], v[2:3], v[94:95] op_sel_hi:[0,1]
	v_pk_mul_f32 v[8:9], v[2:3], v[96:97] op_sel_hi:[0,1]
	v_cvt_pk_bf16_f32 v6, v6, v7
	v_cvt_pk_bf16_f32 v7, v8, v9
	v_cvt_pk_bf16_f32 v8, v14, v15
	v_cvt_pk_bf16_f32 v9, v12, v13
	global_store_dwordx4 v[10:11], v[6:9], off sc1
	v_pk_mul_f32 v[12:13], v[2:3], v[80:81] op_sel_hi:[0,1]
	v_pk_mul_f32 v[14:15], v[2:3], v[78:79] op_sel_hi:[0,1]
	v_pk_mul_f32 v[6:7], v[2:3], v[86:87] op_sel_hi:[0,1]
	v_pk_mul_f32 v[8:9], v[2:3], v[88:89] op_sel_hi:[0,1]
	v_cvt_pk_bf16_f32 v6, v6, v7
	v_cvt_pk_bf16_f32 v7, v8, v9
	v_cvt_pk_bf16_f32 v8, v14, v15
	v_cvt_pk_bf16_f32 v9, v12, v13
	global_store_dwordx4 v[10:11], v[6:9], off offset:256 sc1
	v_pk_mul_f32 v[12:13], v[2:3], v[76:77] op_sel_hi:[0,1]
	v_pk_mul_f32 v[14:15], v[2:3], v[74:75] op_sel_hi:[0,1]
	v_add_u32_e32 v6, 0x90, v3
	v_mad_i64_i32 v[6:7], s[56:57], s26, v6, 0
	v_lshl_add_u64 v[10:11], v[6:7], 1, v[4:5]
	v_pk_mul_f32 v[6:7], v[2:3], v[82:83] op_sel_hi:[0,1]
	v_pk_mul_f32 v[8:9], v[2:3], v[84:85] op_sel_hi:[0,1]
	v_cvt_pk_bf16_f32 v6, v6, v7
	v_cvt_pk_bf16_f32 v7, v8, v9
	v_cvt_pk_bf16_f32 v8, v14, v15
	v_cvt_pk_bf16_f32 v9, v12, v13
	global_store_dwordx4 v[10:11], v[6:9], off sc1
	v_pk_mul_f32 v[12:13], v[2:3], v[64:65] op_sel_hi:[0,1]
	v_pk_mul_f32 v[14:15], v[2:3], v[62:63] op_sel_hi:[0,1]
	v_pk_mul_f32 v[6:7], v[2:3], v[70:71] op_sel_hi:[0,1]
	v_pk_mul_f32 v[8:9], v[2:3], v[72:73] op_sel_hi:[0,1]
	v_cvt_pk_bf16_f32 v6, v6, v7
	v_cvt_pk_bf16_f32 v7, v8, v9
	v_cvt_pk_bf16_f32 v8, v14, v15
	v_cvt_pk_bf16_f32 v9, v12, v13
	global_store_dwordx4 v[10:11], v[6:9], off offset:256 sc1
	v_pk_mul_f32 v[12:13], v[2:3], v[60:61] op_sel_hi:[0,1]
	v_pk_mul_f32 v[14:15], v[2:3], v[58:59] op_sel_hi:[0,1]
	v_add_u32_e32 v6, 0xa0, v3
	v_mad_i64_i32 v[6:7], s[56:57], s26, v6, 0
	v_lshl_add_u64 v[10:11], v[6:7], 1, v[4:5]
	v_pk_mul_f32 v[6:7], v[2:3], v[66:67] op_sel_hi:[0,1]
	v_pk_mul_f32 v[8:9], v[2:3], v[68:69] op_sel_hi:[0,1]
	v_cvt_pk_bf16_f32 v6, v6, v7
	v_cvt_pk_bf16_f32 v7, v8, v9
	v_cvt_pk_bf16_f32 v8, v14, v15
	v_cvt_pk_bf16_f32 v9, v12, v13
	global_store_dwordx4 v[10:11], v[6:9], off sc1
	v_pk_mul_f32 v[12:13], v[2:3], v[48:49] op_sel_hi:[0,1]
	v_pk_mul_f32 v[14:15], v[2:3], v[46:47] op_sel_hi:[0,1]
	v_pk_mul_f32 v[6:7], v[2:3], v[54:55] op_sel_hi:[0,1]
	v_pk_mul_f32 v[8:9], v[2:3], v[56:57] op_sel_hi:[0,1]
	v_cvt_pk_bf16_f32 v6, v6, v7
	v_cvt_pk_bf16_f32 v7, v8, v9
	v_add_u32_e32 v3, 0xb0, v3
	v_cvt_pk_bf16_f32 v8, v14, v15
	v_cvt_pk_bf16_f32 v9, v12, v13
	global_store_dwordx4 v[10:11], v[6:9], off offset:256 sc1
	v_pk_mul_f32 v[10:11], v[2:3], v[44:45] op_sel_hi:[0,1]
	v_pk_mul_f32 v[12:13], v[2:3], v[42:43] op_sel_hi:[0,1]
	v_mad_i64_i32 v[6:7], s[26:27], s26, v3, 0
	v_lshl_add_u64 v[8:9], v[6:7], 1, v[4:5]
	v_pk_mul_f32 v[4:5], v[2:3], v[50:51] op_sel_hi:[0,1]
	v_pk_mul_f32 v[6:7], v[2:3], v[52:53] op_sel_hi:[0,1]
	v_cvt_pk_bf16_f32 v4, v4, v5
	v_cvt_pk_bf16_f32 v5, v6, v7
	v_cvt_pk_bf16_f32 v6, v12, v13
	v_cvt_pk_bf16_f32 v7, v10, v11
	global_store_dwordx4 v[8:9], v[4:7], off sc1
	s_andn2_b64 vcc, exec, s[0:1]
	s_mov_b64 s[0:1], -1
	v_pk_mul_f32 v[4:5], v[2:3], v[40:41] op_sel_hi:[0,1]
	v_pk_mul_f32 v[6:7], v[2:3], v[38:39] op_sel_hi:[0,1]
	v_pk_mul_f32 v[10:11], v[2:3], v[36:37] op_sel_hi:[0,1]
	v_pk_mul_f32 v[12:13], v[2:3], v[34:35] op_sel_hi:[0,1]
	v_cvt_pk_bf16_f32 v2, v6, v7
	v_cvt_pk_bf16_f32 v3, v4, v5
	v_cvt_pk_bf16_f32 v4, v12, v13
	v_cvt_pk_bf16_f32 v5, v10, v11
	global_store_dwordx4 v[8:9], v[2:5], off offset:256 sc1
	s_cbranch_vccnz .LBB0_977
	s_andn2_b64 vcc, exec, s[12:13]
	s_cbranch_vccnz .LBB0_976
	s_barrier
	s_branch .LBB0_976

.LBB0_1195:
	v_lshl_or_b32 v146, s2, 8, v198
	v_ashrrev_i32_e32 v147, 31, v146
	v_lshl_add_u64 v[66:67], v[146:147], 2, s[42:43]
	global_load_dwordx4 v[86:89], v[66:67], off
	global_load_dwordx4 v[82:85], v[66:67], off offset:16
	global_load_dwordx4 v[70:73], v[66:67], off offset:512
	s_nop 0
	global_load_dwordx4 v[66:69], v[66:67], off offset:528
	v_lshl_add_u32 v186, s54, 8, v196
	v_ashrrev_i32_e32 v187, 31, v186
	v_lshlrev_b64 v[184:185], 1, v[146:147]
	v_lshlrev_b64 v[146:147], 11, v[186:187]
	v_lshl_add_u64 v[188:189], s[4:5], 0, v[184:185]
	v_lshl_add_u64 v[146:147], v[188:189], 0, v[146:147]
	global_load_dwordx4 v[202:205], v[146:147], off
	global_load_dwordx4 v[166:169], v[146:147], off offset:256
	v_or_b32_e32 v194, 16, v186
	v_or_b32_e32 v192, 32, v186
	v_or_b32_e32 v190, 48, v186
	v_ashrrev_i32_e32 v195, 31, v194
	v_ashrrev_i32_e32 v193, 31, v192
	v_readlane_b32 s26, v254, 58
	v_ashrrev_i32_e32 v191, 31, v190
	v_lshlrev_b64 v[146:147], 12, v[186:187]
	v_lshlrev_b64 v[148:149], 11, v[194:195]
	v_lshlrev_b64 v[150:151], 11, v[192:193]
	v_readlane_b32 s27, v254, 59
	v_lshlrev_b64 v[152:153], 11, v[190:191]
	v_lshl_add_u64 v[148:149], v[188:189], 0, v[148:149]
	v_lshl_add_u64 v[146:147], s[26:27], 0, v[146:147]
	v_lshl_add_u64 v[150:151], v[188:189], 0, v[150:151]
	v_lshl_add_u64 v[210:211], v[188:189], 0, v[152:153]
	v_lshl_add_u64 v[212:213], v[146:147], 0, v[184:185]
	global_load_dwordx4 v[206:209], v[148:149], off
	global_load_dwordx4 v[162:165], v[148:149], off offset:256
	global_load_dwordx4 v[158:161], v[150:151], off
	global_load_dwordx4 v[154:157], v[150:151], off offset:256
	s_nop 0
	global_load_dwordx4 v[150:153], v[210:211], off
	global_load_dwordx4 v[146:149], v[210:211], off offset:256
	s_andn2_b64 vcc, exec, s[0:1]
	s_mov_b64 s[0:1], -1
	s_waitcnt vmcnt(0)
	v_pk_add_f32 v[142:143], v[142:143], v[86:87]
	v_pk_add_f32 v[144:145], v[144:145], v[88:89]
	v_pk_add_f32 v[140:141], v[140:141], v[84:85]
	v_pk_add_f32 v[214:215], v[130:131], v[66:67]
	v_pk_mul_f32 v[130:131], v[142:143], s[38:39] op_sel_hi:[1,0]
	v_pk_add_f32 v[138:139], v[138:139], v[82:83]
	v_pk_add_f32 v[210:211], v[132:133], v[68:69]
	v_pk_mul_f32 v[132:133], v[144:145], s[38:39] op_sel_hi:[1,0]
	v_exp_f32_e32 v130, v130
	v_exp_f32_e32 v131, v131
	v_pk_mul_f32 v[138:139], v[138:139], s[38:39] op_sel_hi:[1,0]
	v_pk_mul_f32 v[140:141], v[140:141], s[38:39] op_sel_hi:[1,0]
	v_exp_f32_e32 v132, v132
	v_exp_f32_e32 v133, v133
	v_exp_f32_e32 v138, v138
	v_exp_f32_e32 v139, v139
	v_exp_f32_e32 v140, v140
	v_exp_f32_e32 v141, v141
	v_pk_add_f32 v[136:137], v[136:137], v[72:73]
	v_pk_add_f32 v[130:131], v[130:131], 1.0 op_sel_hi:[1,0]
	v_pk_mul_f32 v[136:137], v[136:137], s[38:39] op_sel_hi:[1,0]
	v_pk_add_f32 v[132:133], v[132:133], 1.0 op_sel_hi:[1,0]
	v_rcp_f32_e32 v130, v130
	v_rcp_f32_e32 v131, v131
	v_exp_f32_e32 v136, v136
	v_exp_f32_e32 v137, v137
	v_pk_add_f32 v[138:139], v[138:139], 1.0 op_sel_hi:[1,0]
	v_pk_add_f32 v[140:141], v[140:141], 1.0 op_sel_hi:[1,0]
	v_rcp_f32_e32 v132, v132
	v_rcp_f32_e32 v133, v133
	v_rcp_f32_e32 v138, v138
	v_rcp_f32_e32 v139, v139
	v_rcp_f32_e32 v140, v140
	v_rcp_f32_e32 v141, v141
	v_lshlrev_b32_e32 v142, 16, v202
	v_and_b32_e32 v143, 0xffff0000, v202
	v_lshlrev_b32_e32 v144, 16, v203
	v_and_b32_e32 v145, 0xffff0000, v203
	v_pk_mul_f32 v[130:131], v[142:143], v[130:131]
	v_pk_add_f32 v[134:135], v[134:135], v[70:71]
	v_lshlrev_b32_e32 v202, 16, v204
	v_and_b32_e32 v203, 0xffff0000, v204
	v_lshlrev_b32_e32 v204, 16, v205
	v_and_b32_e32 v205, 0xffff0000, v205
	v_pk_add_f32 v[136:137], v[136:137], 1.0 op_sel_hi:[1,0]
	v_pk_mul_f32 v[132:133], v[144:145], v[132:133]
	v_cvt_pk_bf16_f32 v130, v130, v131
	v_pk_mul_f32 v[134:135], v[134:135], s[38:39] op_sel_hi:[1,0]
	v_cvt_pk_bf16_f32 v131, v132, v133
	v_pk_mul_f32 v[138:139], v[202:203], v[138:139]
	v_pk_mul_f32 v[140:141], v[204:205], v[140:141]
	v_cvt_pk_bf16_f32 v132, v138, v139
	v_exp_f32_e32 v134, v134
	v_cvt_pk_bf16_f32 v133, v140, v141
	global_store_dwordx4 v[212:213], v[130:133], off offset:2048 sc1
	v_exp_f32_e32 v135, v135
	v_pk_mul_f32 v[138:139], v[210:211], s[38:39] op_sel_hi:[1,0]
	v_rcp_f32_e32 v130, v136
	v_rcp_f32_e32 v131, v137
	v_pk_mul_f32 v[136:137], v[214:215], s[38:39] op_sel_hi:[1,0]
	v_pk_add_f32 v[126:127], v[126:127], v[86:87]
	v_exp_f32_e32 v136, v136
	v_exp_f32_e32 v137, v137
	v_exp_f32_e32 v138, v138
	v_exp_f32_e32 v139, v139
	v_pk_add_f32 v[122:123], v[122:123], v[82:83]
	v_pk_mul_f32 v[126:127], v[126:127], s[38:39] op_sel_hi:[1,0]
	v_pk_mul_f32 v[122:123], v[122:123], s[38:39] op_sel_hi:[1,0]
	v_exp_f32_e32 v126, v126
	v_exp_f32_e32 v127, v127
	v_pk_add_f32 v[128:129], v[128:129], v[88:89]
	v_exp_f32_e32 v122, v122
	v_exp_f32_e32 v123, v123
	v_pk_add_f32 v[134:135], v[134:135], 1.0 op_sel_hi:[1,0]
	v_pk_add_f32 v[136:137], v[136:137], 1.0 op_sel_hi:[1,0]
	v_pk_add_f32 v[124:125], v[124:125], v[84:85]
	v_pk_mul_f32 v[128:129], v[128:129], s[38:39] op_sel_hi:[1,0]
	v_rcp_f32_e32 v134, v134
	v_rcp_f32_e32 v135, v135
	v_rcp_f32_e32 v136, v136
	v_rcp_f32_e32 v137, v137
	v_pk_add_f32 v[138:139], v[138:139], 1.0 op_sel_hi:[1,0]
	v_exp_f32_e32 v128, v128
	v_exp_f32_e32 v129, v129
	v_pk_mul_f32 v[124:125], v[124:125], s[38:39] op_sel_hi:[1,0]
	v_pk_add_f32 v[118:119], v[118:119], v[70:71]
	v_rcp_f32_e32 v138, v138
	v_rcp_f32_e32 v139, v139
	v_pk_add_f32 v[126:127], v[126:127], 1.0 op_sel_hi:[1,0]
	v_exp_f32_e32 v124, v124
	v_exp_f32_e32 v125, v125
	v_pk_add_f32 v[120:121], v[120:121], v[72:73]
	v_pk_add_f32 v[114:115], v[114:115], v[66:67]
	v_pk_mul_f32 v[118:119], v[118:119], s[38:39] op_sel_hi:[1,0]
	v_lshlrev_b32_e32 v132, 16, v167
	v_and_b32_e32 v133, 0xffff0000, v167
	v_rcp_f32_e32 v126, v126
	v_rcp_f32_e32 v127, v127
	v_pk_add_f32 v[122:123], v[122:123], 1.0 op_sel_hi:[1,0]
	v_pk_add_f32 v[116:117], v[116:117], v[68:69]
	v_exp_f32_e32 v118, v118
	v_exp_f32_e32 v119, v119
	v_pk_mul_f32 v[120:121], v[120:121], s[38:39] op_sel_hi:[1,0]
	v_pk_mul_f32 v[114:115], v[114:115], s[38:39] op_sel_hi:[1,0]
	v_lshlrev_b32_e32 v216, 16, v166
	v_and_b32_e32 v217, 0xffff0000, v166
	v_pk_mul_f32 v[132:133], v[132:133], v[130:131]
	v_lshlrev_b32_e32 v130, 16, v168
	v_and_b32_e32 v131, 0xffff0000, v168
	v_rcp_f32_e32 v122, v122
	v_rcp_f32_e32 v123, v123
	v_exp_f32_e32 v120, v120
	v_exp_f32_e32 v121, v121
	v_exp_f32_e32 v114, v114
	v_exp_f32_e32 v115, v115
	v_pk_mul_f32 v[116:117], v[116:117], s[38:39] op_sel_hi:[1,0]
	v_pk_add_f32 v[110:111], v[110:111], v[86:87]
	v_pk_mul_f32 v[134:135], v[216:217], v[134:135]
	v_lshlrev_b32_e32 v140, 16, v169
	v_and_b32_e32 v141, 0xffff0000, v169
	v_pk_mul_f32 v[136:137], v[130:131], v[136:137]
	v_cvt_pk_bf16_f32 v130, v134, v135
	v_cvt_pk_bf16_f32 v131, v132, v133
	v_pk_add_f32 v[128:129], v[128:129], 1.0 op_sel_hi:[1,0]
	v_exp_f32_e32 v116, v116
	v_exp_f32_e32 v117, v117
	v_pk_add_f32 v[106:107], v[106:107], v[82:83]
	v_pk_mul_f32 v[110:111], v[110:111], s[38:39] op_sel_hi:[1,0]
	v_pk_mul_f32 v[138:139], v[140:141], v[138:139]
	v_cvt_pk_bf16_f32 v132, v136, v137
	v_rcp_f32_e32 v128, v128
	v_cvt_pk_bf16_f32 v133, v138, v139
	global_store_dwordx4 v[212:213], v[130:133], off offset:2304 sc1
	v_rcp_f32_e32 v129, v129
	v_pk_add_f32 v[124:125], v[124:125], 1.0 op_sel_hi:[1,0]
	v_lshlrev_b32_e32 v130, 16, v206
	v_and_b32_e32 v131, 0xffff0000, v206
	v_exp_f32_e32 v110, v110
	v_exp_f32_e32 v111, v111
	v_pk_mul_f32 v[106:107], v[106:107], s[38:39] op_sel_hi:[1,0]
	v_pk_mul_f32 v[126:127], v[126:127], v[130:131]
	v_lshlrev_b32_e32 v130, 16, v208
	v_and_b32_e32 v131, 0xffff0000, v208
	v_rcp_f32_e32 v124, v124
	v_rcp_f32_e32 v125, v125
	v_pk_add_f32 v[118:119], v[118:119], 1.0 op_sel_hi:[1,0]
	v_pk_add_f32 v[112:113], v[112:113], v[88:89]
	v_exp_f32_e32 v106, v106
	v_exp_f32_e32 v107, v107
	v_pk_mul_f32 v[130:131], v[122:123], v[130:131]
	v_cvt_pk_bf16_f32 v122, v126, v127
	v_lshlrev_b64 v[126:127], 12, v[194:195]
	v_rcp_f32_e32 v118, v118
	v_rcp_f32_e32 v119, v119
	v_pk_add_f32 v[120:121], v[120:121], 1.0 op_sel_hi:[1,0]
	v_pk_add_f32 v[114:115], v[114:115], 1.0 op_sel_hi:[1,0]
	v_pk_add_f32 v[108:109], v[108:109], v[84:85]
	v_pk_mul_f32 v[112:113], v[112:113], s[38:39] op_sel_hi:[1,0]
	v_lshlrev_b32_e32 v132, 16, v207
	v_and_b32_e32 v133, 0xffff0000, v207
	v_lshl_add_u64 v[126:127], s[26:27], 0, v[126:127]
	v_rcp_f32_e32 v120, v120
	v_rcp_f32_e32 v121, v121
	v_rcp_f32_e32 v114, v114
	v_rcp_f32_e32 v115, v115
	v_pk_add_f32 v[116:117], v[116:117], 1.0 op_sel_hi:[1,0]
	v_exp_f32_e32 v112, v112
	v_exp_f32_e32 v113, v113
	v_pk_mul_f32 v[108:109], v[108:109], s[38:39] op_sel_hi:[1,0]
	v_pk_add_f32 v[102:103], v[102:103], v[70:71]
	v_pk_mul_f32 v[128:129], v[128:129], v[132:133]
	v_lshlrev_b32_e32 v132, 16, v209
	v_and_b32_e32 v133, 0xffff0000, v209
	v_cvt_pk_bf16_f32 v123, v128, v129
	v_lshl_add_u64 v[126:127], v[126:127], 0, v[184:185]
	v_rcp_f32_e32 v116, v116
	v_rcp_f32_e32 v117, v117
	v_pk_add_f32 v[110:111], v[110:111], 1.0 op_sel_hi:[1,0]
	v_exp_f32_e32 v108, v108
	v_exp_f32_e32 v109, v109
	v_pk_add_f32 v[104:105], v[104:105], v[72:73]
	v_pk_add_f32 v[98:99], v[98:99], v[66:67]
	v_pk_mul_f32 v[102:103], v[102:103], s[38:39] op_sel_hi:[1,0]
	v_pk_mul_f32 v[132:133], v[124:125], v[132:133]
	v_cvt_pk_bf16_f32 v124, v130, v131
	v_rcp_f32_e32 v110, v110
	v_cvt_pk_bf16_f32 v125, v132, v133
	global_store_dwordx4 v[126:127], v[122:125], off offset:2048 sc1
	v_rcp_f32_e32 v111, v111
	v_pk_add_f32 v[106:107], v[106:107], 1.0 op_sel_hi:[1,0]
	v_lshlrev_b32_e32 v122, 16, v162
	v_and_b32_e32 v123, 0xffff0000, v162
	v_pk_add_f32 v[100:101], v[100:101], v[68:69]
	v_exp_f32_e32 v102, v102
	v_exp_f32_e32 v103, v103
	v_pk_mul_f32 v[104:105], v[104:105], s[38:39] op_sel_hi:[1,0]
	v_pk_mul_f32 v[98:99], v[98:99], s[38:39] op_sel_hi:[1,0]
	v_lshlrev_b32_e32 v124, 16, v163
	v_and_b32_e32 v125, 0xffff0000, v163
	v_pk_mul_f32 v[118:119], v[118:119], v[122:123]
	v_lshlrev_b32_e32 v122, 16, v164
	v_and_b32_e32 v123, 0xffff0000, v164
	v_rcp_f32_e32 v106, v106
	v_rcp_f32_e32 v107, v107
	v_exp_f32_e32 v104, v104
	v_exp_f32_e32 v105, v105
	v_exp_f32_e32 v98, v98
	v_exp_f32_e32 v99, v99
	v_pk_mul_f32 v[100:101], v[100:101], s[38:39] op_sel_hi:[1,0]
	v_pk_add_f32 v[94:95], v[94:95], v[86:87]
	v_pk_mul_f32 v[120:121], v[120:121], v[124:125]
	v_lshlrev_b32_e32 v124, 16, v165
	v_and_b32_e32 v125, 0xffff0000, v165
	v_pk_mul_f32 v[122:123], v[122:123], v[114:115]
	v_cvt_pk_bf16_f32 v114, v118, v119
	v_cvt_pk_bf16_f32 v115, v120, v121
	v_pk_add_f32 v[112:113], v[112:113], 1.0 op_sel_hi:[1,0]
	v_exp_f32_e32 v100, v100
	v_exp_f32_e32 v101, v101
	v_pk_add_f32 v[90:91], v[90:91], v[82:83]
	v_pk_mul_f32 v[94:95], v[94:95], s[38:39] op_sel_hi:[1,0]
	v_pk_mul_f32 v[124:125], v[124:125], v[116:117]
	v_cvt_pk_bf16_f32 v116, v122, v123
	v_rcp_f32_e32 v112, v112
	v_cvt_pk_bf16_f32 v117, v124, v125
	global_store_dwordx4 v[126:127], v[114:117], off offset:2304 sc1
	v_rcp_f32_e32 v113, v113
	v_pk_add_f32 v[108:109], v[108:109], 1.0 op_sel_hi:[1,0]
	v_lshlrev_b32_e32 v114, 16, v158
	v_and_b32_e32 v115, 0xffff0000, v158
	v_exp_f32_e32 v94, v94
	v_exp_f32_e32 v95, v95
	v_pk_mul_f32 v[90:91], v[90:91], s[38:39] op_sel_hi:[1,0]
	v_pk_mul_f32 v[110:111], v[110:111], v[114:115]
	v_lshlrev_b32_e32 v114, 16, v160
	v_and_b32_e32 v115, 0xffff0000, v160
	v_rcp_f32_e32 v108, v108
	v_rcp_f32_e32 v109, v109
	v_pk_add_f32 v[102:103], v[102:103], 1.0 op_sel_hi:[1,0]
	v_pk_add_f32 v[96:97], v[96:97], v[88:89]
	v_exp_f32_e32 v90, v90
	v_exp_f32_e32 v91, v91
	v_pk_mul_f32 v[114:115], v[106:107], v[114:115]
	v_cvt_pk_bf16_f32 v106, v110, v111
	v_lshlrev_b64 v[110:111], 12, v[192:193]
	v_rcp_f32_e32 v102, v102
	v_rcp_f32_e32 v103, v103
	v_pk_add_f32 v[104:105], v[104:105], 1.0 op_sel_hi:[1,0]
	v_pk_add_f32 v[98:99], v[98:99], 1.0 op_sel_hi:[1,0]
	v_pk_add_f32 v[92:93], v[92:93], v[84:85]
	v_pk_mul_f32 v[96:97], v[96:97], s[38:39] op_sel_hi:[1,0]
	v_lshlrev_b32_e32 v116, 16, v159
	v_and_b32_e32 v117, 0xffff0000, v159
	v_lshl_add_u64 v[110:111], s[26:27], 0, v[110:111]
	v_rcp_f32_e32 v104, v104
	v_rcp_f32_e32 v105, v105
	v_rcp_f32_e32 v98, v98
	v_rcp_f32_e32 v99, v99
	v_pk_add_f32 v[100:101], v[100:101], 1.0 op_sel_hi:[1,0]
	v_exp_f32_e32 v96, v96
	v_exp_f32_e32 v97, v97
	v_pk_mul_f32 v[92:93], v[92:93], s[38:39] op_sel_hi:[1,0]
	v_pk_add_f32 v[78:79], v[78:79], v[70:71]
	v_pk_mul_f32 v[112:113], v[112:113], v[116:117]
	v_lshlrev_b32_e32 v116, 16, v161
	v_and_b32_e32 v117, 0xffff0000, v161
	v_cvt_pk_bf16_f32 v107, v112, v113
	v_lshl_add_u64 v[110:111], v[110:111], 0, v[184:185]
	v_rcp_f32_e32 v100, v100
	v_rcp_f32_e32 v101, v101
	v_pk_add_f32 v[94:95], v[94:95], 1.0 op_sel_hi:[1,0]
	v_exp_f32_e32 v92, v92
	v_exp_f32_e32 v93, v93
	v_pk_add_f32 v[74:75], v[74:75], v[66:67]
	v_pk_mul_f32 v[78:79], v[78:79], s[38:39] op_sel_hi:[1,0]
	v_pk_mul_f32 v[116:117], v[108:109], v[116:117]
	v_cvt_pk_bf16_f32 v108, v114, v115
	v_rcp_f32_e32 v94, v94
	v_cvt_pk_bf16_f32 v109, v116, v117
	global_store_dwordx4 v[110:111], v[106:109], off offset:2048 sc1
	v_rcp_f32_e32 v95, v95
	v_pk_add_f32 v[90:91], v[90:91], 1.0 op_sel_hi:[1,0]
	v_lshlrev_b32_e32 v106, 16, v154
	v_and_b32_e32 v107, 0xffff0000, v154
	v_pk_add_f32 v[80:81], v[80:81], v[72:73]
	v_exp_f32_e32 v78, v78
	v_exp_f32_e32 v79, v79
	v_pk_mul_f32 v[74:75], v[74:75], s[38:39] op_sel_hi:[1,0]
	v_lshlrev_b32_e32 v108, 16, v155
	v_and_b32_e32 v109, 0xffff0000, v155
	v_pk_mul_f32 v[102:103], v[102:103], v[106:107]
	v_lshlrev_b32_e32 v106, 16, v156
	v_and_b32_e32 v107, 0xffff0000, v156
	v_rcp_f32_e32 v90, v90
	v_rcp_f32_e32 v91, v91
	v_pk_add_f32 v[76:77], v[76:77], v[68:69]
	v_pk_mul_f32 v[80:81], v[80:81], s[38:39] op_sel_hi:[1,0]
	v_exp_f32_e32 v74, v74
	v_exp_f32_e32 v75, v75
	v_pk_mul_f32 v[104:105], v[104:105], v[108:109]
	v_lshlrev_b32_e32 v108, 16, v157
	v_and_b32_e32 v109, 0xffff0000, v157
	v_pk_mul_f32 v[106:107], v[98:99], v[106:107]
	v_cvt_pk_bf16_f32 v98, v102, v103
	v_cvt_pk_bf16_f32 v99, v104, v105
	v_pk_add_f32 v[96:97], v[96:97], 1.0 op_sel_hi:[1,0]
	v_exp_f32_e32 v80, v80
	v_exp_f32_e32 v81, v81
	v_pk_mul_f32 v[76:77], v[76:77], s[38:39] op_sel_hi:[1,0]
	v_pk_mul_f32 v[108:109], v[100:101], v[108:109]
	v_cvt_pk_bf16_f32 v100, v106, v107
	v_rcp_f32_e32 v96, v96
	v_cvt_pk_bf16_f32 v101, v108, v109
	global_store_dwordx4 v[110:111], v[98:101], off offset:2304 sc1
	v_rcp_f32_e32 v97, v97
	v_pk_add_f32 v[92:93], v[92:93], 1.0 op_sel_hi:[1,0]
	v_lshlrev_b32_e32 v98, 16, v150
	v_and_b32_e32 v99, 0xffff0000, v150
	v_exp_f32_e32 v76, v76
	v_exp_f32_e32 v77, v77
	v_pk_mul_f32 v[94:95], v[94:95], v[98:99]
	v_lshlrev_b32_e32 v98, 16, v152
	v_and_b32_e32 v99, 0xffff0000, v152
	v_rcp_f32_e32 v92, v92
	v_rcp_f32_e32 v93, v93
	v_pk_add_f32 v[78:79], v[78:79], 1.0 op_sel_hi:[1,0]
	v_pk_mul_f32 v[98:99], v[90:91], v[98:99]
	v_cvt_pk_bf16_f32 v90, v94, v95
	v_lshlrev_b64 v[94:95], 12, v[190:191]
	v_rcp_f32_e32 v78, v78
	v_rcp_f32_e32 v79, v79
	v_pk_add_f32 v[74:75], v[74:75], 1.0 op_sel_hi:[1,0]
	v_lshlrev_b32_e32 v100, 16, v151
	v_and_b32_e32 v101, 0xffff0000, v151
	v_lshl_add_u64 v[94:95], s[26:27], 0, v[94:95]
	v_pk_add_f32 v[80:81], v[80:81], 1.0 op_sel_hi:[1,0]
	v_rcp_f32_e32 v74, v74
	v_rcp_f32_e32 v75, v75
	v_pk_mul_f32 v[96:97], v[96:97], v[100:101]
	v_lshlrev_b32_e32 v100, 16, v153
	v_and_b32_e32 v101, 0xffff0000, v153
	v_cvt_pk_bf16_f32 v91, v96, v97
	v_lshl_add_u64 v[94:95], v[94:95], 0, v[184:185]
	v_rcp_f32_e32 v80, v80
	v_rcp_f32_e32 v81, v81
	v_pk_add_f32 v[76:77], v[76:77], 1.0 op_sel_hi:[1,0]
	v_pk_mul_f32 v[100:101], v[92:93], v[100:101]
	v_cvt_pk_bf16_f32 v92, v98, v99
	v_rcp_f32_e32 v76, v76
	v_cvt_pk_bf16_f32 v93, v100, v101
	global_store_dwordx4 v[94:95], v[90:93], off offset:2048 sc1
	v_rcp_f32_e32 v77, v77
	v_add_u32_e32 v120, 0x80, v186
	v_lshlrev_b32_e32 v90, 16, v146
	v_and_b32_e32 v91, 0xffff0000, v146
	v_pk_mul_f32 v[78:79], v[78:79], v[90:91]
	v_lshlrev_b32_e32 v90, 16, v148
	v_and_b32_e32 v91, 0xffff0000, v148
	v_ashrrev_i32_e32 v121, 31, v120
	v_lshlrev_b32_e32 v92, 16, v147
	v_and_b32_e32 v93, 0xffff0000, v147
	v_pk_mul_f32 v[90:91], v[74:75], v[90:91]
	v_cvt_pk_bf16_f32 v74, v78, v79
	v_lshlrev_b64 v[78:79], 11, v[120:121]
	v_pk_mul_f32 v[80:81], v[80:81], v[92:93]
	v_lshlrev_b32_e32 v92, 16, v149
	v_and_b32_e32 v93, 0xffff0000, v149
	v_lshl_add_u64 v[78:79], v[188:189], 0, v[78:79]
	v_pk_mul_f32 v[92:93], v[76:77], v[92:93]
	v_cvt_pk_bf16_f32 v75, v80, v81
	v_cvt_pk_bf16_f32 v76, v90, v91
	v_add_u32_e32 v110, 0x90, v186
	v_cvt_pk_bf16_f32 v77, v92, v93
	global_load_dwordx4 v[112:115], v[78:79], off
	v_ashrrev_i32_e32 v111, 31, v110
	global_store_dwordx4 v[94:95], v[74:77], off offset:2304 sc1
	global_load_dwordx4 v[116:119], v[78:79], off offset:256
	v_add_u32_e32 v108, 0xa0, v186
	v_lshlrev_b64 v[74:75], 11, v[110:111]
	v_lshl_add_u64 v[74:75], v[188:189], 0, v[74:75]
	global_load_dwordx4 v[102:105], v[74:75], off
	global_load_dwordx4 v[98:101], v[74:75], off offset:256
	v_ashrrev_i32_e32 v109, 31, v108
	v_lshlrev_b64 v[74:75], 11, v[108:109]
	v_lshl_add_u64 v[74:75], v[188:189], 0, v[74:75]
	global_load_dwordx4 v[94:97], v[74:75], off
	global_load_dwordx4 v[90:93], v[74:75], off offset:256
	v_add_u32_e32 v106, 0xb0, v186
	v_ashrrev_i32_e32 v107, 31, v106
	v_lshlrev_b64 v[74:75], 11, v[106:107]
	v_lshl_add_u64 v[74:75], v[188:189], 0, v[74:75]
	global_load_dwordx4 v[78:81], v[74:75], off
	s_nop 0
	global_load_dwordx4 v[74:77], v[74:75], off offset:256
	v_pk_add_f32 v[64:65], v[64:65], v[88:89]
	v_pk_add_f32 v[62:63], v[62:63], v[86:87]
	v_pk_add_f32 v[58:59], v[58:59], v[82:83]
	v_pk_mul_f32 v[62:63], v[62:63], s[38:39] op_sel_hi:[1,0]
	v_pk_mul_f32 v[64:65], v[64:65], s[38:39] op_sel_hi:[1,0]
	v_exp_f32_e32 v62, v62
	v_exp_f32_e32 v63, v63
	v_exp_f32_e32 v64, v64
	v_exp_f32_e32 v65, v65
	v_pk_mul_f32 v[58:59], v[58:59], s[38:39] op_sel_hi:[1,0]
	v_pk_add_f32 v[60:61], v[60:61], v[84:85]
	v_exp_f32_e32 v58, v58
	v_exp_f32_e32 v59, v59
	v_pk_mul_f32 v[60:61], v[60:61], s[38:39] op_sel_hi:[1,0]
	v_pk_add_f32 v[54:55], v[54:55], v[70:71]
	v_pk_add_f32 v[62:63], v[62:63], 1.0 op_sel_hi:[1,0]
	v_pk_add_f32 v[64:65], v[64:65], 1.0 op_sel_hi:[1,0]
	v_exp_f32_e32 v60, v60
	v_exp_f32_e32 v61, v61
	v_pk_add_f32 v[56:57], v[56:57], v[72:73]
	v_pk_add_f32 v[50:51], v[50:51], v[66:67]
	v_pk_mul_f32 v[54:55], v[54:55], s[38:39] op_sel_hi:[1,0]
	v_rcp_f32_e32 v62, v62
	v_rcp_f32_e32 v63, v63
	v_rcp_f32_e32 v64, v64
	v_rcp_f32_e32 v65, v65
	v_pk_add_f32 v[58:59], v[58:59], 1.0 op_sel_hi:[1,0]
	v_pk_add_f32 v[52:53], v[52:53], v[68:69]
	v_exp_f32_e32 v54, v54
	v_exp_f32_e32 v55, v55
	v_pk_mul_f32 v[56:57], v[56:57], s[38:39] op_sel_hi:[1,0]
	v_pk_mul_f32 v[50:51], v[50:51], s[38:39] op_sel_hi:[1,0]
	v_rcp_f32_e32 v58, v58
	v_rcp_f32_e32 v59, v59
	v_exp_f32_e32 v56, v56
	v_exp_f32_e32 v57, v57
	v_exp_f32_e32 v50, v50
	v_exp_f32_e32 v51, v51
	v_pk_mul_f32 v[52:53], v[52:53], s[38:39] op_sel_hi:[1,0]
	v_pk_add_f32 v[46:47], v[46:47], v[86:87]
	v_exp_f32_e32 v52, v52
	v_exp_f32_e32 v53, v53
	v_pk_add_f32 v[42:43], v[42:43], v[82:83]
	v_pk_mul_f32 v[46:47], v[46:47], s[38:39] op_sel_hi:[1,0]
	v_pk_add_f32 v[60:61], v[60:61], 1.0 op_sel_hi:[1,0]
	v_exp_f32_e32 v46, v46
	v_exp_f32_e32 v47, v47
	v_pk_mul_f32 v[42:43], v[42:43], s[38:39] op_sel_hi:[1,0]
	v_rcp_f32_e32 v60, v60
	v_rcp_f32_e32 v61, v61
	v_pk_add_f32 v[54:55], v[54:55], 1.0 op_sel_hi:[1,0]
	v_pk_add_f32 v[48:49], v[48:49], v[88:89]
	v_exp_f32_e32 v42, v42
	v_exp_f32_e32 v43, v43
	v_rcp_f32_e32 v54, v54
	v_rcp_f32_e32 v55, v55
	v_pk_add_f32 v[56:57], v[56:57], 1.0 op_sel_hi:[1,0]
	v_pk_add_f32 v[50:51], v[50:51], 1.0 op_sel_hi:[1,0]
	v_pk_add_f32 v[44:45], v[44:45], v[84:85]
	v_pk_mul_f32 v[48:49], v[48:49], s[38:39] op_sel_hi:[1,0]
	v_rcp_f32_e32 v56, v56
	v_rcp_f32_e32 v57, v57
	v_rcp_f32_e32 v50, v50
	s_waitcnt vmcnt(8)
	v_lshlrev_b32_e32 v122, 16, v112
	v_and_b32_e32 v123, 0xffff0000, v112
	v_lshlrev_b32_e32 v112, 16, v113
	v_and_b32_e32 v113, 0xffff0000, v113
	v_pk_mul_f32 v[62:63], v[62:63], v[122:123]
	v_pk_mul_f32 v[64:65], v[64:65], v[112:113]
	v_lshlrev_b32_e32 v112, 16, v114
	v_and_b32_e32 v113, 0xffff0000, v114
	v_pk_mul_f32 v[112:113], v[58:59], v[112:113]
	v_cvt_pk_bf16_f32 v58, v62, v63
	v_lshlrev_b64 v[62:63], 12, v[120:121]
	v_lshl_add_u64 v[62:63], s[26:27], 0, v[62:63]
	v_rcp_f32_e32 v51, v51
	v_pk_add_f32 v[52:53], v[52:53], 1.0 op_sel_hi:[1,0]
	v_exp_f32_e32 v48, v48
	v_exp_f32_e32 v49, v49
	v_pk_mul_f32 v[44:45], v[44:45], s[38:39] op_sel_hi:[1,0]
	v_pk_add_f32 v[38:39], v[38:39], v[70:71]
	v_lshlrev_b32_e32 v114, 16, v115
	v_and_b32_e32 v115, 0xffff0000, v115
	v_cvt_pk_bf16_f32 v59, v64, v65
	v_lshl_add_u64 v[62:63], v[62:63], 0, v[184:185]
	v_rcp_f32_e32 v52, v52
	v_rcp_f32_e32 v53, v53
	v_pk_add_f32 v[46:47], v[46:47], 1.0 op_sel_hi:[1,0]
	v_exp_f32_e32 v44, v44
	v_exp_f32_e32 v45, v45
	v_pk_add_f32 v[40:41], v[40:41], v[72:73]
	v_pk_add_f32 v[34:35], v[34:35], v[66:67]
	v_pk_mul_f32 v[38:39], v[38:39], s[38:39] op_sel_hi:[1,0]
	v_pk_mul_f32 v[114:115], v[60:61], v[114:115]
	v_cvt_pk_bf16_f32 v60, v112, v113
	v_rcp_f32_e32 v46, v46
	v_cvt_pk_bf16_f32 v61, v114, v115
	global_store_dwordx4 v[62:63], v[58:61], off offset:2048 sc1
	v_rcp_f32_e32 v47, v47
	v_pk_add_f32 v[42:43], v[42:43], 1.0 op_sel_hi:[1,0]
	s_waitcnt vmcnt(7)
	v_lshlrev_b32_e32 v58, 16, v116
	v_and_b32_e32 v59, 0xffff0000, v116
	v_pk_add_f32 v[36:37], v[36:37], v[68:69]
	v_exp_f32_e32 v38, v38
	v_exp_f32_e32 v39, v39
	v_pk_mul_f32 v[40:41], v[40:41], s[38:39] op_sel_hi:[1,0]
	v_pk_mul_f32 v[34:35], v[34:35], s[38:39] op_sel_hi:[1,0]
	v_lshlrev_b32_e32 v60, 16, v117
	v_and_b32_e32 v61, 0xffff0000, v117
	v_pk_mul_f32 v[54:55], v[54:55], v[58:59]
	v_lshlrev_b32_e32 v58, 16, v118
	v_and_b32_e32 v59, 0xffff0000, v118
	v_rcp_f32_e32 v42, v42
	v_rcp_f32_e32 v43, v43
	v_exp_f32_e32 v40, v40
	v_exp_f32_e32 v41, v41
	v_exp_f32_e32 v34, v34
	v_exp_f32_e32 v35, v35
	v_pk_mul_f32 v[36:37], v[36:37], s[38:39] op_sel_hi:[1,0]
	v_pk_add_f32 v[30:31], v[30:31], v[86:87]
	v_pk_mul_f32 v[56:57], v[56:57], v[60:61]
	v_lshlrev_b32_e32 v60, 16, v119
	v_and_b32_e32 v61, 0xffff0000, v119
	v_pk_mul_f32 v[58:59], v[50:51], v[58:59]
	v_cvt_pk_bf16_f32 v50, v54, v55
	v_cvt_pk_bf16_f32 v51, v56, v57
	v_pk_add_f32 v[48:49], v[48:49], 1.0 op_sel_hi:[1,0]
	v_exp_f32_e32 v36, v36
	v_exp_f32_e32 v37, v37
	v_pk_add_f32 v[26:27], v[26:27], v[82:83]
	v_pk_mul_f32 v[30:31], v[30:31], s[38:39] op_sel_hi:[1,0]
	v_pk_mul_f32 v[60:61], v[52:53], v[60:61]
	v_cvt_pk_bf16_f32 v52, v58, v59
	v_rcp_f32_e32 v48, v48
	v_cvt_pk_bf16_f32 v53, v60, v61
	global_store_dwordx4 v[62:63], v[50:53], off offset:2304 sc1
	v_rcp_f32_e32 v49, v49
	v_pk_add_f32 v[44:45], v[44:45], 1.0 op_sel_hi:[1,0]
	s_waitcnt vmcnt(7)
	v_lshlrev_b32_e32 v50, 16, v102
	v_and_b32_e32 v51, 0xffff0000, v102
	v_exp_f32_e32 v30, v30
	v_exp_f32_e32 v31, v31
	v_pk_mul_f32 v[26:27], v[26:27], s[38:39] op_sel_hi:[1,0]
	v_pk_mul_f32 v[46:47], v[46:47], v[50:51]
	v_lshlrev_b32_e32 v50, 16, v104
	v_and_b32_e32 v51, 0xffff0000, v104
	v_rcp_f32_e32 v44, v44
	v_rcp_f32_e32 v45, v45
	v_pk_add_f32 v[38:39], v[38:39], 1.0 op_sel_hi:[1,0]
	v_pk_add_f32 v[32:33], v[32:33], v[88:89]
	v_exp_f32_e32 v26, v26
	v_exp_f32_e32 v27, v27
	v_pk_mul_f32 v[50:51], v[42:43], v[50:51]
	v_cvt_pk_bf16_f32 v42, v46, v47
	v_lshlrev_b64 v[46:47], 12, v[110:111]
	v_rcp_f32_e32 v38, v38
	v_rcp_f32_e32 v39, v39
	v_pk_add_f32 v[40:41], v[40:41], 1.0 op_sel_hi:[1,0]
	v_pk_add_f32 v[34:35], v[34:35], 1.0 op_sel_hi:[1,0]
	v_pk_add_f32 v[28:29], v[28:29], v[84:85]
	v_pk_mul_f32 v[32:33], v[32:33], s[38:39] op_sel_hi:[1,0]
	v_lshlrev_b32_e32 v52, 16, v103
	v_and_b32_e32 v53, 0xffff0000, v103
	v_lshl_add_u64 v[46:47], s[26:27], 0, v[46:47]
	v_rcp_f32_e32 v40, v40
	v_rcp_f32_e32 v41, v41
	v_rcp_f32_e32 v34, v34
	v_rcp_f32_e32 v35, v35
	v_pk_add_f32 v[36:37], v[36:37], 1.0 op_sel_hi:[1,0]
	v_exp_f32_e32 v32, v32
	v_exp_f32_e32 v33, v33
	v_pk_mul_f32 v[28:29], v[28:29], s[38:39] op_sel_hi:[1,0]
	v_pk_add_f32 v[22:23], v[22:23], v[70:71]
	v_pk_mul_f32 v[48:49], v[48:49], v[52:53]
	v_lshlrev_b32_e32 v52, 16, v105
	v_and_b32_e32 v53, 0xffff0000, v105
	v_cvt_pk_bf16_f32 v43, v48, v49
	v_lshl_add_u64 v[46:47], v[46:47], 0, v[184:185]
	v_rcp_f32_e32 v36, v36
	v_rcp_f32_e32 v37, v37
	v_pk_add_f32 v[30:31], v[30:31], 1.0 op_sel_hi:[1,0]
	v_exp_f32_e32 v28, v28
	v_exp_f32_e32 v29, v29
	v_pk_add_f32 v[24:25], v[24:25], v[72:73]
	v_pk_add_f32 v[18:19], v[18:19], v[66:67]
	v_pk_mul_f32 v[22:23], v[22:23], s[38:39] op_sel_hi:[1,0]
	v_pk_mul_f32 v[52:53], v[44:45], v[52:53]
	v_cvt_pk_bf16_f32 v44, v50, v51
	v_rcp_f32_e32 v30, v30
	v_cvt_pk_bf16_f32 v45, v52, v53
	global_store_dwordx4 v[46:47], v[42:45], off offset:2048 sc1
	v_rcp_f32_e32 v31, v31
	v_pk_add_f32 v[26:27], v[26:27], 1.0 op_sel_hi:[1,0]
	s_waitcnt vmcnt(7)
	v_lshlrev_b32_e32 v42, 16, v98
	v_and_b32_e32 v43, 0xffff0000, v98
	v_pk_add_f32 v[20:21], v[20:21], v[68:69]
	v_exp_f32_e32 v22, v22
	v_exp_f32_e32 v23, v23
	v_pk_mul_f32 v[24:25], v[24:25], s[38:39] op_sel_hi:[1,0]
	v_pk_mul_f32 v[18:19], v[18:19], s[38:39] op_sel_hi:[1,0]
	v_lshlrev_b32_e32 v44, 16, v99
	v_and_b32_e32 v45, 0xffff0000, v99
	v_pk_mul_f32 v[38:39], v[38:39], v[42:43]
	v_lshlrev_b32_e32 v42, 16, v100
	v_and_b32_e32 v43, 0xffff0000, v100
	v_rcp_f32_e32 v26, v26
	v_rcp_f32_e32 v27, v27
	v_exp_f32_e32 v24, v24
	v_exp_f32_e32 v25, v25
	v_exp_f32_e32 v18, v18
	v_exp_f32_e32 v19, v19
	v_pk_mul_f32 v[20:21], v[20:21], s[38:39] op_sel_hi:[1,0]
	v_pk_add_f32 v[14:15], v[14:15], v[86:87]
	v_pk_mul_f32 v[40:41], v[40:41], v[44:45]
	v_lshlrev_b32_e32 v44, 16, v101
	v_and_b32_e32 v45, 0xffff0000, v101
	v_pk_mul_f32 v[42:43], v[34:35], v[42:43]
	v_cvt_pk_bf16_f32 v34, v38, v39
	v_cvt_pk_bf16_f32 v35, v40, v41
	v_pk_add_f32 v[32:33], v[32:33], 1.0 op_sel_hi:[1,0]
	v_exp_f32_e32 v20, v20
	v_exp_f32_e32 v21, v21
	v_pk_add_f32 v[10:11], v[10:11], v[82:83]
	v_pk_mul_f32 v[14:15], v[14:15], s[38:39] op_sel_hi:[1,0]
	v_pk_mul_f32 v[44:45], v[36:37], v[44:45]
	v_cvt_pk_bf16_f32 v36, v42, v43
	v_rcp_f32_e32 v32, v32
	v_cvt_pk_bf16_f32 v37, v44, v45
	global_store_dwordx4 v[46:47], v[34:37], off offset:2304 sc1
	v_rcp_f32_e32 v33, v33
	v_pk_add_f32 v[28:29], v[28:29], 1.0 op_sel_hi:[1,0]
	s_waitcnt vmcnt(7)
	v_lshlrev_b32_e32 v34, 16, v94
	v_and_b32_e32 v35, 0xffff0000, v94
	v_pk_add_f32 v[16:17], v[16:17], v[88:89]
	v_exp_f32_e32 v14, v14
	v_exp_f32_e32 v15, v15
	v_pk_mul_f32 v[10:11], v[10:11], s[38:39] op_sel_hi:[1,0]
	v_pk_mul_f32 v[30:31], v[30:31], v[34:35]
	v_lshlrev_b32_e32 v34, 16, v96
	v_and_b32_e32 v35, 0xffff0000, v96
	v_rcp_f32_e32 v28, v28
	v_rcp_f32_e32 v29, v29
	v_pk_add_f32 v[22:23], v[22:23], 1.0 op_sel_hi:[1,0]
	v_pk_add_f32 v[12:13], v[12:13], v[84:85]
	v_pk_mul_f32 v[16:17], v[16:17], s[38:39] op_sel_hi:[1,0]
	v_exp_f32_e32 v10, v10
	v_exp_f32_e32 v11, v11
	v_pk_mul_f32 v[34:35], v[26:27], v[34:35]
	v_cvt_pk_bf16_f32 v26, v30, v31
	v_lshlrev_b64 v[30:31], 12, v[108:109]
	v_rcp_f32_e32 v22, v22
	v_rcp_f32_e32 v23, v23
	v_pk_add_f32 v[24:25], v[24:25], 1.0 op_sel_hi:[1,0]
	v_pk_add_f32 v[18:19], v[18:19], 1.0 op_sel_hi:[1,0]
	v_exp_f32_e32 v16, v16
	v_exp_f32_e32 v17, v17
	v_pk_mul_f32 v[12:13], v[12:13], s[38:39] op_sel_hi:[1,0]
	v_lshlrev_b32_e32 v36, 16, v95
	v_and_b32_e32 v37, 0xffff0000, v95
	v_lshl_add_u64 v[30:31], s[26:27], 0, v[30:31]
	v_rcp_f32_e32 v24, v24
	v_rcp_f32_e32 v25, v25
	v_rcp_f32_e32 v18, v18
	v_rcp_f32_e32 v19, v19
	v_pk_add_f32 v[20:21], v[20:21], 1.0 op_sel_hi:[1,0]
	v_exp_f32_e32 v12, v12
	v_exp_f32_e32 v13, v13
	v_pk_add_f32 v[8:9], v[8:9], v[72:73]
	v_pk_add_f32 v[6:7], v[6:7], v[70:71]
	v_pk_mul_f32 v[32:33], v[32:33], v[36:37]
	v_lshlrev_b32_e32 v36, 16, v97
	v_and_b32_e32 v37, 0xffff0000, v97
	v_cvt_pk_bf16_f32 v27, v32, v33
	v_lshl_add_u64 v[30:31], v[30:31], 0, v[184:185]
	v_rcp_f32_e32 v20, v20
	v_rcp_f32_e32 v21, v21
	v_pk_add_f32 v[14:15], v[14:15], 1.0 op_sel_hi:[1,0]
	v_pk_add_f32 v[4:5], v[4:5], v[68:69]
	v_pk_add_f32 v[2:3], v[2:3], v[66:67]
	v_pk_mul_f32 v[6:7], v[6:7], s[38:39] op_sel_hi:[1,0]
	v_pk_mul_f32 v[8:9], v[8:9], s[38:39] op_sel_hi:[1,0]
	v_pk_mul_f32 v[36:37], v[28:29], v[36:37]
	v_cvt_pk_bf16_f32 v28, v34, v35
	v_rcp_f32_e32 v14, v14
	v_cvt_pk_bf16_f32 v29, v36, v37
	global_store_dwordx4 v[30:31], v[26:29], off offset:2048 sc1
	v_rcp_f32_e32 v15, v15
	v_pk_add_f32 v[10:11], v[10:11], 1.0 op_sel_hi:[1,0]
	s_waitcnt vmcnt(7)
	v_lshlrev_b32_e32 v26, 16, v90
	v_and_b32_e32 v27, 0xffff0000, v90
	v_exp_f32_e32 v6, v6
	v_exp_f32_e32 v7, v7
	v_exp_f32_e32 v8, v8
	v_exp_f32_e32 v9, v9
	v_pk_mul_f32 v[2:3], v[2:3], s[38:39] op_sel_hi:[1,0]
	v_pk_mul_f32 v[4:5], v[4:5], s[38:39] op_sel_hi:[1,0]
	v_lshlrev_b32_e32 v28, 16, v91
	v_and_b32_e32 v29, 0xffff0000, v91
	v_pk_mul_f32 v[22:23], v[22:23], v[26:27]
	v_lshlrev_b32_e32 v26, 16, v92
	v_and_b32_e32 v27, 0xffff0000, v92
	v_pk_add_f32 v[16:17], v[16:17], 1.0 op_sel_hi:[1,0]
	v_rcp_f32_e32 v10, v10
	v_rcp_f32_e32 v11, v11
	v_exp_f32_e32 v2, v2
	v_exp_f32_e32 v3, v3
	v_exp_f32_e32 v4, v4
	v_exp_f32_e32 v5, v5
	v_pk_mul_f32 v[24:25], v[24:25], v[28:29]
	v_lshlrev_b32_e32 v28, 16, v93
	v_and_b32_e32 v29, 0xffff0000, v93
	v_pk_mul_f32 v[26:27], v[18:19], v[26:27]
	v_cvt_pk_bf16_f32 v18, v22, v23
	v_cvt_pk_bf16_f32 v19, v24, v25
	v_rcp_f32_e32 v16, v16
	v_rcp_f32_e32 v17, v17
	v_pk_add_f32 v[12:13], v[12:13], 1.0 op_sel_hi:[1,0]
	v_pk_mul_f32 v[28:29], v[20:21], v[28:29]
	v_cvt_pk_bf16_f32 v20, v26, v27
	v_rcp_f32_e32 v12, v12
	v_cvt_pk_bf16_f32 v21, v28, v29
	global_store_dwordx4 v[30:31], v[18:21], off offset:2304 sc1
	v_rcp_f32_e32 v13, v13
	v_pk_add_f32 v[6:7], v[6:7], 1.0 op_sel_hi:[1,0]
	s_waitcnt vmcnt(7)
	v_lshlrev_b32_e32 v18, 16, v78
	v_and_b32_e32 v19, 0xffff0000, v78
	v_pk_mul_f32 v[14:15], v[14:15], v[18:19]
	v_lshlrev_b32_e32 v18, 16, v80
	v_and_b32_e32 v19, 0xffff0000, v80
	v_pk_add_f32 v[8:9], v[8:9], 1.0 op_sel_hi:[1,0]
	v_lshlrev_b32_e32 v20, 16, v79
	v_and_b32_e32 v21, 0xffff0000, v79
	v_pk_mul_f32 v[18:19], v[10:11], v[18:19]
	v_cvt_pk_bf16_f32 v10, v14, v15
	v_lshlrev_b64 v[14:15], 12, v[106:107]
	v_rcp_f32_e32 v6, v6
	v_rcp_f32_e32 v7, v7
	v_rcp_f32_e32 v8, v8
	v_rcp_f32_e32 v9, v9
	v_pk_add_f32 v[2:3], v[2:3], 1.0 op_sel_hi:[1,0]
	v_pk_add_f32 v[4:5], v[4:5], 1.0 op_sel_hi:[1,0]
	v_pk_mul_f32 v[16:17], v[16:17], v[20:21]
	v_lshlrev_b32_e32 v20, 16, v81
	v_and_b32_e32 v21, 0xffff0000, v81
	v_lshl_add_u64 v[14:15], s[26:27], 0, v[14:15]
	v_rcp_f32_e32 v2, v2
	v_rcp_f32_e32 v3, v3
	v_rcp_f32_e32 v4, v4
	v_rcp_f32_e32 v5, v5
	v_pk_mul_f32 v[20:21], v[12:13], v[20:21]
	v_cvt_pk_bf16_f32 v11, v16, v17
	v_cvt_pk_bf16_f32 v12, v18, v19
	v_lshl_add_u64 v[14:15], v[14:15], 0, v[184:185]
	v_cvt_pk_bf16_f32 v13, v20, v21
	global_store_dwordx4 v[14:15], v[10:13], off offset:2048 sc1
	s_waitcnt vmcnt(7)
	s_nop 0
	v_lshlrev_b32_e32 v10, 16, v74
	v_and_b32_e32 v11, 0xffff0000, v74
	v_lshlrev_b32_e32 v12, 16, v75
	v_and_b32_e32 v13, 0xffff0000, v75
	v_pk_mul_f32 v[6:7], v[6:7], v[10:11]
	v_pk_mul_f32 v[8:9], v[8:9], v[12:13]
	v_lshlrev_b32_e32 v10, 16, v76
	v_and_b32_e32 v11, 0xffff0000, v76
	v_lshlrev_b32_e32 v12, 16, v77
	v_and_b32_e32 v13, 0xffff0000, v77
	v_pk_mul_f32 v[10:11], v[2:3], v[10:11]
	v_pk_mul_f32 v[12:13], v[4:5], v[12:13]
	v_cvt_pk_bf16_f32 v2, v6, v7
	v_cvt_pk_bf16_f32 v3, v8, v9
	v_cvt_pk_bf16_f32 v4, v10, v11
	s_nop 0
	v_cvt_pk_bf16_f32 v5, v12, v13
	global_store_dwordx4 v[14:15], v[2:5], off offset:2304 sc1
	s_cbranch_vccnz .LBB0_1184
	s_andn2_b64 vcc, exec, s[14:15]
	s_cbranch_vccnz .LBB0_1183
	s_barrier
	s_branch .LBB0_1183

.LBB0_1202:
	v_add_u32_e32 v64, s3, v1
	v_cmp_gt_i32_e64 s[6:7], s2, v64
	v_add_u32_e32 v66, s21, v1
	v_cmp_gt_i32_e64 s[4:5], s2, v66
	v_cndmask_b32_e64 v3, v1, v64, s[6:7]
	v_ashrrev_i32_e32 v2, 7, v3
	v_and_b32_e32 v5, 0x7f, v3
	v_ashrrev_i32_e32 v4, 19, v3
	v_lshlrev_b32_e32 v3, 8, v3
	s_waitcnt vmcnt(3)
	v_and_b32_e32 v12, 0x7000, v3
	v_ashrrev_i32_e32 v3, 31, v2
	v_lshlrev_b64 v[6:7], 11, v[2:3]
	v_and_b32_e32 v8, 0xfff, v2
	v_lshl_add_u64 v[6:7], s[12:13], 0, v[6:7]
	v_lshlrev_b32_e32 v38, 4, v5
	v_ashrrev_i32_e32 v5, 31, v4
	v_lshl_add_u64 v[10:11], v[6:7], 0, v[38:39]
	v_or_b32_e32 v3, v12, v8
	v_lshlrev_b64 v[6:7], 18, v[4:5]
	v_lshlrev_b32_e32 v38, 3, v3
	v_lshl_add_u64 v[6:7], s[14:15], 0, v[6:7]
	v_lshl_add_u64 v[6:7], v[6:7], 0, v[38:39]
	global_load_dwordx2 v[46:47], v[6:7], off
	global_load_dwordx4 v[18:21], v[10:11], off
	v_bfe_u32 v3, v2, 2, 10
	v_lshlrev_b32_e32 v6, 10, v2
	v_and_b32_e32 v6, 0xc00, v6
	v_or_b32_e32 v3, v3, v12
	v_lshlrev_b64 v[4:5], 15, v[4:5]
	v_or3_b32 v6, v4, v3, v6
	v_mov_b32_e32 v7, v5
	v_lshl_add_u64 v[6:7], v[6:7], 3, s[14:15]
	v_add_co_u32_e32 v6, vcc, s24, v6
	v_bfe_u32 v3, v2, 4, 8
	v_lshlrev_b32_e32 v2, 8, v2
	v_addc_co_u32_e32 v7, vcc, 0, v7, vcc
	v_and_b32_e32 v2, 0xf00, v2
	v_or_b32_e32 v3, v3, v12
	v_add_co_u32_e32 v8, vcc, s25, v10
	v_or3_b32 v4, v4, v3, v2
	s_nop 0
	v_addc_co_u32_e32 v9, vcc, 0, v11, vcc
	v_lshl_add_u64 v[2:3], v[4:5], 3, s[14:15]
	v_add_co_u32_e32 v2, vcc, s2, v2
	global_load_dwordx2 v[48:49], v[6:7], off
	s_nop 0
	global_load_dwordx4 v[6:9], v[8:9], off
	v_addc_co_u32_e32 v3, vcc, 0, v3, vcc
	v_add_co_u32_e32 v4, vcc, s33, v10
	v_add_u32_e32 v65, s22, v1
	s_nop 0
	v_addc_co_u32_e32 v5, vcc, 0, v11, vcc
	global_load_dwordx2 v[54:55], v[2:3], off
	global_load_dwordx4 v[14:17], v[4:5], off
	v_cndmask_b32_e64 v2, v1, v66, s[4:5]
	v_ashrrev_i32_e32 v10, 7, v2
	v_and_b32_e32 v4, 0x7f, v2
	v_ashrrev_i32_e32 v12, 19, v2
	v_lshlrev_b32_e32 v2, 8, v2
	v_ashrrev_i32_e32 v11, 31, v10
	v_cmp_gt_i32_e64 s[0:1], s2, v65
	v_and_b32_e32 v34, 0x7000, v2
	v_lshlrev_b64 v[2:3], 11, v[10:11]
	s_waitcnt vmcnt(7)
	v_lshlrev_b32_e32 v24, 10, v10
	v_cndmask_b32_e64 v25, v1, v65, s[0:1]
	v_and_b32_e32 v5, 0xfff, v10
	v_lshl_add_u64 v[2:3], s[12:13], 0, v[2:3]
	v_lshlrev_b32_e32 v38, 4, v4
	v_ashrrev_i32_e32 v13, 31, v12
	v_and_b32_e32 v35, 0xc00, v24
	v_ashrrev_i32_e32 v24, 7, v25
	v_and_b32_e32 v28, 0x7f, v25
	v_ashrrev_i32_e32 v52, 19, v25
	v_lshlrev_b32_e32 v25, 8, v25
	v_lshl_add_u64 v[22:23], v[2:3], 0, v[38:39]
	v_or_b32_e32 v4, v34, v5
	v_lshlrev_b64 v[2:3], 18, v[12:13]
	v_and_b32_e32 v67, 0x7000, v25
	v_ashrrev_i32_e32 v25, 31, v24
	v_lshlrev_b32_e32 v38, 3, v4
	v_lshl_add_u64 v[2:3], s[14:15], 0, v[2:3]
	v_lshlrev_b64 v[26:27], 11, v[24:25]
	v_lshl_add_u64 v[2:3], v[2:3], 0, v[38:39]
	v_and_b32_e32 v29, 0xfff, v24
	v_lshl_add_u64 v[26:27], s[12:13], 0, v[26:27]
	v_lshlrev_b32_e32 v38, 4, v28
	v_ashrrev_i32_e32 v53, 31, v52
	v_ashrrev_i32_e32 v28, 19, v1
	v_lshl_add_u64 v[56:57], v[26:27], 0, v[38:39]
	v_or_b32_e32 v25, v67, v29
	v_lshlrev_b64 v[26:27], 18, v[52:53]
	v_ashrrev_i32_e32 v80, 7, v1
	v_ashrrev_i32_e32 v29, 31, v28
	v_lshlrev_b32_e32 v38, 3, v25
	v_lshl_add_u64 v[26:27], s[14:15], 0, v[26:27]
	v_and_b32_e32 v25, 0x3f8, v63
	v_readlane_b32 s18, v254, 58
	v_bfe_u32 v1, v80, 4, 8
	v_lshlrev_b64 v[30:31], 15, v[28:29]
	v_lshl_add_u64 v[26:27], v[26:27], 0, v[38:39]
	v_lshlrev_b32_e32 v38, 1, v25
	v_readlane_b32 s19, v254, 59
	v_or3_b32 v32, v1, v62, v30
	v_lshlrev_b32_e32 v1, 8, v80
	v_lshl_add_u64 v[42:43], s[18:19], 0, v[38:39]
	v_mov_b32_e32 v33, v31
	v_and_b32_e32 v38, 0xf00, v1
	v_bfe_u32 v1, v80, 2, 10
	v_lshl_add_u64 v[32:33], v[32:33], 0, v[38:39]
	v_or3_b32 v30, v1, v62, v30
	v_lshlrev_b32_e32 v1, 10, v80
	v_lshl_add_u64 v[32:33], v[32:33], 3, s[14:15]
	v_and_b32_e32 v38, 0xc00, v1
	v_add_co_u32_e32 v32, vcc, s2, v32
	v_lshl_add_u64 v[30:31], v[30:31], 0, v[38:39]
	s_nop 0
	v_addc_co_u32_e32 v33, vcc, 0, v33, vcc
	v_lshl_add_u64 v[30:31], v[30:31], 3, s[14:15]
	v_add_co_u32_e32 v30, vcc, s24, v30
	v_lshlrev_b64 v[28:29], 18, v[28:29]
	v_and_or_b32 v1, v80, s23, v62
	v_addc_co_u32_e32 v31, vcc, 0, v31, vcc
	v_lshl_add_u64 v[28:29], s[14:15], 0, v[28:29]
	v_lshlrev_b32_e32 v38, 3, v1
	global_load_dwordx2 v[44:45], v[2:3], off
	s_nop 0
	global_load_dwordx4 v[2:5], v[22:23], off
	global_load_dwordx2 v[82:83], v[32:33], off
	v_lshl_add_u64 v[28:29], v[28:29], 0, v[38:39]
	global_load_dwordx2 v[84:85], v[30:31], off
	global_load_dwordx2 v[86:87], v[28:29], off
	v_bfe_u32 v11, v10, 2, 10
	v_or_b32_e32 v1, v11, v34
	v_lshlrev_b64 v[12:13], 15, v[12:13]
	v_or3_b32 v28, v12, v1, v35
	v_mov_b32_e32 v29, v13
	v_lshl_add_u64 v[28:29], v[28:29], 3, s[14:15]
	v_add_co_u32_e32 v28, vcc, s24, v28
	v_bfe_u32 v1, v10, 4, 8
	v_lshlrev_b32_e32 v10, 8, v10
	v_addc_co_u32_e32 v29, vcc, 0, v29, vcc
	v_and_b32_e32 v10, 0xf00, v10
	v_or_b32_e32 v1, v1, v34
	v_add_co_u32_e32 v30, vcc, s25, v22
	v_or3_b32 v12, v12, v1, v10
	s_nop 0
	v_addc_co_u32_e32 v31, vcc, 0, v23, vcc
	v_lshl_add_u64 v[10:11], v[12:13], 3, s[14:15]
	v_ashrrev_i32_e32 v81, 31, v80
	v_add_co_u32_e32 v10, vcc, s2, v10
	v_lshlrev_b64 v[12:13], 11, v[80:81]
	s_nop 0
	v_addc_co_u32_e32 v11, vcc, 0, v11, vcc
	v_lshl_add_u64 v[12:13], v[40:41], 0, v[12:13]
	global_load_dwordx2 v[58:59], v[28:29], off
	s_nop 0
	global_load_dwordx4 v[30:33], v[30:31], off
	v_add_co_u32_e32 v28, vcc, s33, v12
	v_bfe_u32 v1, v24, 2, 10
	s_nop 0
	v_addc_co_u32_e32 v29, vcc, 0, v13, vcc
	global_load_dwordx4 v[68:71], v[28:29], off
	global_load_dwordx4 v[72:75], v[12:13], off
	v_add_co_u32_e32 v22, vcc, s33, v22
	v_or_b32_e32 v1, v1, v67
	s_nop 0
	v_addc_co_u32_e32 v23, vcc, 0, v23, vcc
	global_load_dwordx2 v[60:61], v[10:11], off
	global_load_dwordx4 v[34:37], v[22:23], off
	global_load_dwordx2 v[50:51], v[26:27], off
	s_nop 0
	global_load_dwordx4 v[26:29], v[56:57], off
	v_lshlrev_b32_e32 v10, 10, v24
	v_and_b32_e32 v25, 0xc00, v10
	v_add_co_u32_e32 v10, vcc, s25, v12
	v_lshlrev_b64 v[22:23], 15, v[52:53]
	s_nop 0
	v_addc_co_u32_e32 v11, vcc, 0, v13, vcc
	global_load_dwordx4 v[76:79], v[10:11], off
	v_or3_b32 v10, v22, v1, v25
	v_mov_b32_e32 v11, v23
	v_lshl_add_u64 v[10:11], v[10:11], 3, s[14:15]
	v_add_co_u32_e32 v10, vcc, s24, v10
	v_bfe_u32 v1, v24, 4, 8
	v_lshlrev_b32_e32 v24, 8, v24
	v_addc_co_u32_e32 v11, vcc, 0, v11, vcc
	v_and_b32_e32 v24, 0xf00, v24
	v_or_b32_e32 v1, v1, v67
	v_add_co_u32_e32 v12, vcc, s25, v56
	v_or3_b32 v22, v22, v1, v24
	s_nop 0
	v_addc_co_u32_e32 v13, vcc, 0, v57, vcc
	v_lshl_add_u64 v[22:23], v[22:23], 3, s[14:15]
	v_add_co_u32_e32 v22, vcc, s2, v22
	global_load_dwordx2 v[52:53], v[10:11], off
	s_nop 0
	global_load_dwordx4 v[10:13], v[12:13], off
	v_addc_co_u32_e32 v23, vcc, 0, v23, vcc
	v_add_co_u32_e32 v24, vcc, s33, v56
	s_waitcnt vmcnt(11)
	v_max3_f32 v1, v86, v84, v82
	v_addc_co_u32_e32 v25, vcc, 0, v57, vcc
	global_load_dwordx2 v[56:57], v[22:23], off
	s_nop 0
	global_load_dwordx4 v[22:25], v[24:25], off
	v_sub_f32_e32 v38, v86, v1
	v_mul_f32_e32 v38, 0x3fb8aa3b, v38
	v_exp_f32_e32 v67, v38
	v_sub_f32_e32 v38, v84, v1
	v_sub_f32_e32 v1, v82, v1
	v_mul_f32_e32 v38, 0x3fb8aa3b, v38
	v_mul_f32_e32 v1, 0x3fb8aa3b, v1
	v_exp_f32_e32 v89, v38
	v_exp_f32_e32 v88, v1
	v_mov_b32_e32 v84, v83
	v_fma_f32 v1, v87, v67, 0
	v_pk_mul_f32 v[82:83], v[84:85], v[88:89]
	s_nop 0
	v_add_f32_e32 v1, v83, v1
	v_add_f32_e32 v1, v82, v1
	v_div_scale_f32 v38, s[18:19], v1, v1, 1.0
	v_rcp_f32_e32 v82, v38
	s_nop 0
	v_fma_f32 v83, -v38, v82, 1.0
	v_fmac_f32_e32 v82, v83, v82
	v_div_scale_f32 v83, vcc, 1.0, v1, 1.0
	v_mul_f32_e32 v84, v83, v82
	v_fma_f32 v85, -v38, v84, v83
	v_fmac_f32_e32 v84, v85, v82
	v_fma_f32 v38, -v38, v84, v83
	v_div_fmas_f32 v38, v38, v82, v84
	v_div_fixup_f32 v38, v38, v1, 1.0
	v_mul_f32_e32 v1, v67, v38
	s_waitcnt vmcnt(9)
	v_lshlrev_b32_e32 v67, 16, v72
	v_and_b32_e32 v72, 0xffff0000, v72
	v_fma_f32 v84, v1, v72, 0
	v_lshlrev_b32_e32 v72, 16, v73
	v_fma_f32 v85, v1, v72, 0
	v_and_b32_e32 v72, 0xffff0000, v73
	v_fma_f32 v86, v1, v72, 0
	v_lshlrev_b32_e32 v72, 16, v74
	v_fma_f32 v87, v1, v72, 0
	v_and_b32_e32 v72, 0xffff0000, v74
	v_fma_f32 v90, v1, v72, 0
	v_lshlrev_b32_e32 v72, 16, v75
	v_fma_f32 v82, v1, v72, 0
	v_and_b32_e32 v72, 0xffff0000, v75
	v_fma_f32 v67, v1, v67, 0
	v_fma_f32 v1, v1, v72, 0
	v_pk_mul_f32 v[72:73], v[88:89], v[38:39] op_sel_hi:[1,0]
	s_waitcnt vmcnt(4)
	v_lshlrev_b32_e32 v75, 16, v79
	v_lshlrev_b32_e32 v74, 16, v71
	v_pk_mul_f32 v[74:75], v[72:73], v[74:75]
	v_lshlrev_b32_e32 v83, 16, v76
	v_add_f32_e32 v38, v75, v82
	v_lshlrev_b32_e32 v82, 16, v68
	v_pk_mul_f32 v[82:83], v[72:73], v[82:83]
	v_add_f32_e32 v38, v74, v38
	v_add_f32_e32 v67, v83, v67
	v_add_f32_e32 v67, v82, v67
	v_and_b32_e32 v83, 0xffff0000, v76
	v_and_b32_e32 v82, 0xffff0000, v68
	v_pk_mul_f32 v[82:83], v[72:73], v[82:83]
	v_and_b32_e32 v76, 0xffff0000, v69
	v_add_f32_e32 v68, v83, v84
	v_add_f32_e32 v75, v82, v68
	v_lshlrev_b32_e32 v83, 16, v77
	v_lshlrev_b32_e32 v82, 16, v69
	v_pk_mul_f32 v[82:83], v[72:73], v[82:83]
	v_and_b32_e32 v77, 0xffff0000, v77
	v_add_f32_e32 v68, v83, v85
	v_add_f32_e32 v82, v82, v68
	v_pk_mul_f32 v[68:69], v[72:73], v[76:77]
	s_nop 0
	v_add_f32_e32 v69, v69, v86
	v_add_f32_e32 v76, v68, v69
	v_lshlrev_b32_e32 v69, 16, v78
	v_lshlrev_b32_e32 v68, 16, v70
	v_pk_mul_f32 v[68:69], v[72:73], v[68:69]
	s_nop 0
	v_add_f32_e32 v69, v69, v87
	v_add_f32_e32 v77, v68, v69
	v_and_b32_e32 v69, 0xffff0000, v78
	v_and_b32_e32 v68, 0xffff0000, v70
	v_pk_mul_f32 v[68:69], v[72:73], v[68:69]
	s_nop 0
	v_add_f32_e32 v69, v69, v90
	v_add_f32_e32 v70, v68, v69
	v_and_b32_e32 v69, 0xffff0000, v79
	v_and_b32_e32 v68, 0xffff0000, v71
	v_pk_mul_f32 v[68:69], v[72:73], v[68:69]
	v_lshlrev_b64 v[72:73], 12, v[80:81]
	v_add_f32_e32 v1, v69, v1
	v_lshl_add_u64 v[72:73], v[42:43], 0, v[72:73]
	v_add_f32_e32 v1, v68, v1
	v_cvt_pk_bf16_f32 v68, v67, v75
	v_cvt_pk_bf16_f32 v69, v82, v76
	v_cvt_pk_bf16_f32 v70, v77, v70
	v_cvt_pk_bf16_f32 v71, v38, v1
	global_store_dwordx4 v[72:73], v[68:71], off sc1
	s_and_saveexec_b64 s[18:19], s[6:7]
	s_cbranch_execz .LBB0_1201
	v_max3_f32 v1, v46, v48, v54
	v_sub_f32_e32 v38, v46, v1
	v_mul_f32_e32 v38, 0x3fb8aa3b, v38
	v_exp_f32_e32 v67, v38
	v_sub_f32_e32 v38, v48, v1
	v_sub_f32_e32 v1, v54, v1
	v_mul_f32_e32 v38, 0x3fb8aa3b, v38
	v_mul_f32_e32 v1, 0x3fb8aa3b, v1
	v_exp_f32_e32 v69, v38
	v_exp_f32_e32 v68, v1
	v_mov_b32_e32 v48, v55
	v_fma_f32 v1, v47, v67, 0
	v_pk_mul_f32 v[46:47], v[48:49], v[68:69]
	s_nop 0
	v_add_f32_e32 v1, v47, v1
	v_add_f32_e32 v1, v46, v1
	v_div_scale_f32 v38, s[6:7], v1, v1, 1.0
	v_rcp_f32_e32 v46, v38
	s_nop 0
	v_fma_f32 v47, -v38, v46, 1.0
	v_fmac_f32_e32 v46, v47, v46
	v_div_scale_f32 v47, vcc, 1.0, v1, 1.0
	v_mul_f32_e32 v48, v47, v46
	v_fma_f32 v49, -v38, v48, v47
	v_fmac_f32_e32 v48, v49, v46
	v_fma_f32 v38, -v38, v48, v47
	v_div_fmas_f32 v38, v38, v46, v48
	v_div_fixup_f32 v38, v38, v1, 1.0
	v_mul_f32_e32 v1, v67, v38
	v_lshlrev_b32_e32 v46, 16, v18
	v_and_b32_e32 v18, 0xffff0000, v18
	v_fma_f32 v49, v1, v18, 0
	v_lshlrev_b32_e32 v18, 16, v19
	v_fma_f32 v54, v1, v18, 0
	v_and_b32_e32 v18, 0xffff0000, v19
	v_fma_f32 v55, v1, v18, 0
	v_lshlrev_b32_e32 v18, 16, v20
	v_fma_f32 v67, v1, v18, 0
	v_and_b32_e32 v18, 0xffff0000, v20
	v_fma_f32 v70, v1, v18, 0
	v_lshlrev_b32_e32 v18, 16, v21
	v_fma_f32 v48, v1, v46, 0
	v_fma_f32 v46, v1, v18, 0
	v_and_b32_e32 v18, 0xffff0000, v21
	v_fma_f32 v1, v1, v18, 0
	v_pk_mul_f32 v[18:19], v[68:69], v[38:39] op_sel_hi:[1,0]
	v_lshlrev_b32_e32 v21, 16, v9
	v_lshlrev_b32_e32 v20, 16, v17
	v_pk_mul_f32 v[20:21], v[18:19], v[20:21]
	v_lshlrev_b32_e32 v47, 16, v6
	v_add_f32_e32 v21, v21, v46
	v_lshlrev_b32_e32 v46, 16, v14
	v_pk_mul_f32 v[46:47], v[18:19], v[46:47]
	s_nop 0
	v_add_f32_e32 v38, v47, v48
	v_add_f32_e32 v38, v46, v38
	v_and_b32_e32 v47, 0xffff0000, v6
	v_and_b32_e32 v46, 0xffff0000, v14
	v_pk_mul_f32 v[46:47], v[18:19], v[46:47]
	v_ashrrev_i32_e32 v14, 7, v64
	v_add_f32_e32 v6, v47, v49
	v_add_f32_e32 v48, v46, v6
	v_lshlrev_b32_e32 v47, 16, v7
	v_lshlrev_b32_e32 v46, 16, v15
	v_pk_mul_f32 v[46:47], v[18:19], v[46:47]
	v_and_b32_e32 v7, 0xffff0000, v7
	v_add_f32_e32 v6, v47, v54
	v_add_f32_e32 v46, v46, v6
	v_and_b32_e32 v6, 0xffff0000, v15
	v_pk_mul_f32 v[6:7], v[18:19], v[6:7]
	s_nop 0
	v_add_f32_e32 v7, v7, v55
	v_add_f32_e32 v15, v6, v7
	v_lshlrev_b32_e32 v7, 16, v8
	v_lshlrev_b32_e32 v6, 16, v16
	v_pk_mul_f32 v[6:7], v[18:19], v[6:7]
	s_nop 0
	v_add_f32_e32 v7, v7, v67
	v_add_f32_e32 v47, v6, v7
	v_and_b32_e32 v7, 0xffff0000, v8
	v_and_b32_e32 v6, 0xffff0000, v16
	v_pk_mul_f32 v[6:7], v[18:19], v[6:7]
	v_add_f32_e32 v16, v20, v21
	v_add_f32_e32 v7, v7, v70
	v_add_f32_e32 v8, v6, v7
	v_and_b32_e32 v7, 0xffff0000, v9
	v_and_b32_e32 v6, 0xffff0000, v17
	v_pk_mul_f32 v[6:7], v[18:19], v[6:7]
	v_cvt_pk_bf16_f32 v8, v47, v8
	s_nop 0
	v_add_f32_e32 v1, v7, v1
	v_cvt_pk_bf16_f32 v7, v46, v15
	v_ashrrev_i32_e32 v15, 31, v14
	v_lshlrev_b64 v[14:15], 12, v[14:15]
	v_lshl_add_u64 v[14:15], v[42:43], 0, v[14:15]
	v_add_f32_e32 v1, v6, v1
	v_cvt_pk_bf16_f32 v6, v38, v48
	v_cvt_pk_bf16_f32 v9, v16, v1
	global_store_dwordx4 v[14:15], v[6:9], off sc1
	s_and_b64 exec, exec, s[4:5]
	s_cbranch_execz .LBB0_1201
	v_max3_f32 v1, v44, v58, v60
	v_sub_f32_e32 v6, v44, v1
	v_mul_f32_e32 v6, 0x3fb8aa3b, v6
	v_exp_f32_e32 v14, v6
	v_sub_f32_e32 v6, v58, v1
	v_sub_f32_e32 v1, v60, v1
	v_mul_f32_e32 v6, 0x3fb8aa3b, v6
	v_mul_f32_e32 v1, 0x3fb8aa3b, v1
	v_exp_f32_e32 v7, v6
	v_exp_f32_e32 v6, v1
	v_mov_b32_e32 v58, v61
	v_fma_f32 v1, v45, v14, 0
	v_pk_mul_f32 v[8:9], v[58:59], v[6:7]
	s_nop 0
	v_add_f32_e32 v1, v9, v1
	v_add_f32_e32 v1, v8, v1
	v_div_scale_f32 v8, s[4:5], v1, v1, 1.0
	v_rcp_f32_e32 v9, v8
	s_nop 0
	v_fma_f32 v15, -v8, v9, 1.0
	v_fmac_f32_e32 v9, v15, v9
	v_div_scale_f32 v15, vcc, 1.0, v1, 1.0
	v_mul_f32_e32 v16, v15, v9
	v_fma_f32 v17, -v8, v16, v15
	v_fmac_f32_e32 v16, v17, v9
	v_fma_f32 v8, -v8, v16, v15
	v_div_fmas_f32 v8, v8, v9, v16
	v_div_fixup_f32 v8, v8, v1, 1.0
	v_mul_f32_e32 v1, v14, v8
	v_lshlrev_b32_e32 v9, 16, v2
	v_and_b32_e32 v2, 0xffff0000, v2
	v_fma_f32 v14, v1, v2, 0
	v_lshlrev_b32_e32 v2, 16, v3
	v_fma_f32 v15, v1, v2, 0
	v_and_b32_e32 v2, 0xffff0000, v3
	v_fma_f32 v16, v1, v2, 0
	v_lshlrev_b32_e32 v2, 16, v4
	v_fma_f32 v17, v1, v2, 0
	v_and_b32_e32 v2, 0xffff0000, v4
	v_fma_f32 v18, v1, v2, 0
	v_lshlrev_b32_e32 v2, 16, v5
	v_fma_f32 v9, v1, v9, 0
	v_fma_f32 v19, v1, v2, 0
	v_and_b32_e32 v2, 0xffff0000, v5
	v_fma_f32 v1, v1, v2, 0
	v_pk_mul_f32 v[2:3], v[6:7], v[8:9] op_sel_hi:[1,0]
	v_lshlrev_b32_e32 v7, 16, v30
	v_lshlrev_b32_e32 v6, 16, v34
	v_pk_mul_f32 v[6:7], v[2:3], v[6:7]
	v_lshlrev_b32_e32 v5, 16, v33
	v_add_f32_e32 v7, v7, v9
	v_add_f32_e32 v8, v6, v7
	v_and_b32_e32 v7, 0xffff0000, v30
	v_and_b32_e32 v6, 0xffff0000, v34
	v_pk_mul_f32 v[6:7], v[2:3], v[6:7]
	v_lshlrev_b32_e32 v4, 16, v37
	v_add_f32_e32 v7, v7, v14
	v_add_f32_e32 v9, v6, v7
	v_lshlrev_b32_e32 v7, 16, v31
	v_lshlrev_b32_e32 v6, 16, v35
	v_pk_mul_f32 v[6:7], v[2:3], v[6:7]
	v_pk_mul_f32 v[4:5], v[2:3], v[4:5]
	v_add_f32_e32 v7, v7, v15
	v_add_f32_e32 v14, v6, v7
	v_and_b32_e32 v7, 0xffff0000, v31
	v_and_b32_e32 v6, 0xffff0000, v35
	v_pk_mul_f32 v[6:7], v[2:3], v[6:7]
	v_add_f32_e32 v5, v5, v19
	v_add_f32_e32 v7, v7, v16
	v_add_f32_e32 v15, v6, v7
	v_lshlrev_b32_e32 v7, 16, v32
	v_lshlrev_b32_e32 v6, 16, v36
	v_pk_mul_f32 v[6:7], v[2:3], v[6:7]
	s_nop 0
	v_add_f32_e32 v7, v7, v17
	v_add_f32_e32 v16, v6, v7
	v_and_b32_e32 v7, 0xffff0000, v32
	v_and_b32_e32 v6, 0xffff0000, v36
	v_pk_mul_f32 v[6:7], v[2:3], v[6:7]
	v_add_f32_e32 v17, v4, v5
	v_add_f32_e32 v7, v7, v18
	v_add_f32_e32 v7, v6, v7
	v_and_b32_e32 v5, 0xffff0000, v33
	v_and_b32_e32 v4, 0xffff0000, v37
	v_ashrrev_i32_e32 v6, 7, v66
	v_pk_mul_f32 v[2:3], v[2:3], v[4:5]
	v_cvt_pk_bf16_f32 v4, v16, v7
	v_ashrrev_i32_e32 v7, 31, v6
	v_lshlrev_b64 v[6:7], 12, v[6:7]
	v_add_f32_e32 v1, v3, v1
	v_lshl_add_u64 v[6:7], v[42:43], 0, v[6:7]
	v_add_f32_e32 v1, v2, v1
	v_cvt_pk_bf16_f32 v2, v8, v9
	v_cvt_pk_bf16_f32 v3, v14, v15
	v_cvt_pk_bf16_f32 v5, v17, v1
	global_store_dwordx4 v[6:7], v[2:5], off sc1
	s_and_b64 exec, exec, s[0:1]
	s_cbranch_execz .LBB0_1201
	s_waitcnt vmcnt(4)
	v_max3_f32 v1, v50, v52, v56
	v_sub_f32_e32 v2, v50, v1
	v_mul_f32_e32 v2, 0x3fb8aa3b, v2
	v_exp_f32_e32 v6, v2
	v_sub_f32_e32 v2, v52, v1
	v_sub_f32_e32 v1, v56, v1
	v_mul_f32_e32 v2, 0x3fb8aa3b, v2
	v_mul_f32_e32 v1, 0x3fb8aa3b, v1
	v_exp_f32_e32 v3, v2
	v_exp_f32_e32 v2, v1
	v_mov_b32_e32 v52, v57
	v_fma_f32 v1, v51, v6, 0
	v_pk_mul_f32 v[4:5], v[52:53], v[2:3]
	s_nop 0
	v_add_f32_e32 v1, v5, v1
	v_add_f32_e32 v1, v4, v1
	v_div_scale_f32 v4, s[0:1], v1, v1, 1.0
	v_rcp_f32_e32 v5, v4
	s_nop 0
	v_fma_f32 v7, -v4, v5, 1.0
	v_fmac_f32_e32 v5, v7, v5
	v_div_scale_f32 v7, vcc, 1.0, v1, 1.0
	v_mul_f32_e32 v8, v7, v5
	v_fma_f32 v9, -v4, v8, v7
	v_fmac_f32_e32 v8, v9, v5
	v_fma_f32 v4, -v4, v8, v7
	v_div_fmas_f32 v4, v4, v5, v8
	v_div_fixup_f32 v4, v4, v1, 1.0
	v_mul_f32_e32 v1, v6, v4
	v_lshlrev_b32_e32 v5, 16, v26
	v_fma_f32 v8, v1, v5, 0
	v_and_b32_e32 v5, 0xffff0000, v26
	v_fma_f32 v9, v1, v5, 0
	v_lshlrev_b32_e32 v5, 16, v27
	v_fma_f32 v14, v1, v5, 0
	v_and_b32_e32 v5, 0xffff0000, v27
	v_fma_f32 v15, v1, v5, 0
	v_lshlrev_b32_e32 v5, 16, v28
	v_fma_f32 v16, v1, v5, 0
	v_and_b32_e32 v5, 0xffff0000, v28
	v_fma_f32 v17, v1, v5, 0
	v_lshlrev_b32_e32 v5, 16, v29
	v_fma_f32 v6, v1, v5, 0
	v_and_b32_e32 v5, 0xffff0000, v29
	v_fma_f32 v1, v1, v5, 0
	v_pk_mul_f32 v[2:3], v[2:3], v[4:5] op_sel_hi:[1,0]
	v_lshlrev_b32_e32 v5, 16, v13
	s_waitcnt vmcnt(3)
	v_lshlrev_b32_e32 v4, 16, v25
	v_pk_mul_f32 v[4:5], v[2:3], v[4:5]
	v_lshlrev_b32_e32 v7, 16, v10
	v_add_f32_e32 v5, v5, v6
	v_lshlrev_b32_e32 v6, 16, v22
	v_pk_mul_f32 v[6:7], v[2:3], v[6:7]
	s_nop 0
	v_add_f32_e32 v7, v7, v8
	v_add_f32_e32 v8, v6, v7
	v_and_b32_e32 v7, 0xffff0000, v10
	v_and_b32_e32 v6, 0xffff0000, v22
	v_pk_mul_f32 v[6:7], v[2:3], v[6:7]
	s_nop 0
	v_add_f32_e32 v7, v7, v9
	v_add_f32_e32 v9, v6, v7
	v_lshlrev_b32_e32 v7, 16, v11
	v_lshlrev_b32_e32 v6, 16, v23
	v_pk_mul_f32 v[6:7], v[2:3], v[6:7]
	s_nop 0
	v_add_f32_e32 v7, v7, v14
	v_add_f32_e32 v10, v6, v7
	v_and_b32_e32 v7, 0xffff0000, v11
	v_and_b32_e32 v6, 0xffff0000, v23
	v_pk_mul_f32 v[6:7], v[2:3], v[6:7]
	s_nop 0
	v_add_f32_e32 v7, v7, v15
	v_add_f32_e32 v11, v6, v7
	v_lshlrev_b32_e32 v7, 16, v12
	v_lshlrev_b32_e32 v6, 16, v24
	v_pk_mul_f32 v[6:7], v[2:3], v[6:7]
	s_nop 0
	v_add_f32_e32 v7, v7, v16
	v_add_f32_e32 v14, v6, v7
	v_and_b32_e32 v7, 0xffff0000, v12
	v_and_b32_e32 v6, 0xffff0000, v24
	v_pk_mul_f32 v[6:7], v[2:3], v[6:7]
	v_add_f32_e32 v12, v4, v5
	v_add_f32_e32 v7, v7, v17
	v_add_f32_e32 v7, v6, v7
	v_and_b32_e32 v5, 0xffff0000, v13
	v_and_b32_e32 v4, 0xffff0000, v25
	v_ashrrev_i32_e32 v6, 7, v65
	v_pk_mul_f32 v[2:3], v[2:3], v[4:5]
	v_cvt_pk_bf16_f32 v4, v14, v7
	v_ashrrev_i32_e32 v7, 31, v6
	v_lshlrev_b64 v[6:7], 12, v[6:7]
	v_add_f32_e32 v1, v3, v1
	v_lshl_add_u64 v[6:7], v[42:43], 0, v[6:7]
	v_add_f32_e32 v1, v2, v1
	v_cvt_pk_bf16_f32 v2, v8, v9
	v_cvt_pk_bf16_f32 v3, v10, v11
	v_cvt_pk_bf16_f32 v5, v12, v1
	global_store_dwordx4 v[6:7], v[2:5], off sc1
	s_branch .LBB0_1201

.LBB0_1274:
	v_lshl_or_b32 v144, s2, 8, v157
	v_lshl_add_u32 v154, s56, 8, v1
	v_ashrrev_i32_e32 v145, 31, v144
	v_lshlrev_b64 v[144:145], 2, v[144:145]
	v_ashrrev_i32_e32 v155, 31, v154
	v_lshl_add_u64 v[146:147], s[78:79], 0, v[144:145]
	v_lshlrev_b64 v[148:149], 13, v[154:155]
	v_or_b32_e32 v174, 16, v154
	v_lshl_add_u64 v[170:171], v[146:147], 0, v[148:149]
	v_ashrrev_i32_e32 v175, 31, v174
	global_load_dwordx4 v[150:153], v[170:171], off
	global_load_dwordx4 v[162:165], v[170:171], off offset:64
	global_load_dwordx4 v[166:169], v[170:171], off offset:512
	s_nop 0
	global_load_dwordx4 v[170:173], v[170:171], off offset:576
	v_lshlrev_b64 v[224:225], 13, v[174:175]
	v_or_b32_e32 v190, 32, v154
	v_lshl_add_u64 v[186:187], v[146:147], 0, v[224:225]
	v_ashrrev_i32_e32 v191, 31, v190
	global_load_dwordx4 v[174:177], v[186:187], off
	global_load_dwordx4 v[178:181], v[186:187], off offset:64
	global_load_dwordx4 v[182:185], v[186:187], off offset:512
	s_nop 0
	global_load_dwordx4 v[186:189], v[186:187], off offset:576
	v_lshlrev_b64 v[226:227], 13, v[190:191]
	v_or_b32_e32 v154, 48, v154
	v_lshl_add_u64 v[202:203], v[146:147], 0, v[226:227]
	v_ashrrev_i32_e32 v155, 31, v154
	global_load_dwordx4 v[190:193], v[202:203], off
	global_load_dwordx4 v[194:197], v[202:203], off offset:64
	global_load_dwordx4 v[198:201], v[202:203], off offset:512
	s_nop 0
	global_load_dwordx4 v[202:205], v[202:203], off offset:576
	v_lshlrev_b64 v[154:155], 13, v[154:155]
	v_lshl_add_u64 v[220:221], v[146:147], 0, v[154:155]
	global_load_dwordx4 v[206:209], v[220:221], off
	global_load_dwordx4 v[210:213], v[220:221], off offset:64
	global_load_dwordx4 v[214:217], v[220:221], off offset:512
	s_nop 0
	global_load_dwordx4 v[220:223], v[220:221], off offset:576
	s_mov_b64 s[56:57], -1
	s_andn2_b64 vcc, exec, s[0:1]
	s_waitcnt vmcnt(0)
	v_pk_add_f32 v[126:127], v[126:127], v[150:151]
	v_lshl_add_u64 v[150:151], s[78:79], 0, v[148:149]
	v_lshl_add_u64 v[150:151], v[150:151], 0, v[144:145]
	v_pk_add_f32 v[112:113], v[112:113], v[168:169]
	v_pk_add_f32 v[110:111], v[110:111], v[166:167]
	global_store_dwordx4 v[150:151], v[110:113], off offset:512 sc1
	v_pk_add_f32 v[104:105], v[104:105], v[172:173]
	v_pk_add_f32 v[96:97], v[96:97], v[184:185]
	v_lshl_add_u64 v[110:111], s[78:79], 0, v[224:225]
	v_lshl_add_u64 v[110:111], v[110:111], 0, v[144:145]
	v_pk_add_f32 v[94:95], v[94:95], v[182:183]
	global_store_dwordx4 v[110:111], v[94:97], off offset:512 sc1
	v_pk_add_f32 v[80:81], v[80:81], v[200:201]
	v_pk_add_f32 v[78:79], v[78:79], v[198:199]
	v_lshl_add_u64 v[94:95], s[78:79], 0, v[226:227]
	v_lshl_add_u64 v[94:95], v[94:95], 0, v[144:145]
	v_pk_add_f32 v[102:103], v[102:103], v[170:171]
	v_pk_add_f32 v[88:89], v[88:89], v[188:189]
	v_pk_add_f32 v[86:87], v[86:87], v[186:187]
	global_store_dwordx4 v[94:95], v[78:81], off offset:512 sc1
	v_pk_add_f32 v[76:77], v[76:77], v[204:205]
	v_pk_add_f32 v[74:75], v[74:75], v[202:203]
	v_lshl_add_u64 v[78:79], s[78:79], 0, v[154:155]
	global_store_dwordx4 v[150:151], v[102:105], off offset:576 sc1
	global_store_dwordx4 v[110:111], v[86:89], off offset:576 sc1
	global_store_dwordx4 v[94:95], v[74:77], off offset:576 sc1
	v_pk_add_f32 v[104:105], v[120:121], v[176:177]
	v_pk_add_f32 v[102:103], v[118:119], v[174:175]
	v_pk_add_f32 v[88:89], v[108:109], v[192:193]
	v_pk_add_f32 v[86:87], v[106:107], v[190:191]
	v_pk_add_f32 v[76:77], v[92:93], v[208:209]
	v_pk_add_f32 v[74:75], v[90:91], v[206:207]
	v_lshl_add_u64 v[78:79], v[78:79], 0, v[144:145]
	v_pk_add_f32 v[128:129], v[128:129], v[152:153]
	v_pk_add_f32 v[124:125], v[124:125], v[164:165]
	v_pk_add_f32 v[122:123], v[122:123], v[162:163]
	global_store_dwordx4 v[110:111], v[102:105], off sc1
	global_store_dwordx4 v[94:95], v[86:89], off sc1
	global_store_dwordx4 v[78:79], v[74:77], off sc1
	v_pk_add_f32 v[104:105], v[116:117], v[180:181]
	v_pk_add_f32 v[102:103], v[114:115], v[178:179]
	v_pk_add_f32 v[88:89], v[100:101], v[196:197]
	v_pk_add_f32 v[86:87], v[98:99], v[194:195]
	v_pk_add_f32 v[76:77], v[84:85], v[212:213]
	v_pk_add_f32 v[74:75], v[82:83], v[210:211]
	v_pk_add_f32 v[72:73], v[72:73], v[216:217]
	v_pk_add_f32 v[70:71], v[70:71], v[214:215]
	v_pk_add_f32 v[68:69], v[68:69], v[222:223]
	v_pk_add_f32 v[66:67], v[66:67], v[220:221]
	v_lshl_add_u64 v[154:155], v[148:149], 0, s[36:37]
	global_store_dwordx4 v[150:151], v[126:129], off sc1
	global_store_dwordx4 v[150:151], v[122:125], off offset:64 sc1
	global_store_dwordx4 v[110:111], v[102:105], off offset:64 sc1
	global_store_dwordx4 v[94:95], v[86:89], off offset:64 sc1
	global_store_dwordx4 v[78:79], v[74:77], off offset:64 sc1
	global_store_dwordx4 v[78:79], v[70:73], off offset:512 sc1
	global_store_dwordx4 v[78:79], v[66:69], off offset:576 sc1
	v_lshl_add_u64 v[152:153], v[148:149], 0, s[38:39]
	v_lshl_add_u64 v[150:151], v[148:149], 0, s[40:41]
	v_lshl_add_u64 v[66:67], v[146:147], 0, v[154:155]
	global_load_dwordx4 v[118:121], v[66:67], off
	global_load_dwordx4 v[106:109], v[66:67], off offset:64
	global_load_dwordx4 v[102:105], v[66:67], off offset:512
	global_load_dwordx4 v[94:97], v[66:67], off offset:576
	v_lshl_add_u64 v[66:67], v[146:147], 0, v[152:153]
	global_load_dwordx4 v[98:101], v[66:67], off
	global_load_dwordx4 v[90:93], v[66:67], off offset:64
	global_load_dwordx4 v[82:85], v[66:67], off offset:512
	global_load_dwordx4 v[78:81], v[66:67], off offset:576
	v_lshl_add_u64 v[66:67], v[146:147], 0, v[150:151]
	global_load_dwordx4 v[86:89], v[66:67], off
	global_load_dwordx4 v[74:77], v[66:67], off offset:64
	global_load_dwordx4 v[70:73], v[66:67], off offset:512
	s_nop 0
	global_load_dwordx4 v[66:69], v[66:67], off offset:576
	v_lshl_add_u64 v[148:149], v[148:149], 0, s[42:43]
	v_lshl_add_u64 v[126:127], v[146:147], 0, v[148:149]
	global_load_dwordx4 v[122:125], v[126:127], off
	global_load_dwordx4 v[114:117], v[126:127], off offset:64
	global_load_dwordx4 v[110:113], v[126:127], off offset:512
	s_nop 0
	global_load_dwordx4 v[126:129], v[126:127], off offset:576
	s_waitcnt vmcnt(15)
	v_pk_add_f32 v[62:63], v[62:63], v[118:119]
	v_lshl_add_u64 v[118:119], s[78:79], 0, v[154:155]
	v_lshl_add_u64 v[118:119], v[118:119], 0, v[144:145]
	s_waitcnt vmcnt(13)
	v_pk_add_f32 v[52:53], v[52:53], v[104:105]
	v_pk_add_f32 v[50:51], v[50:51], v[102:103]
	global_store_dwordx4 v[118:119], v[50:53], off offset:512 sc1
	s_waitcnt vmcnt(10)
	v_pk_add_f32 v[36:37], v[36:37], v[84:85]
	v_pk_add_f32 v[34:35], v[34:35], v[82:83]
	v_lshl_add_u64 v[50:51], s[78:79], 0, v[152:153]
	v_lshl_add_u64 v[50:51], v[50:51], 0, v[144:145]
	global_store_dwordx4 v[50:51], v[34:37], off offset:512 sc1
	s_waitcnt vmcnt(7)
	v_pk_add_f32 v[20:21], v[20:21], v[72:73]
	v_pk_add_f32 v[18:19], v[18:19], v[70:71]
	v_lshl_add_u64 v[34:35], s[78:79], 0, v[150:151]
	v_lshl_add_u64 v[34:35], v[34:35], 0, v[144:145]
	v_pk_add_f32 v[44:45], v[44:45], v[96:97]
	v_pk_add_f32 v[42:43], v[42:43], v[94:95]
	v_pk_add_f32 v[28:29], v[28:29], v[80:81]
	v_pk_add_f32 v[26:27], v[26:27], v[78:79]
	global_store_dwordx4 v[34:35], v[18:21], off offset:512 sc1
	s_waitcnt vmcnt(7)
	v_pk_add_f32 v[12:13], v[12:13], v[68:69]
	v_pk_add_f32 v[10:11], v[10:11], v[66:67]
	v_lshl_add_u64 v[18:19], s[78:79], 0, v[148:149]
	global_store_dwordx4 v[118:119], v[42:45], off offset:576 sc1
	global_store_dwordx4 v[50:51], v[26:29], off offset:576 sc1
	global_store_dwordx4 v[34:35], v[10:13], off offset:576 sc1
	v_pk_add_f32 v[44:45], v[56:57], v[100:101]
	v_pk_add_f32 v[42:43], v[54:55], v[98:99]
	v_pk_add_f32 v[28:29], v[40:41], v[88:89]
	v_pk_add_f32 v[26:27], v[38:39], v[86:87]
	s_waitcnt vmcnt(9)
	v_pk_add_f32 v[12:13], v[24:25], v[124:125]
	v_pk_add_f32 v[10:11], v[22:23], v[122:123]
	v_lshl_add_u64 v[18:19], v[18:19], 0, v[144:145]
	v_pk_add_f32 v[64:65], v[64:65], v[120:121]
	v_pk_add_f32 v[60:61], v[60:61], v[108:109]
	v_pk_add_f32 v[58:59], v[58:59], v[106:107]
	global_store_dwordx4 v[50:51], v[42:45], off sc1
	global_store_dwordx4 v[34:35], v[26:29], off sc1
	global_store_dwordx4 v[18:19], v[10:13], off sc1
	v_pk_add_f32 v[44:45], v[48:49], v[92:93]
	v_pk_add_f32 v[42:43], v[46:47], v[90:91]
	v_pk_add_f32 v[28:29], v[32:33], v[76:77]
	v_pk_add_f32 v[26:27], v[30:31], v[74:75]
	s_waitcnt vmcnt(11)
	v_pk_add_f32 v[12:13], v[16:17], v[116:117]
	v_pk_add_f32 v[10:11], v[14:15], v[114:115]
	s_waitcnt vmcnt(10)
	v_pk_add_f32 v[8:9], v[8:9], v[112:113]
	v_pk_add_f32 v[6:7], v[6:7], v[110:111]
	s_waitcnt vmcnt(9)
	v_pk_add_f32 v[4:5], v[4:5], v[128:129]
	v_pk_add_f32 v[2:3], v[2:3], v[126:127]
	global_store_dwordx4 v[118:119], v[62:65], off sc1
	global_store_dwordx4 v[118:119], v[58:61], off offset:64 sc1
	global_store_dwordx4 v[50:51], v[42:45], off offset:64 sc1
	global_store_dwordx4 v[34:35], v[26:29], off offset:64 sc1
	global_store_dwordx4 v[18:19], v[10:13], off offset:64 sc1
	global_store_dwordx4 v[18:19], v[6:9], off offset:512 sc1
	global_store_dwordx4 v[18:19], v[2:5], off offset:576 sc1
	s_cbranch_vccnz .LBB0_1263
	s_andn2_b64 vcc, exec, s[12:13]
	s_cbranch_vccnz .LBB0_1262
	s_barrier
	s_branch .LBB0_1262

.LBB0_1419:
	s_ashr_i32 s9, s8, 31
	s_ashr_i32 s45, s44, 31
	s_ashr_i32 s43, s42, 31
	s_ashr_i32 s11, s10, 31
	s_lshl_b64 s[52:53], s[8:9], 11
	s_lshl_b64 s[54:55], s[44:45], 11
	s_lshl_b64 s[56:57], s[42:43], 11
	s_lshl_b64 s[58:59], s[10:11], 11
	v_lshl_add_u64 v[40:41], v[10:11], 0, s[52:53]
	v_lshl_add_u64 v[48:49], v[10:11], 0, s[54:55]
	v_lshl_add_u64 v[56:57], v[10:11], 0, s[56:57]
	v_lshl_add_u64 v[64:65], v[10:11], 0, s[58:59]
	global_load_dwordx4 v[36:39], v[40:41], off
	s_nop 0
	global_load_dwordx4 v[40:43], v[40:41], off offset:1024
	s_nop 0
	global_load_dwordx4 v[44:47], v[48:49], off
	s_nop 0
	global_load_dwordx4 v[48:51], v[48:49], off offset:1024
	s_nop 0
	global_load_dwordx4 v[52:55], v[56:57], off
	s_nop 0
	global_load_dwordx4 v[56:59], v[56:57], off offset:1024
	s_nop 0
	global_load_dwordx4 v[60:63], v[64:65], off
	s_nop 0
	global_load_dwordx4 v[64:67], v[64:65], off offset:1024
	v_mov_b32_e32 v35, s51
	ds_read2_b32 v[68:69], v35 offset1:8
	ds_read2_b32 v[70:71], v35 offset0:16 offset1:24
	s_addk_i32 s51, 0x80
	s_add_i32 s15, s15, 32
	s_add_i32 s8, s8, 16
	s_waitcnt lgkmcnt(1)
	v_ashrrev_i32_e32 v73, 31, v68
	v_mov_b32_e32 v72, v68
	s_add_i32 s10, s10, 16
	s_add_i32 s42, s42, 16
	s_add_i32 s44, s44, 16
	v_ashrrev_i32_e32 v75, 31, v69
	v_mov_b32_e32 v74, v69
	s_waitcnt lgkmcnt(0)
	v_ashrrev_i32_e32 v69, 31, v70
	v_mov_b32_e32 v68, v70
	v_ashrrev_i32_e32 v77, 31, v71
	v_mov_b32_e32 v76, v71
	v_lshlrev_b64 v[70:71], 11, v[72:73]
	s_cmpk_gt_u32 s15, 0x5f
	v_lshlrev_b64 v[72:73], 11, v[74:75]
	v_lshlrev_b64 v[68:69], 11, v[68:69]
	v_lshlrev_b64 v[74:75], 11, v[76:77]
	v_lshl_add_u64 v[70:71], v[6:7], 0, v[70:71]
	v_lshl_add_u64 v[72:73], v[6:7], 0, v[72:73]
	v_lshl_add_u64 v[68:69], v[6:7], 0, v[68:69]
	v_lshl_add_u64 v[74:75], v[6:7], 0, v[74:75]
	s_waitcnt vmcnt(7)
	global_store_dwordx4 v[70:71], v[36:39], off sc1
	s_waitcnt vmcnt(7)
	global_store_dwordx4 v[70:71], v[40:43], off offset:1024 sc1
	s_waitcnt vmcnt(7)
	global_store_dwordx4 v[72:73], v[44:47], off sc1
	s_waitcnt vmcnt(7)
	global_store_dwordx4 v[72:73], v[48:51], off offset:1024 sc1
	s_waitcnt vmcnt(7)
	global_store_dwordx4 v[68:69], v[52:55], off sc1
	s_waitcnt vmcnt(7)
	global_store_dwordx4 v[68:69], v[56:59], off offset:1024 sc1
	s_waitcnt vmcnt(7)
	global_store_dwordx4 v[74:75], v[60:63], off sc1
	s_waitcnt vmcnt(7)
	global_store_dwordx4 v[74:75], v[64:67], off offset:1024 sc1
	s_cbranch_scc0 .LBB0_1419

.LBB0_1423:
	s_mov_b32 s14, s12
	s_mov_b32 s15, s12
	s_mov_b32 s13, s12
	v_add_u32_e32 v14, 8, v14
	v_mov_b64_e32 v[38:39], s[14:15]
	v_mov_b64_e32 v[36:37], s[12:13]
	v_cmp_lt_i32_e32 vcc, v14, v34
	global_store_dwordx4 v[16:17], v[36:39], off sc1
	global_store_dwordx4 v[16:17], v[36:39], off offset:1024 sc1
	v_lshl_add_u64 v[16:17], v[16:17], 0, s[40:41]
	s_cbranch_vccnz .LBB0_1423

.LBB0_1571:
	v_lshl_add_u32 v8, s54, 8, v1
	v_lshl_or_b32 v2, s2, 8, v185
	v_ashrrev_i32_e32 v9, 31, v8
	v_ashrrev_i32_e32 v3, 31, v2
	v_lshlrev_b64 v[4:5], 12, v[8:9]
	v_lshl_add_u64 v[4:5], s[22:23], 0, v[4:5]
	v_lshlrev_b64 v[10:11], 1, v[2:3]
	s_nop 15
	s_nop 15
	v_lshl_add_u64 v[2:3], v[4:5], 0, v[10:11]
	v_cvt_pk_bf16_f32 v4, v158, v159
	v_cvt_pk_bf16_f32 v5, v160, v161
	v_cvt_pk_bf16_f32 v6, v154, v155
	v_cvt_pk_bf16_f32 v7, v156, v157
	global_store_dwordx4 v[2:3], v[4:7], off sc1
	s_nop 1
	v_cvt_pk_bf16_f32 v4, v146, v147
	v_cvt_pk_bf16_f32 v5, v148, v149
	v_cvt_pk_bf16_f32 v6, v138, v139
	v_cvt_pk_bf16_f32 v7, v140, v141
	global_store_dwordx4 v[2:3], v[4:7], off offset:256 sc1
	s_nop 1
	v_or_b32_e32 v4, 16, v8
	v_ashrrev_i32_e32 v5, 31, v4
	v_lshlrev_b64 v[4:5], 12, v[4:5]
	v_lshl_add_u64 v[4:5], s[22:23], 0, v[4:5]
	v_lshl_add_u64 v[12:13], v[4:5], 0, v[10:11]
	v_cvt_pk_bf16_f32 v4, v150, v151
	v_cvt_pk_bf16_f32 v5, v152, v153
	v_cvt_pk_bf16_f32 v6, v142, v143
	v_cvt_pk_bf16_f32 v7, v144, v145
	global_store_dwordx4 v[12:13], v[4:7], off sc1
	s_nop 1
	v_cvt_pk_bf16_f32 v4, v130, v131
	v_cvt_pk_bf16_f32 v5, v132, v133
	v_cvt_pk_bf16_f32 v6, v122, v123
	v_cvt_pk_bf16_f32 v7, v124, v125
	global_store_dwordx4 v[12:13], v[4:7], off offset:256 sc1
	s_nop 1
	v_or_b32_e32 v4, 32, v8
	v_ashrrev_i32_e32 v5, 31, v4
	v_lshlrev_b64 v[4:5], 12, v[4:5]
	v_lshl_add_u64 v[4:5], s[22:23], 0, v[4:5]
	v_lshl_add_u64 v[12:13], v[4:5], 0, v[10:11]
	v_cvt_pk_bf16_f32 v4, v134, v135
	v_cvt_pk_bf16_f32 v5, v136, v137
	v_cvt_pk_bf16_f32 v6, v126, v127
	v_cvt_pk_bf16_f32 v7, v128, v129
	global_store_dwordx4 v[12:13], v[4:7], off sc1
	s_nop 1
	v_cvt_pk_bf16_f32 v4, v114, v115
	v_cvt_pk_bf16_f32 v5, v116, v117
	v_cvt_pk_bf16_f32 v6, v106, v107
	v_cvt_pk_bf16_f32 v7, v108, v109
	global_store_dwordx4 v[12:13], v[4:7], off offset:256 sc1
	s_nop 1
	v_or_b32_e32 v4, 48, v8
	v_ashrrev_i32_e32 v5, 31, v4
	v_lshlrev_b64 v[4:5], 12, v[4:5]
	v_lshl_add_u64 v[4:5], s[22:23], 0, v[4:5]
	v_lshl_add_u64 v[8:9], v[4:5], 0, v[10:11]
	v_cvt_pk_bf16_f32 v4, v118, v119
	v_cvt_pk_bf16_f32 v5, v120, v121
	v_cvt_pk_bf16_f32 v6, v110, v111
	v_cvt_pk_bf16_f32 v7, v112, v113
	global_store_dwordx4 v[8:9], v[4:7], off sc1
	v_add_co_u32_e32 v10, vcc, s71, v2
	s_nop 0
	v_cvt_pk_bf16_f32 v4, v102, v103
	v_cvt_pk_bf16_f32 v5, v104, v105
	v_cvt_pk_bf16_f32 v6, v98, v99
	v_cvt_pk_bf16_f32 v7, v100, v101
	global_store_dwordx4 v[8:9], v[4:7], off offset:256 sc1
	v_addc_co_u32_e32 v11, vcc, 0, v3, vcc
	s_nop 0
	v_cvt_pk_bf16_f32 v4, v94, v95
	v_cvt_pk_bf16_f32 v5, v96, v97
	v_cvt_pk_bf16_f32 v6, v90, v91
	v_cvt_pk_bf16_f32 v7, v92, v93
	v_lshl_add_u64 v[8:9], v[2:3], 0, s[46:47]
	global_store_dwordx4 v[10:11], v[4:7], off sc1
	v_add_co_u32_e32 v10, vcc, s72, v2
	s_nop 0
	v_cvt_pk_bf16_f32 v4, v82, v83
	v_cvt_pk_bf16_f32 v5, v84, v85
	v_cvt_pk_bf16_f32 v6, v74, v75
	v_cvt_pk_bf16_f32 v7, v76, v77
	global_store_dwordx4 v[8:9], v[4:7], off offset:256 sc1
	v_addc_co_u32_e32 v11, vcc, 0, v3, vcc
	s_nop 0
	v_cvt_pk_bf16_f32 v4, v86, v87
	v_cvt_pk_bf16_f32 v5, v88, v89
	v_cvt_pk_bf16_f32 v6, v78, v79
	v_cvt_pk_bf16_f32 v7, v80, v81
	v_lshl_add_u64 v[8:9], v[2:3], 0, s[48:49]
	global_store_dwordx4 v[10:11], v[4:7], off sc1
	v_add_co_u32_e32 v10, vcc, s73, v2
	s_nop 0
	v_cvt_pk_bf16_f32 v4, v66, v67
	v_cvt_pk_bf16_f32 v5, v68, v69
	v_cvt_pk_bf16_f32 v6, v58, v59
	v_cvt_pk_bf16_f32 v7, v60, v61
	global_store_dwordx4 v[8:9], v[4:7], off offset:256 sc1
	v_lshl_add_u64 v[8:9], v[2:3], 0, s[50:51]
	v_addc_co_u32_e32 v11, vcc, 0, v3, vcc
	v_cvt_pk_bf16_f32 v4, v70, v71
	v_cvt_pk_bf16_f32 v5, v72, v73
	v_cvt_pk_bf16_f32 v6, v62, v63
	v_cvt_pk_bf16_f32 v7, v64, v65
	global_store_dwordx4 v[10:11], v[4:7], off sc1
	s_nop 1
	v_cvt_pk_bf16_f32 v4, v50, v51
	v_cvt_pk_bf16_f32 v5, v52, v53
	v_cvt_pk_bf16_f32 v6, v42, v43
	v_cvt_pk_bf16_f32 v7, v44, v45
	global_store_dwordx4 v[8:9], v[4:7], off offset:256 sc1
	v_lshl_add_u64 v[8:9], v[2:3], 0, s[20:21]
	v_add_co_u32_e32 v2, vcc, s74, v2
	v_cvt_pk_bf16_f32 v4, v54, v55
	v_cvt_pk_bf16_f32 v5, v56, v57
	v_cvt_pk_bf16_f32 v6, v46, v47
	v_cvt_pk_bf16_f32 v7, v48, v49
	s_nop 1
	v_addc_co_u32_e32 v3, vcc, 0, v3, vcc
	s_and_b64 vcc, exec, s[0:1]
	s_mov_b64 s[0:1], -1
	global_store_dwordx4 v[2:3], v[4:7], off sc1
	v_cvt_pk_bf16_f32 v2, v38, v39
	v_cvt_pk_bf16_f32 v3, v40, v41
	s_nop 1
	v_cvt_pk_bf16_f32 v4, v34, v35
	v_cvt_pk_bf16_f32 v5, v36, v37
	global_store_dwordx4 v[8:9], v[2:5], off offset:256 sc1
	s_cbranch_vccnz .LBB0_1560
	s_andn2_b64 vcc, exec, s[18:19]
	s_cbranch_vccnz .LBB0_1559
	s_barrier
	s_branch .LBB0_1559

.LBB0_1629:
	v_ashrrev_i32_e32 v47, 31, v44
	v_mov_b32_e32 v46, v44
	v_ashrrev_i32_e32 v57, 31, v45
	v_mov_b32_e32 v56, v45
	v_lshlrev_b64 v[46:47], 12, v[46:47]
	v_lshlrev_b64 v[56:57], 12, v[56:57]
	v_lshl_add_u64 v[44:45], v[34:35], 0, v[46:47]
	v_lshl_add_u64 v[46:47], v[34:35], 0, v[56:57]
	global_load_dwordx2 v[84:85], v[46:47], off
	global_load_dwordx2 v[86:87], v[44:45], off
	global_load_dwordx2 v[88:89], v[46:47], off offset:512
	global_load_dwordx2 v[90:91], v[44:45], off offset:512
	global_load_dwordx2 v[92:93], v[46:47], off offset:1024
	global_load_dwordx2 v[94:95], v[44:45], off offset:1024
	global_load_dwordx2 v[96:97], v[46:47], off offset:1536
	global_load_dwordx4 v[56:59], v[36:37], off offset:-4096
	global_load_dwordx4 v[60:63], v[36:37], off offset:-3072
	global_load_dwordx4 v[64:67], v[36:37], off offset:-2048
	global_load_dwordx2 v[98:99], v[44:45], off offset:1536
	global_load_dwordx4 v[68:71], v[36:37], off offset:-1024
	global_load_dwordx4 v[72:75], v[36:37], off
	global_load_dwordx4 v[76:79], v[36:37], off offset:1024
	global_load_dwordx4 v[80:83], v[36:37], off offset:2048
	global_load_dwordx2 v[100:101], v[44:45], off offset:2048
	global_load_dwordx2 v[102:103], v[44:45], off offset:2560
	global_load_dwordx2 v[104:105], v[44:45], off offset:3072
	global_load_dwordx2 v[106:107], v[46:47], off offset:2048
	global_load_dwordx2 v[108:109], v[46:47], off offset:2560
	global_load_dwordx2 v[110:111], v[46:47], off offset:3072
	s_add_i32 s4, s4, s15
	s_waitcnt vmcnt(20)
	v_lshlrev_b32_e32 v112, 16, v84
	s_waitcnt vmcnt(19)
	v_and_b32_e32 v113, 0xffff0000, v86
	v_lshlrev_b32_e32 v114, 16, v86
	v_and_b32_e32 v115, 0xffff0000, v84
	v_lshlrev_b32_e32 v116, 16, v85
	v_and_b32_e32 v117, 0xffff0000, v87
	v_lshlrev_b32_e32 v84, 16, v87
	v_and_b32_e32 v85, 0xffff0000, v85
	s_waitcnt vmcnt(18)
	v_lshlrev_b32_e32 v86, 16, v88
	s_waitcnt vmcnt(17)
	v_and_b32_e32 v87, 0xffff0000, v90
	v_lshlrev_b32_e32 v118, 16, v90
	v_and_b32_e32 v119, 0xffff0000, v88
	v_lshlrev_b32_e32 v120, 16, v89
	v_lshlrev_b32_e32 v88, 16, v91
	v_and_b32_e32 v89, 0xffff0000, v89
	s_waitcnt vmcnt(16)
	v_lshlrev_b32_e32 v90, 16, v92
	s_waitcnt vmcnt(15)
	v_lshlrev_b32_e32 v122, 16, v94
	v_and_b32_e32 v123, 0xffff0000, v92
	v_lshlrev_b32_e32 v124, 16, v93
	v_lshlrev_b32_e32 v92, 16, v95
	v_and_b32_e32 v93, 0xffff0000, v93
	v_and_b32_e32 v121, 0xffff0000, v91
	v_and_b32_e32 v91, 0xffff0000, v94
	v_and_b32_e32 v125, 0xffff0000, v95
	v_pk_mul_f32 v[114:115], v[42:43], v[114:115]
	v_pk_mul_f32 v[84:85], v[42:43], v[84:85]
	v_pk_mul_f32 v[118:119], v[42:43], v[118:119]
	v_pk_mul_f32 v[88:89], v[42:43], v[88:89]
	v_pk_mul_f32 v[122:123], v[42:43], v[122:123]
	v_pk_mul_f32 v[92:93], v[42:43], v[92:93]
	v_pk_fma_f32 v[112:113], v[42:43], v[112:113], v[114:115] op_sel:[1,0,0] op_sel_hi:[0,1,1]
	v_pk_fma_f32 v[84:85], v[42:43], v[116:117], v[84:85] op_sel:[1,0,0] op_sel_hi:[0,1,1]
	v_pk_fma_f32 v[86:87], v[42:43], v[86:87], v[118:119] op_sel:[1,0,0] op_sel_hi:[0,1,1]
	v_pk_fma_f32 v[88:89], v[42:43], v[120:121], v[88:89] op_sel:[1,0,0] op_sel_hi:[0,1,1]
	v_pk_fma_f32 v[90:91], v[42:43], v[90:91], v[122:123] op_sel:[1,0,0] op_sel_hi:[0,1,1]
	v_pk_fma_f32 v[92:93], v[42:43], v[124:125], v[92:93] op_sel:[1,0,0] op_sel_hi:[0,1,1]
	s_waitcnt vmcnt(13)
	v_pk_add_f32 v[56:57], v[56:57], v[112:113]
	v_pk_add_f32 v[58:59], v[58:59], v[84:85]
	s_waitcnt vmcnt(12)
	v_pk_add_f32 v[60:61], v[60:61], v[86:87]
	v_pk_add_f32 v[62:63], v[62:63], v[88:89]
	s_waitcnt vmcnt(11)
	v_pk_add_f32 v[64:65], v[64:65], v[90:91]
	v_pk_add_f32 v[66:67], v[66:67], v[92:93]
	v_mov_b32_e32 v86, v57
	v_mov_b32_e32 v87, v61
	v_mov_b32_e32 v88, v58
	v_mov_b32_e32 v89, v62
	v_pk_mov_b32 v[92:93], v[64:65], v[66:67] op_sel:[1,0]
	v_mov_b32_e32 v84, v56
	v_mov_b32_e32 v85, v60
	v_mov_b32_e32 v90, v59
	v_mov_b32_e32 v91, v63
	v_mov_b32_e32 v112, v64
	v_mov_b32_e32 v113, v67
	v_pk_mul_f32 v[86:87], v[86:87], v[86:87]
	v_pk_mul_f32 v[88:89], v[88:89], v[88:89]
	v_pk_mul_f32 v[92:93], v[92:93], v[92:93]
	v_pk_fma_f32 v[84:85], v[84:85], v[84:85], v[86:87]
	v_pk_fma_f32 v[86:87], v[90:91], v[90:91], v[88:89]
	v_pk_fma_f32 v[88:89], v[112:113], v[112:113], v[92:93]
	v_pk_add_f32 v[84:85], v[84:85], v[86:87]
	v_pk_add_f32 v[86:87], v[88:89], v[88:89] op_sel:[0,1] op_sel_hi:[1,0]
	s_waitcnt vmcnt(10)
	v_lshlrev_b32_e32 v88, 16, v98
	global_load_dwordx2 v[90:91], v[46:47], off offset:3584
	global_load_dwordx2 v[92:93], v[44:45], off offset:3584
	v_and_b32_e32 v89, 0xffff0000, v96
	v_lshlrev_b32_e32 v94, 16, v96
	v_and_b32_e32 v95, 0xffff0000, v98
	v_pk_mul_f32 v[44:45], v[42:43], v[88:89]
	v_and_b32_e32 v89, 0xffff0000, v99
	v_pk_fma_f32 v[44:45], v[42:43], v[94:95], v[44:45] op_sel:[1,0,0] op_sel_hi:[0,1,1]
	s_waitcnt vmcnt(11)
	v_pk_add_f32 v[68:69], v[68:69], v[44:45]
	global_load_dwordx4 v[44:47], v[36:37], off offset:3072
	v_lshlrev_b32_e32 v94, 16, v99
	s_waitcnt vmcnt(8)
	v_lshlrev_b32_e32 v98, 16, v100
	s_waitcnt vmcnt(5)
	v_and_b32_e32 v99, 0xffff0000, v106
	v_lshlrev_b32_e32 v88, 16, v97
	v_and_b32_e32 v95, 0xffff0000, v97
	v_lshlrev_b32_e32 v96, 16, v106
	v_and_b32_e32 v97, 0xffff0000, v100
	v_pk_mul_f32 v[98:99], v[42:43], v[98:99]
	v_pk_mul_f32 v[94:95], v[42:43], v[94:95]
	v_pk_fma_f32 v[96:97], v[42:43], v[96:97], v[98:99] op_sel:[1,0,0] op_sel_hi:[0,1,1]
	v_lshlrev_b32_e32 v98, 16, v101
	v_and_b32_e32 v99, 0xffff0000, v107
	v_pk_fma_f32 v[88:89], v[42:43], v[88:89], v[94:95] op_sel:[1,0,0] op_sel_hi:[0,1,1]
	v_pk_add_f32 v[72:73], v[72:73], v[96:97]
	v_lshlrev_b32_e32 v96, 16, v107
	v_and_b32_e32 v97, 0xffff0000, v101
	v_pk_mul_f32 v[98:99], v[42:43], v[98:99]
	v_pk_add_f32 v[70:71], v[70:71], v[88:89]
	v_mul_f32_e32 v32, v69, v69
	v_pk_fma_f32 v[96:97], v[42:43], v[96:97], v[98:99] op_sel:[1,0,0] op_sel_hi:[0,1,1]
	v_pk_fma_f32 v[88:89], v[68:69], v[68:69], v[32:33] op_sel_hi:[1,1,0]
	v_mul_f32_e32 v32, v71, v71
	v_pk_add_f32 v[74:75], v[74:75], v[96:97]
	v_pk_add_f32 v[84:85], v[84:85], v[84:85] op_sel:[0,1] op_sel_hi:[1,0]
	v_pk_fma_f32 v[94:95], v[70:71], v[70:71], v[32:33] op_sel_hi:[1,1,0]
	v_pk_mul_f32 v[96:97], v[72:73], v[72:73]
	v_pk_mul_f32 v[98:99], v[74:75], v[74:75]
	v_mov_b32_e32 v85, v96
	v_mov_b32_e32 v87, v97
	v_mov_b32_e32 v89, v99
	v_mov_b32_e32 v95, v98
	v_pk_add_f32 v[84:85], v[84:85], v[86:87]
	v_pk_add_f32 v[86:87], v[88:89], v[94:95]
	v_lshlrev_b32_e32 v88, 16, v102
	s_waitcnt vmcnt(4)
	v_and_b32_e32 v89, 0xffff0000, v108
	v_pk_add_f32 v[84:85], v[84:85], v[86:87]
	v_lshlrev_b32_e32 v86, 16, v108
	v_and_b32_e32 v87, 0xffff0000, v102
	v_pk_mul_f32 v[88:89], v[42:43], v[88:89]
	v_lshlrev_b32_e32 v94, 16, v104
	v_pk_fma_f32 v[86:87], v[42:43], v[86:87], v[88:89] op_sel:[1,0,0] op_sel_hi:[0,1,1]
	v_lshlrev_b32_e32 v88, 16, v103
	v_and_b32_e32 v89, 0xffff0000, v109
	v_pk_add_f32 v[76:77], v[76:77], v[86:87]
	v_lshlrev_b32_e32 v86, 16, v109
	v_and_b32_e32 v87, 0xffff0000, v103
	v_pk_mul_f32 v[88:89], v[42:43], v[88:89]
	s_waitcnt vmcnt(3)
	v_and_b32_e32 v95, 0xffff0000, v110
	v_pk_fma_f32 v[86:87], v[42:43], v[86:87], v[88:89] op_sel:[1,0,0] op_sel_hi:[0,1,1]
	v_pk_add_f32 v[78:79], v[78:79], v[86:87]
	v_mov_b32_e32 v88, v76
	v_pk_mov_b32 v[86:87], v[76:77], v[78:79] op_sel:[1,0]
	v_mov_b32_e32 v89, v79
	v_pk_mul_f32 v[86:87], v[86:87], v[86:87]
	v_pk_mul_f32 v[94:95], v[42:43], v[94:95]
	v_pk_fma_f32 v[86:87], v[88:89], v[88:89], v[86:87]
	v_lshlrev_b32_e32 v88, 16, v110
	v_and_b32_e32 v89, 0xffff0000, v104
	v_pk_fma_f32 v[88:89], v[42:43], v[88:89], v[94:95] op_sel:[1,0,0] op_sel_hi:[0,1,1]
	v_lshlrev_b32_e32 v94, 16, v105
	v_and_b32_e32 v95, 0xffff0000, v111
	v_pk_add_f32 v[80:81], v[80:81], v[88:89]
	v_lshlrev_b32_e32 v88, 16, v111
	v_and_b32_e32 v89, 0xffff0000, v105
	v_pk_mul_f32 v[94:95], v[42:43], v[94:95]
	v_mul_f32_e32 v32, v81, v81
	v_pk_fma_f32 v[88:89], v[42:43], v[88:89], v[94:95] op_sel:[1,0,0] op_sel_hi:[0,1,1]
	v_pk_add_f32 v[82:83], v[82:83], v[88:89]
	v_pk_fma_f32 v[88:89], v[80:81], v[80:81], v[32:33] op_sel_hi:[1,1,0]
	v_mul_f32_e32 v32, v83, v83
	s_waitcnt vmcnt(2)
	v_and_b32_e32 v99, 0xffff0000, v90
	s_waitcnt vmcnt(1)
	v_lshlrev_b32_e32 v98, 16, v92
	v_lshlrev_b32_e32 v96, 16, v90
	v_and_b32_e32 v97, 0xffff0000, v92
	v_pk_mul_f32 v[98:99], v[42:43], v[98:99]
	v_lshlrev_b32_e32 v90, 16, v93
	v_pk_fma_f32 v[96:97], v[42:43], v[96:97], v[98:99] op_sel:[1,0,0] op_sel_hi:[0,1,1]
	v_pk_add_f32 v[84:85], v[84:85], v[84:85] op_sel:[0,1] op_sel_hi:[1,0]
	v_pk_add_f32 v[86:87], v[86:87], v[86:87] op_sel:[0,1] op_sel_hi:[1,0]
	s_waitcnt vmcnt(0)
	v_pk_add_f32 v[96:97], v[44:45], v[96:97]
	v_lshlrev_b32_e32 v44, 16, v91
	v_and_b32_e32 v91, 0xffff0000, v91
	v_and_b32_e32 v45, 0xffff0000, v93
	v_pk_mul_f32 v[90:91], v[42:43], v[90:91]
	v_pk_fma_f32 v[94:95], v[82:83], v[82:83], v[32:33] op_sel_hi:[1,1,0]
	v_pk_fma_f32 v[42:43], v[42:43], v[44:45], v[90:91] op_sel:[1,0,0] op_sel_hi:[0,1,1]
	v_pk_add_f32 v[46:47], v[46:47], v[42:43]
	v_pk_mul_f32 v[42:43], v[96:97], v[96:97]
	v_pk_mul_f32 v[44:45], v[46:47], v[46:47]
	v_mov_b32_e32 v85, v42
	v_mov_b32_e32 v87, v43
	v_mov_b32_e32 v89, v45
	v_mov_b32_e32 v95, v44
	v_pk_add_f32 v[42:43], v[84:85], v[86:87]
	v_pk_add_f32 v[44:45], v[88:89], v[94:95]
	s_nop 0
	v_pk_add_f32 v[42:43], v[42:43], v[44:45]
	s_nop 0
	v_add_f32_e32 v32, v42, v43
	ds_bpermute_b32 v42, v49, v32
	s_waitcnt lgkmcnt(0)
	v_add_f32_e32 v32, v32, v42
	ds_bpermute_b32 v42, v50, v32
	s_waitcnt lgkmcnt(0)
	v_add_f32_e32 v32, v32, v42
	ds_bpermute_b32 v42, v51, v32
	s_waitcnt lgkmcnt(0)
	v_add_f32_e32 v32, v32, v42
	ds_bpermute_b32 v42, v52, v32
	s_waitcnt lgkmcnt(0)
	v_add_f32_e32 v32, v32, v42
	ds_bpermute_b32 v42, v53, v32
	s_waitcnt lgkmcnt(0)
	v_add_f32_e32 v32, v32, v42
	ds_bpermute_b32 v42, v54, v32
	s_waitcnt lgkmcnt(0)
	v_add_f32_e32 v32, v32, v42
	v_fmamk_f32 v32, v32, 0x3a000000, v48
	v_mul_f32_e32 v42, 0x4b800000, v32
	v_cmp_gt_f32_e32 vcc, s14, v32
	s_nop 1
	v_cndmask_b32_e32 v32, v32, v42, vcc
	v_rsq_f32_e32 v32, v32
	s_nop 0
	v_mul_f32_e32 v42, 0x45800000, v32
	v_cndmask_b32_e32 v32, v32, v42, vcc
	v_pk_mul_f32 v[42:43], v[56:57], v[32:33] op_sel_hi:[1,0]
	v_pk_mul_f32 v[44:45], v[58:59], v[32:33] op_sel_hi:[1,0]
	v_pk_mul_f32 v[42:43], v[0:1], v[42:43]
	v_pk_mul_f32 v[44:45], v[2:3], v[44:45]
	global_store_dwordx4 v[36:37], v[42:45], off offset:-4096 sc1
	s_andn2_b64 vcc, exec, s[8:9]
	s_nop 0
	v_pk_mul_f32 v[42:43], v[60:61], v[32:33] op_sel_hi:[1,0]
	v_pk_mul_f32 v[44:45], v[62:63], v[32:33] op_sel_hi:[1,0]
	v_pk_mul_f32 v[42:43], v[4:5], v[42:43]
	v_pk_mul_f32 v[44:45], v[6:7], v[44:45]
	global_store_dwordx4 v[36:37], v[42:45], off offset:-3072 sc1
	s_nop 1
	v_pk_mul_f32 v[42:43], v[64:65], v[32:33] op_sel_hi:[1,0]
	v_pk_mul_f32 v[44:45], v[66:67], v[32:33] op_sel_hi:[1,0]
	v_pk_mul_f32 v[42:43], v[8:9], v[42:43]
	v_pk_mul_f32 v[44:45], v[10:11], v[44:45]
	global_store_dwordx4 v[36:37], v[42:45], off offset:-2048 sc1
	s_nop 1
	v_pk_mul_f32 v[42:43], v[68:69], v[32:33] op_sel_hi:[1,0]
	v_pk_mul_f32 v[44:45], v[70:71], v[32:33] op_sel_hi:[1,0]
	v_pk_mul_f32 v[42:43], v[12:13], v[42:43]
	v_pk_mul_f32 v[44:45], v[14:15], v[44:45]
	global_store_dwordx4 v[36:37], v[42:45], off offset:-1024 sc1
	s_nop 1
	v_pk_mul_f32 v[42:43], v[72:73], v[32:33] op_sel_hi:[1,0]
	v_pk_mul_f32 v[44:45], v[74:75], v[32:33] op_sel_hi:[1,0]
	v_pk_mul_f32 v[42:43], v[16:17], v[42:43]
	v_pk_mul_f32 v[44:45], v[18:19], v[44:45]
	global_store_dwordx4 v[36:37], v[42:45], off sc1
	s_nop 1
	v_pk_mul_f32 v[42:43], v[76:77], v[32:33] op_sel_hi:[1,0]
	v_pk_mul_f32 v[44:45], v[78:79], v[32:33] op_sel_hi:[1,0]
	v_pk_mul_f32 v[42:43], v[20:21], v[42:43]
	v_pk_mul_f32 v[44:45], v[22:23], v[44:45]
	global_store_dwordx4 v[36:37], v[42:45], off offset:1024 sc1
	s_nop 1
	v_pk_mul_f32 v[42:43], v[80:81], v[32:33] op_sel_hi:[1,0]
	v_pk_mul_f32 v[44:45], v[82:83], v[32:33] op_sel_hi:[1,0]
	v_pk_mul_f32 v[42:43], v[24:25], v[42:43]
	v_pk_mul_f32 v[44:45], v[26:27], v[44:45]
	global_store_dwordx4 v[36:37], v[42:45], off offset:2048 sc1
	s_nop 1
	v_pk_mul_f32 v[42:43], v[96:97], v[32:33] op_sel_hi:[1,0]
	v_pk_mul_f32 v[44:45], v[46:47], v[32:33] op_sel_hi:[1,0]
	v_pk_mul_f32 v[42:43], v[28:29], v[42:43]
	v_pk_mul_f32 v[44:45], v[30:31], v[44:45]
	global_store_dwordx4 v[36:37], v[42:45], off offset:3072 sc1
	v_lshl_add_u64 v[36:37], v[36:37], 0, s[6:7]
	s_nop 0
	v_mov_b64_e32 v[42:43], v[38:39]
	v_mov_b64_e32 v[44:45], v[40:41]
	s_cbranch_vccz .LBB0_1632
